# original copy loops with nt loads/stores (no new routine) + padding-row MFMA skip in MoE GEMM loops
# baseline (speedup 1.0000x reference)
.LBB0_1358:
	s_mul_i32 s64, s26, 0x18000
	s_mov_b32 s65, s90
	s_or_b32 s15, s64, 0x7800
	s_add_i32 s67, s64, 0xfc00
	s_and_b32 s12, s65, 7
	s_and_b32 s18, s65, 0xffffffc0
	s_cmpk_eq_i32 s18, 0x80
	v_readlane_b32 s2, v253, 11
	s_cselect_b64 s[0:1], -1, 0
	v_readlane_b32 s3, v253, 12
	s_and_b64 s[0:1], s[2:3], s[0:1]
	v_and_b32_e32 v8, 63, v154
	s_andn2_b64 vcc, exec, s[0:1]
	s_cbranch_vccnz .LBB0_1429
	s_and_b32 s1, s65, 0xb8
	v_readlane_b32 s2, v254, 61
	s_lshl_b32 s0, s12, 6
	s_add_i32 s2, s2, s1
	s_add_i32 s3, s2, s0
	s_add_i32 s25, s3, s15
	s_cmp_ge_u32 s25, s67
	s_cbranch_scc1 .LBB0_1428
	s_mul_hi_u32 s0, s25, 0xaaaaaaab
	s_lshr_b32 s7, s0, 16
	s_mul_i32 s6, s7, 0xfffe8000
	s_add_i32 s6, s6, s25
	s_add_i32 s0, s6, 0x7fff
	s_cmpk_gt_u32 s0, 0xfffe
	s_mov_b64 s[0:1], -1
	s_cbranch_scc0 .LBB0_1366
	s_and_b32 s0, s6, 0xffff8000
	s_cmpk_lg_u32 s0, 0x8000
	s_mov_b64 s[0:1], -1
	s_cbranch_scc0 .LBB0_1363
	v_readlane_b32 s0, v253, 6
	s_nop 1
	v_mov_b32_e32 v2, s0
	ds_read_b64 v[4:5], v2
	s_mov_b64 s[0:1], 0
	s_waitcnt lgkmcnt(0)
	v_readfirstlane_b32 s16, v4
	v_readfirstlane_b32 s17, v5
.LBB0_1363:
	s_andn2_b64 vcc, exec, s[0:1]
	s_cbranch_vccnz .LBB0_1365
	v_readlane_b32 s0, v252, 36
	s_nop 1
	v_mov_b32_e32 v2, s0
	ds_read_b64 v[4:5], v2
	s_waitcnt lgkmcnt(0)
	v_readfirstlane_b32 s16, v4
	v_readfirstlane_b32 s17, v5

.LBB0_1366:
	s_andn2_b64 vcc, exec, s[0:1]
	s_cbranch_vccnz .LBB0_1368
	v_readlane_b32 s0, v253, 31
	s_nop 1
	v_mov_b32_e32 v2, s0
	ds_read_b64 v[4:5], v2
	s_waitcnt lgkmcnt(0)
	v_readfirstlane_b32 s16, v4
	v_readfirstlane_b32 s17, v5
.LBB0_1368:
	s_ashr_i32 s0, s6, 31
	s_lshr_b32 s0, s0, 17
	s_add_i32 s26, s6, s0
	s_and_b32 s0, s26, 0xffff8000
	s_sub_i32 s0, s6, s0
	s_ashr_i32 s0, s0, 11
	s_lshl_b32 s1, s7, 4
	s_add_i32 s34, s0, s1
	s_ashr_i32 s35, s34, 31
	s_cmp_lt_i32 s6, 0x10000
	s_cselect_b64 s[0:1], -1, 0
	s_cmp_gt_i32 s6, 0xffff
	s_mov_b64 s[8:9], -1
	s_cbranch_scc0 .LBB0_1370
	s_lshl_b64 s[6:7], s[34:35], 23
	s_add_u32 s6, s40, s6
	s_addc_u32 s7, s41, s7
	s_add_u32 s38, s6, 0x23840000
	s_addc_u32 s39, s7, 0
	s_lshl_b64 s[6:7], s[34:35], 24
	s_mov_b64 s[8:9], 0
.LBB0_1370:
	s_andn2_b64 vcc, exec, s[8:9]
	s_cbranch_vccnz .LBB0_1372
	s_lshl_b64 s[6:7], s[34:35], 24
	s_add_u32 s8, s40, s6
	s_addc_u32 s9, s41, s7
	s_add_u32 s38, s8, 0x3840000
	s_addc_u32 s39, s9, 0
.LBB0_1372:
	s_lshl_b32 s8, s2, 5
	s_and_b32 s8, s8, 0x7e0
	v_lshrrev_b32_e32 v9, 3, v8
	s_and_b32 s3, s3, 0x7c0
	v_or_b32_e32 v2, s3, v9
	s_add_u32 s6, s16, s6
	v_lshlrev_b32_e32 v2, 13, v2
	s_addc_u32 s7, s17, s7
	v_lshl_add_u64 v[4:5], s[6:7], 0, v[2:3]
	s_lshl_b32 s92, s8, 2
	v_and_b32_e32 v12, 7, v154
	v_lshl_add_u64 v[4:5], v[4:5], 0, s[92:93]
	v_lshlrev_b32_e32 v2, 4, v12
	v_lshl_add_u64 v[4:5], v[4:5], 0, v[2:3]
	s_mov_b32 s6, m0
	s_mov_b32 m0, s94
	s_nop 0
	global_load_lds_dwordx4 v[4:5], off nt
	s_mov_b32 m0, s6
	s_mov_b64 s[6:7], 0x10000
	v_lshl_add_u64 v[6:7], v[4:5], 0, s[6:7]
	s_add_i32 s16, s94, 0x410
	s_mov_b32 s6, m0
	s_mov_b32 m0, s16
	s_nop 0
	global_load_lds_dwordx4 v[6:7], off nt
	s_mov_b32 m0, s6
	v_lshl_add_u64 v[6:7], v[4:5], 0, s[84:85]
	s_add_i32 s17, s94, 0x820
	s_mov_b32 s6, m0
	s_mov_b32 m0, s17
	s_nop 0
	global_load_lds_dwordx4 v[6:7], off nt
	s_mov_b32 m0, s6
	s_mov_b64 s[6:7], 0x30000
	v_lshl_add_u64 v[6:7], v[4:5], 0, s[6:7]
	s_add_i32 s19, s94, 0xc30
	s_mov_b32 s6, m0
	s_mov_b32 m0, s19
	s_nop 0
	global_load_lds_dwordx4 v[6:7], off nt
	s_mov_b32 m0, s6
	s_mov_b64 s[6:7], 0x40000
	v_lshl_add_u64 v[6:7], v[4:5], 0, s[6:7]
	s_add_i32 s20, s94, 0x1040
	s_mov_b32 s6, m0
	s_mov_b32 m0, s20
	s_nop 0
	global_load_lds_dwordx4 v[6:7], off nt
	s_mov_b32 m0, s6
	s_mov_b64 s[6:7], 0x50000
	v_lshl_add_u64 v[6:7], v[4:5], 0, s[6:7]
	s_add_i32 s21, s94, 0x1450
	s_mov_b32 s6, m0
	s_mov_b32 m0, s21
	s_nop 0
	global_load_lds_dwordx4 v[6:7], off nt
	s_mov_b32 m0, s6
	s_mov_b64 s[6:7], 0x60000
	v_lshl_add_u64 v[6:7], v[4:5], 0, s[6:7]
	s_add_i32 s22, s94, 0x1860
	s_mov_b32 s6, m0
	s_mov_b32 m0, s22
	s_nop 0
	global_load_lds_dwordx4 v[6:7], off nt
	s_mov_b32 m0, s6
	s_add_i32 s23, s94, 0x1c70
	s_add_i32 s24, s25, 0x200
	s_mov_b64 s[6:7], 0x70000
	s_cmp_lt_u32 s24, s67
	v_lshl_add_u64 v[4:5], v[4:5], 0, s[6:7]
	s_mov_b32 s6, m0
	s_mov_b32 m0, s23
	s_nop 0
	global_load_lds_dwordx4 v[4:5], off nt
	s_mov_b32 m0, s6
	s_cselect_b64 s[34:35], -1, 0
	s_cmp_ge_u32 s24, s67
	s_cselect_b64 s[36:37], -1, 0
	s_mov_b64 s[6:7], -1
	s_and_b64 vcc, exec, s[36:37]
	s_cbranch_vccz .LBB0_1374
	s_waitcnt vmcnt(0)
	s_mov_b64 s[6:7], 0
.LBB0_1374:
	s_ashr_i32 s9, s26, 15
	s_lshl_b32 s2, s2, 6
	s_and_b32 s2, s2, 0xf00
	s_lshl_b32 s9, s9, 7
	s_add_i32 s9, s9, s2
	v_bitop3_b32 v14, s8, v209, v9 bitop3:0xc8
	v_or_b32_e32 v13, s8, v9
	v_or_b32_e32 v4, s9, v14
	v_cndmask_b32_e64 v4, v13, v4, s[0:1]
	v_ashrrev_i32_e32 v5, 31, v4
	v_lshlrev_b64 v[4:5], 12, v[4:5]
	v_lshl_add_u64 v[4:5], s[38:39], 0, v[4:5]
	s_lshl_b32 s0, s3, 1
	s_mov_b32 s1, s93
	v_lshl_add_u64 v[4:5], v[4:5], 0, s[0:1]
	v_lshl_add_u64 v[4:5], v[4:5], 0, v[2:3]
	v_lshlrev_b32_e32 v10, 2, v12
	v_lshlrev_b32_e32 v11, 3, v12
	s_andn2_b64 vcc, exec, s[6:7]
	v_mov_b64_e32 v[6:7], v[4:5]
	s_cbranch_vccnz .LBB0_1388
	s_mul_hi_u32 s0, s24, 0xaaaaaaab
	s_lshr_b32 s7, s0, 16
	s_mul_i32 s6, s7, 0xfffe8000
	s_add_i32 s6, s6, s24
	s_add_i32 s0, s6, 0x7fff
	s_cmpk_gt_u32 s0, 0xfffe
	s_mov_b64 s[0:1], -1
	s_cbranch_scc0 .LBB0_1381
	s_and_b32 s0, s6, 0xffff8000
	s_cmpk_lg_u32 s0, 0x8000
	s_mov_b64 s[0:1], -1
	s_cbranch_scc0 .LBB0_1378
	v_readlane_b32 s0, v253, 6
	s_nop 1
	v_mov_b32_e32 v2, s0
	ds_read_b64 v[6:7], v2
	s_mov_b64 s[0:1], 0
	s_waitcnt lgkmcnt(0)
	v_readfirstlane_b32 s3, v6
	v_readfirstlane_b32 s26, v7

.LBB0_1383:
	s_ashr_i32 s0, s6, 31
	s_lshr_b32 s0, s0, 17
	s_add_i32 s27, s6, s0
	s_and_b32 s0, s27, 0xffff8000
	s_sub_i32 s0, s6, s0
	s_ashr_i32 s0, s0, 11
	s_lshl_b32 s1, s7, 4
	s_add_i32 s42, s0, s1
	s_ashr_i32 s43, s42, 31
	s_cmp_lt_i32 s6, 0x10000
	s_cselect_b64 s[0:1], -1, 0
	s_cmp_gt_i32 s6, 0xffff
	s_mov_b64 s[8:9], -1
	s_cbranch_scc0 .LBB0_1385
	s_lshl_b64 s[6:7], s[42:43], 23
	s_add_u32 s6, s40, s6
	s_addc_u32 s7, s41, s7
	s_add_u32 s38, s6, 0x23840000
	s_addc_u32 s39, s7, 0
	s_lshl_b64 s[6:7], s[42:43], 24
	s_mov_b64 s[8:9], 0
.LBB0_1385:
	s_andn2_b64 vcc, exec, s[8:9]
	s_ashr_i32 s8, s27, 15
	s_cbranch_vccnz .LBB0_1387
	s_lshl_b64 s[6:7], s[42:43], 24
	s_add_u32 s9, s40, s6
	s_addc_u32 s27, s41, s7
	s_add_u32 s38, s9, 0x3840000
	s_addc_u32 s39, s27, 0
.LBB0_1387:
	s_lshl_b32 s8, s8, 7
	s_add_i32 s8, s8, s2
	v_or_b32_e32 v2, s8, v14
	s_and_b32 s2, s24, 0x7c0
	v_cndmask_b32_e64 v6, v13, v2, s[0:1]
	v_or_b32_e32 v2, s2, v9
	s_add_u32 s0, s3, s6
	v_lshlrev_b32_e32 v2, 13, v2
	s_addc_u32 s1, s26, s7
	v_lshl_add_u64 v[14:15], s[0:1], 0, v[2:3]
	v_lshl_add_u64 v[14:15], v[14:15], 0, s[92:93]
	v_lshlrev_b32_e32 v2, 2, v10
	v_lshl_add_u64 v[14:15], v[14:15], 0, v[2:3]
	s_add_i32 s0, s94, 0x2080
	s_mov_b32 s1, m0
	s_mov_b32 m0, s0
	s_nop 0
	global_load_lds_dwordx4 v[14:15], off nt
	s_mov_b32 m0, s1
	s_mov_b64 s[0:1], 0x10000
	v_lshl_add_u64 v[16:17], v[14:15], 0, s[0:1]
	s_add_i32 s0, s94, 0x2490
	s_mov_b32 s1, m0
	s_mov_b32 m0, s0
	s_nop 0
	global_load_lds_dwordx4 v[16:17], off nt
	s_mov_b32 m0, s1
	v_lshl_add_u64 v[16:17], v[14:15], 0, s[84:85]
	s_add_i32 s0, s94, 0x28a0
	s_mov_b32 s1, m0
	s_mov_b32 m0, s0
	s_nop 0
	global_load_lds_dwordx4 v[16:17], off nt
	s_mov_b32 m0, s1
	s_mov_b64 s[0:1], 0x30000
	v_lshl_add_u64 v[16:17], v[14:15], 0, s[0:1]
	s_add_i32 s0, s94, 0x2cb0
	s_mov_b32 s1, m0
	s_mov_b32 m0, s0
	s_nop 0
	global_load_lds_dwordx4 v[16:17], off nt
	s_mov_b32 m0, s1
	s_mov_b64 s[0:1], 0x40000
	v_lshl_add_u64 v[16:17], v[14:15], 0, s[0:1]
	s_add_i32 s0, s94, 0x30c0
	s_mov_b32 s1, m0
	s_mov_b32 m0, s0
	s_nop 0
	global_load_lds_dwordx4 v[16:17], off nt
	s_mov_b32 m0, s1
	s_mov_b64 s[0:1], 0x50000
	v_lshl_add_u64 v[16:17], v[14:15], 0, s[0:1]
	s_add_i32 s0, s94, 0x34d0
	s_mov_b32 s1, m0
	s_mov_b32 m0, s0
	s_nop 0
	global_load_lds_dwordx4 v[16:17], off nt
	s_mov_b32 m0, s1
	s_mov_b64 s[0:1], 0x60000
	v_lshl_add_u64 v[16:17], v[14:15], 0, s[0:1]
	s_add_i32 s0, s94, 0x38e0
	s_mov_b32 s1, m0
	s_mov_b32 m0, s0
	s_nop 0
	global_load_lds_dwordx4 v[16:17], off nt
	s_mov_b32 m0, s1
	v_ashrrev_i32_e32 v7, 31, v6
	s_mov_b64 s[0:1], 0x70000
	v_lshlrev_b64 v[6:7], 12, v[6:7]
	v_lshl_add_u64 v[14:15], v[14:15], 0, s[0:1]
	s_add_i32 s0, s94, 0x3cf0
	s_mov_b32 s1, m0
	s_mov_b32 m0, s0
	s_nop 0
	global_load_lds_dwordx4 v[14:15], off nt
	s_mov_b32 m0, s1
	v_lshl_add_u64 v[6:7], s[38:39], 0, v[6:7]
	s_lshl_b32 s92, s2, 1
	s_waitcnt vmcnt(8)
	v_lshl_add_u64 v[6:7], v[6:7], 0, s[92:93]
	v_lshlrev_b32_e32 v2, 1, v11
	v_lshl_add_u64 v[6:7], v[6:7], 0, v[2:3]
.LBB0_1388:
	v_mul_u32_u24_e32 v2, 0x410, v12
	v_lshlrev_b32_e32 v12, 2, v9
	v_add3_u32 v12, s94, v2, v12
	ds_read2_b32 v[18:19], v12 offset0:32 offset1:40
	ds_read2_b32 v[20:21], v12 offset1:8
	ds_read2_b32 v[22:23], v12 offset0:64 offset1:72
	ds_read2_b32 v[24:25], v12 offset0:96 offset1:104
	ds_read2_b32 v[26:27], v12 offset0:128 offset1:136
	ds_read2_b32 v[28:29], v12 offset0:160 offset1:168
	ds_read2_b32 v[30:31], v12 offset0:192 offset1:200
	ds_read2_b32 v[32:33], v12 offset0:224 offset1:232
	s_mov_b32 s0, 0x8000
	s_waitcnt lgkmcnt(0)
	v_cvt_pk_bf16_f32 v14, v20, v18
	v_cvt_pk_bf16_f32 v15, v22, v24
	v_cvt_pk_bf16_f32 v16, v26, v28
	v_cvt_pk_bf16_f32 v17, v30, v32
	v_add_co_u32_e32 v18, vcc, s0, v4
	global_store_dwordx4 v[4:5], v[14:17], off nt
	s_mov_b32 s0, 0x10000
	v_readlane_b32 s26, v254, 28
	v_cvt_pk_bf16_f32 v14, v21, v19
	v_cvt_pk_bf16_f32 v15, v23, v25
	v_cvt_pk_bf16_f32 v16, v27, v29
	v_cvt_pk_bf16_f32 v17, v31, v33
	v_addc_co_u32_e32 v19, vcc, 0, v5, vcc
	global_store_dwordx4 v[18:19], v[14:17], off nt
	ds_read2_b32 v[18:19], v12 offset0:48 offset1:56
	ds_read2_b32 v[20:21], v12 offset0:16 offset1:24
	ds_read2_b32 v[22:23], v12 offset0:80 offset1:88
	ds_read2_b32 v[24:25], v12 offset0:112 offset1:120
	ds_read2_b32 v[26:27], v12 offset0:144 offset1:152
	ds_read2_b32 v[28:29], v12 offset0:176 offset1:184
	ds_read2_b32 v[30:31], v12 offset0:208 offset1:216
	ds_read2_b32 v[32:33], v12 offset0:240 offset1:248
	v_add_co_u32_e32 v34, vcc, s0, v4
	s_waitcnt lgkmcnt(0)
	v_cvt_pk_bf16_f32 v14, v20, v18
	v_addc_co_u32_e32 v35, vcc, 0, v5, vcc
	v_cvt_pk_bf16_f32 v15, v22, v24
	v_cvt_pk_bf16_f32 v16, v26, v28
	v_cvt_pk_bf16_f32 v17, v30, v32
	v_add_co_u32_e32 v18, vcc, 0x18000, v4
	global_store_dwordx4 v[34:35], v[14:17], off nt
	v_readlane_b32 s27, v254, 29
	s_nop 0
	v_cvt_pk_bf16_f32 v14, v21, v19
	v_cvt_pk_bf16_f32 v15, v23, v25
	v_cvt_pk_bf16_f32 v16, v27, v29
	v_cvt_pk_bf16_f32 v17, v31, v33
	v_addc_co_u32_e32 v19, vcc, 0, v5, vcc
	global_store_dwordx4 v[18:19], v[14:17], off nt
	s_waitcnt lgkmcnt(0)
	s_andn2_b64 vcc, exec, s[36:37]
	s_cbranch_vccnz .LBB0_1390
	s_waitcnt vmcnt(0)
	s_mov_b32 s24, s25
.LBB0_1390:
	s_andn2_b64 vcc, exec, s[34:35]
	s_cbranch_vccnz .LBB0_1428
	s_add_u32 s25, s40, 0x23840000
	s_addc_u32 s26, s41, 0
	s_add_u32 s27, s40, 0x3840000
	s_addc_u32 s28, s41, 0
	s_branch .LBB0_1395
.LBB0_1392:
	s_lshl_b32 s6, s24, 5
	s_lshl_b32 s7, s24, 6
	s_and_b32 s6, s6, 0x7e0
	s_and_b32 s7, s7, 0xf00
	s_lshl_b32 s8, s8, 7
	s_add_i32 s8, s8, s7
	v_bitop3_b32 v6, s6, v209, v9 bitop3:0xc8
	v_or_b32_e32 v2, s6, v9
	v_or_b32_e32 v6, s8, v6
	s_and_b32 s7, s2, 0x7c0
	v_cndmask_b32_e64 v6, v2, v6, s[0:1]
	v_or_b32_e32 v2, s7, v9
	s_add_u32 s0, s3, s38
	v_lshlrev_b32_e32 v2, 13, v2
	s_addc_u32 s1, s29, s39
	v_lshl_add_u64 v[14:15], s[0:1], 0, v[2:3]
	s_lshl_b32 s92, s6, 2
	v_lshl_add_u64 v[14:15], v[14:15], 0, s[92:93]
	v_lshlrev_b32_e32 v2, 2, v10
	v_lshl_add_u64 v[14:15], v[14:15], 0, v[2:3]
	s_add_i32 s0, s94, 0x2080
	s_mov_b32 s1, m0
	s_mov_b32 m0, s0
	s_nop 0
	global_load_lds_dwordx4 v[14:15], off nt
	s_mov_b32 m0, s1
	s_mov_b64 s[0:1], 0x10000
	v_lshl_add_u64 v[16:17], v[14:15], 0, s[0:1]
	s_add_i32 s0, s94, 0x2490
	s_mov_b32 s1, m0
	s_mov_b32 m0, s0
	s_nop 0
	global_load_lds_dwordx4 v[16:17], off nt
	s_mov_b32 m0, s1
	v_lshl_add_u64 v[16:17], v[14:15], 0, s[84:85]
	s_add_i32 s0, s94, 0x28a0
	s_mov_b32 s1, m0
	s_mov_b32 m0, s0
	s_nop 0
	global_load_lds_dwordx4 v[16:17], off nt
	s_mov_b32 m0, s1
	s_mov_b64 s[0:1], 0x30000
	v_lshl_add_u64 v[16:17], v[14:15], 0, s[0:1]
	s_add_i32 s0, s94, 0x2cb0
	s_mov_b32 s1, m0
	s_mov_b32 m0, s0
	s_nop 0
	global_load_lds_dwordx4 v[16:17], off nt
	s_mov_b32 m0, s1
	s_mov_b64 s[0:1], 0x40000
	v_lshl_add_u64 v[16:17], v[14:15], 0, s[0:1]
	s_add_i32 s0, s94, 0x30c0
	s_mov_b32 s1, m0
	s_mov_b32 m0, s0
	s_nop 0
	global_load_lds_dwordx4 v[16:17], off nt
	s_mov_b32 m0, s1
	s_mov_b64 s[0:1], 0x50000
	v_lshl_add_u64 v[16:17], v[14:15], 0, s[0:1]
	s_add_i32 s0, s94, 0x34d0
	s_mov_b32 s1, m0
	s_mov_b32 m0, s0
	s_nop 0
	global_load_lds_dwordx4 v[16:17], off nt
	s_mov_b32 m0, s1
	s_mov_b64 s[0:1], 0x60000
	v_lshl_add_u64 v[16:17], v[14:15], 0, s[0:1]
	s_add_i32 s0, s94, 0x38e0
	s_mov_b32 s1, m0
	s_mov_b32 m0, s0
	s_nop 0
	global_load_lds_dwordx4 v[16:17], off nt
	s_mov_b32 m0, s1
	v_ashrrev_i32_e32 v7, 31, v6
	s_mov_b64 s[0:1], 0x70000
	v_lshlrev_b64 v[6:7], 12, v[6:7]
	v_lshl_add_u64 v[14:15], v[14:15], 0, s[0:1]
	s_add_i32 s0, s94, 0x3cf0
	s_mov_b32 s1, m0
	s_mov_b32 m0, s0
	s_nop 0
	global_load_lds_dwordx4 v[14:15], off nt
	s_mov_b32 m0, s1
	v_lshl_add_u64 v[6:7], s[36:37], 0, v[6:7]
	s_lshl_b32 s92, s7, 1
	s_waitcnt vmcnt(12)
	v_lshl_add_u64 v[6:7], v[6:7], 0, s[92:93]
	v_lshlrev_b32_e32 v2, 1, v11
	v_lshl_add_u64 v[6:7], v[6:7], 0, v[2:3]
	s_mov_b32 s29, s2
.LBB0_1393:
	ds_read2_b32 v[18:19], v12 offset0:32 offset1:40
	ds_read2_b32 v[20:21], v12 offset1:8
	ds_read2_b32 v[22:23], v12 offset0:64 offset1:72
	ds_read2_b32 v[24:25], v12 offset0:96 offset1:104
	ds_read2_b32 v[26:27], v12 offset0:128 offset1:136
	ds_read2_b32 v[28:29], v12 offset0:160 offset1:168
	ds_read2_b32 v[30:31], v12 offset0:192 offset1:200
	ds_read2_b32 v[32:33], v12 offset0:224 offset1:232
	s_mov_b32 s0, 0x8000
	s_waitcnt lgkmcnt(0)
	v_cvt_pk_bf16_f32 v14, v20, v18
	v_cvt_pk_bf16_f32 v15, v22, v24
	v_cvt_pk_bf16_f32 v16, v26, v28
	v_cvt_pk_bf16_f32 v17, v30, v32
	v_add_co_u32_e32 v18, vcc, s0, v4
	global_store_dwordx4 v[4:5], v[14:17], off nt
	s_mov_b32 s0, 0x10000
	s_nop 0
	v_cvt_pk_bf16_f32 v14, v21, v19
	v_cvt_pk_bf16_f32 v15, v23, v25
	v_cvt_pk_bf16_f32 v16, v27, v29
	v_cvt_pk_bf16_f32 v17, v31, v33
	v_addc_co_u32_e32 v19, vcc, 0, v5, vcc
	global_store_dwordx4 v[18:19], v[14:17], off nt
	ds_read2_b32 v[18:19], v12 offset0:48 offset1:56
	ds_read2_b32 v[20:21], v12 offset0:16 offset1:24
	ds_read2_b32 v[22:23], v12 offset0:80 offset1:88
	ds_read2_b32 v[24:25], v12 offset0:112 offset1:120
	ds_read2_b32 v[26:27], v12 offset0:144 offset1:152
	ds_read2_b32 v[28:29], v12 offset0:176 offset1:184
	ds_read2_b32 v[30:31], v12 offset0:208 offset1:216
	ds_read2_b32 v[32:33], v12 offset0:240 offset1:248
	v_add_co_u32_e32 v34, vcc, s0, v4
	s_waitcnt lgkmcnt(0)
	v_cvt_pk_bf16_f32 v14, v20, v18
	v_addc_co_u32_e32 v35, vcc, 0, v5, vcc
	v_cvt_pk_bf16_f32 v15, v22, v24
	v_cvt_pk_bf16_f32 v16, v26, v28
	v_cvt_pk_bf16_f32 v17, v30, v32
	v_add_co_u32_e32 v18, vcc, 0x18000, v4
	global_store_dwordx4 v[34:35], v[14:17], off nt
	s_nop 1
	v_cvt_pk_bf16_f32 v14, v21, v19
	v_cvt_pk_bf16_f32 v15, v23, v25
	v_cvt_pk_bf16_f32 v16, v27, v29
	v_cvt_pk_bf16_f32 v17, v31, v33
	v_addc_co_u32_e32 v19, vcc, 0, v5, vcc
	global_store_dwordx4 v[18:19], v[14:17], off nt
	s_waitcnt lgkmcnt(0)
.LBB0_1394:
	s_and_b64 vcc, exec, s[34:35]
	s_mov_b32 s24, s29
	s_cbranch_vccnz .LBB0_1427
.LBB0_1395:
	s_add_i32 s29, s24, 0x200
	s_cmp_lt_i32 s29, s67
	s_cselect_b64 s[36:37], -1, 0
	s_cmp_ge_i32 s29, s67
	s_mov_b64 s[0:1], -1
	s_cbranch_scc0 .LBB0_1397
	s_waitcnt vmcnt(0)
	s_mov_b64 s[0:1], 0
.LBB0_1397:
	s_andn2_b64 vcc, exec, s[0:1]
	s_cbranch_vccnz .LBB0_1411
	s_mul_hi_i32 s0, s29, 0x2aaaaaab
	s_lshr_b32 s1, s0, 31
	s_ashr_i32 s6, s0, 14
	s_add_i32 s6, s6, s1
	s_mul_i32 s8, s6, 0xfffe8000
	s_add_i32 s8, s8, s29
	s_add_i32 s0, s8, 0x7fff
	s_cmpk_gt_u32 s0, 0xfffe
	s_mov_b64 s[0:1], -1
	s_cbranch_scc0 .LBB0_1404
	s_and_b32 s0, s8, 0xffff8000
	s_cmpk_lg_u32 s0, 0x8000
	s_mov_b64 s[0:1], -1
	s_cbranch_scc0 .LBB0_1401
	v_readlane_b32 s0, v253, 6
	s_nop 1
	v_mov_b32_e32 v2, s0
	ds_read_b64 v[4:5], v2
	s_mov_b64 s[0:1], 0
	s_waitcnt lgkmcnt(0)
	v_readfirstlane_b32 s2, v4
	v_readfirstlane_b32 s3, v5

.LBB0_1406:
	s_ashr_i32 s0, s8, 31
	s_lshr_b32 s0, s0, 17
	s_add_i32 s42, s8, s0
	s_and_b32 s0, s42, 0xffff8000
	s_sub_i32 s0, s8, s0
	s_ashr_i32 s0, s0, 11
	s_lshl_b32 s1, s6, 4
	s_add_i32 s6, s0, s1
	s_ashr_i32 s7, s6, 31
	s_cmp_lt_i32 s8, 0x10000
	s_cselect_b64 s[0:1], -1, 0
	s_cmp_gt_i32 s8, 0xffff
	s_mov_b64 s[8:9], -1
	s_cbranch_scc0 .LBB0_1408
	s_lshl_b64 s[8:9], s[6:7], 23
	s_add_u32 s34, s25, s8
	s_addc_u32 s35, s26, s9
	s_lshl_b64 s[38:39], s[6:7], 24
	s_mov_b64 s[8:9], 0
.LBB0_1408:
	s_andn2_b64 vcc, exec, s[8:9]
	s_ashr_i32 s8, s42, 15
	s_cbranch_vccnz .LBB0_1410
	s_lshl_b64 s[38:39], s[6:7], 24
	s_add_u32 s34, s27, s38
	s_addc_u32 s35, s28, s39
.LBB0_1410:
	s_lshl_b32 s6, s24, 5
	s_lshl_b32 s7, s24, 6
	s_and_b32 s6, s6, 0x7e0
	s_and_b32 s7, s7, 0xf00
	s_lshl_b32 s8, s8, 7
	s_add_i32 s8, s8, s7
	v_bitop3_b32 v4, s6, v209, v9 bitop3:0xc8
	v_or_b32_e32 v2, s6, v9
	v_or_b32_e32 v4, s8, v4
	s_and_b32 s7, s29, 0x7c0
	v_cndmask_b32_e64 v4, v2, v4, s[0:1]
	v_or_b32_e32 v2, s7, v9
	s_add_u32 s0, s2, s38
	v_lshlrev_b32_e32 v2, 13, v2
	s_addc_u32 s1, s3, s39
	v_lshl_add_u64 v[14:15], s[0:1], 0, v[2:3]
	s_lshl_b32 s92, s6, 2
	v_lshl_add_u64 v[14:15], v[14:15], 0, s[92:93]
	v_lshlrev_b32_e32 v2, 2, v10
	v_lshl_add_u64 v[14:15], v[14:15], 0, v[2:3]
	s_mov_b32 s0, m0
	s_mov_b32 m0, s94
	s_nop 0
	global_load_lds_dwordx4 v[14:15], off nt
	s_mov_b32 m0, s0
	s_mov_b64 s[0:1], 0x10000
	v_lshl_add_u64 v[16:17], v[14:15], 0, s[0:1]
	s_mov_b32 s0, m0
	s_mov_b32 m0, s16
	s_nop 0
	global_load_lds_dwordx4 v[16:17], off nt
	s_mov_b32 m0, s0
	v_lshl_add_u64 v[16:17], v[14:15], 0, s[84:85]
	s_mov_b32 s0, m0
	s_mov_b32 m0, s17
	s_nop 0
	global_load_lds_dwordx4 v[16:17], off nt
	s_mov_b32 m0, s0
	s_mov_b64 s[0:1], 0x30000
	v_lshl_add_u64 v[16:17], v[14:15], 0, s[0:1]
	s_mov_b32 s0, m0
	s_mov_b32 m0, s19
	s_nop 0
	global_load_lds_dwordx4 v[16:17], off nt
	s_mov_b32 m0, s0
	s_mov_b64 s[0:1], 0x40000
	v_lshl_add_u64 v[16:17], v[14:15], 0, s[0:1]
	s_mov_b32 s0, m0
	s_mov_b32 m0, s20
	s_nop 0
	global_load_lds_dwordx4 v[16:17], off nt
	s_mov_b32 m0, s0
	s_mov_b64 s[0:1], 0x50000
	v_lshl_add_u64 v[16:17], v[14:15], 0, s[0:1]
	s_mov_b32 s0, m0
	s_mov_b32 m0, s21
	s_nop 0
	global_load_lds_dwordx4 v[16:17], off nt
	s_mov_b32 m0, s0
	s_mov_b64 s[0:1], 0x60000
	v_lshl_add_u64 v[16:17], v[14:15], 0, s[0:1]
	s_mov_b32 s0, m0
	s_mov_b32 m0, s22
	s_nop 0
	global_load_lds_dwordx4 v[16:17], off nt
	s_mov_b32 m0, s0
	v_ashrrev_i32_e32 v5, 31, v4
	s_mov_b64 s[0:1], 0x70000
	v_lshlrev_b64 v[4:5], 12, v[4:5]
	v_lshl_add_u64 v[14:15], v[14:15], 0, s[0:1]
	s_mov_b32 s0, m0
	s_mov_b32 m0, s23
	s_nop 0
	global_load_lds_dwordx4 v[14:15], off nt
	s_mov_b32 m0, s0
	v_lshl_add_u64 v[4:5], s[34:35], 0, v[4:5]
	s_lshl_b32 s92, s7, 1
	s_waitcnt vmcnt(12)
	v_lshl_add_u64 v[4:5], v[4:5], 0, s[92:93]
	v_lshlrev_b32_e32 v2, 1, v11
	v_lshl_add_u64 v[4:5], v[4:5], 0, v[2:3]
.LBB0_1411:
	v_add_u32_e32 v2, 0x2000, v12
	v_add_u32_e32 v13, 0x2400, v12
	ds_read2_b32 v[18:19], v2 offset0:64 offset1:72
	ds_read2_b32 v[20:21], v2 offset0:32 offset1:40
	ds_read2_b32 v[22:23], v2 offset0:96 offset1:104
	ds_read2_b32 v[24:25], v2 offset0:128 offset1:136
	ds_read2_b32 v[26:27], v2 offset0:160 offset1:168
	ds_read2_b32 v[28:29], v2 offset0:192 offset1:200
	ds_read2_b32 v[30:31], v2 offset0:224 offset1:232
	ds_read2_b32 v[32:33], v13 offset1:8
	s_mov_b32 s0, 0x8000
	s_waitcnt lgkmcnt(0)
	v_cvt_pk_bf16_f32 v14, v20, v18
	v_cvt_pk_bf16_f32 v15, v22, v24
	v_cvt_pk_bf16_f32 v16, v26, v28
	v_cvt_pk_bf16_f32 v17, v30, v32
	v_add_co_u32_e32 v18, vcc, s0, v6
	global_store_dwordx4 v[6:7], v[14:17], off nt
	s_mov_b32 s0, 0x10000
	s_mov_b64 s[34:35], -1
	v_cvt_pk_bf16_f32 v14, v21, v19
	v_cvt_pk_bf16_f32 v15, v23, v25
	v_cvt_pk_bf16_f32 v16, v27, v29
	v_cvt_pk_bf16_f32 v17, v31, v33
	v_addc_co_u32_e32 v19, vcc, 0, v7, vcc
	global_store_dwordx4 v[18:19], v[14:17], off nt
	ds_read2_b32 v[18:19], v2 offset0:80 offset1:88
	ds_read2_b32 v[20:21], v2 offset0:48 offset1:56
	ds_read2_b32 v[22:23], v2 offset0:112 offset1:120
	ds_read2_b32 v[24:25], v2 offset0:144 offset1:152
	ds_read2_b32 v[26:27], v2 offset0:176 offset1:184
	ds_read2_b32 v[28:29], v2 offset0:208 offset1:216
	ds_read2_b32 v[30:31], v2 offset0:240 offset1:248
	ds_read2_b32 v[32:33], v13 offset0:16 offset1:24
	v_add_co_u32_e32 v34, vcc, s0, v6
	s_waitcnt lgkmcnt(0)
	v_cvt_pk_bf16_f32 v14, v20, v18
	v_addc_co_u32_e32 v35, vcc, 0, v7, vcc
	v_cvt_pk_bf16_f32 v15, v22, v24
	v_cvt_pk_bf16_f32 v16, v26, v28
	v_cvt_pk_bf16_f32 v17, v30, v32
	v_add_co_u32_e32 v18, vcc, 0x18000, v6
	global_store_dwordx4 v[34:35], v[14:17], off nt
	s_nop 1
	v_cvt_pk_bf16_f32 v14, v21, v19
	v_cvt_pk_bf16_f32 v15, v23, v25
	v_cvt_pk_bf16_f32 v16, v27, v29
	v_cvt_pk_bf16_f32 v17, v31, v33
	v_addc_co_u32_e32 v19, vcc, 0, v7, vcc
	global_store_dwordx4 v[18:19], v[14:17], off nt
	s_waitcnt lgkmcnt(0)
	s_andn2_b64 vcc, exec, s[36:37]
	s_cbranch_vccnz .LBB0_1394
	s_add_i32 s2, s24, 0x400
	s_cmp_ge_i32 s2, s67
	s_cselect_b64 s[34:35], -1, 0
	s_mov_b64 s[0:1], -1
	s_and_b64 vcc, exec, s[34:35]
	s_cbranch_vccz .LBB0_1414
	s_waitcnt vmcnt(0)
	s_mov_b64 s[0:1], 0
.LBB0_1414:
	s_andn2_b64 vcc, exec, s[0:1]
	s_cbranch_vccnz .LBB0_1393
	s_mul_hi_i32 s0, s2, 0x2aaaaaab
	s_lshr_b32 s1, s0, 31
	s_ashr_i32 s6, s0, 14
	s_add_i32 s6, s6, s1
	s_mul_i32 s8, s6, 0xfffe8000
	s_add_i32 s8, s8, s2
	s_add_i32 s0, s8, 0x7fff
	s_cmpk_gt_u32 s0, 0xfffe
	s_mov_b64 s[0:1], -1
	s_cbranch_scc0 .LBB0_1421
	s_and_b32 s0, s8, 0xffff8000
	s_cmpk_lg_u32 s0, 0x8000
	s_mov_b64 s[0:1], -1
	s_cbranch_scc0 .LBB0_1418
	v_readlane_b32 s0, v253, 6
	s_nop 1
	v_mov_b32_e32 v2, s0
	ds_read_b64 v[6:7], v2
	s_mov_b64 s[0:1], 0
	s_waitcnt lgkmcnt(0)
	v_readfirstlane_b32 s3, v6
	v_readfirstlane_b32 s29, v7
.LBB0_1418:
	s_andn2_b64 vcc, exec, s[0:1]
	s_cbranch_vccnz .LBB0_1420
	v_readlane_b32 s0, v252, 36
	s_nop 1
	v_mov_b32_e32 v2, s0
	ds_read_b64 v[6:7], v2
	s_waitcnt lgkmcnt(0)
	v_readfirstlane_b32 s3, v6
	v_readfirstlane_b32 s29, v7

.LBB0_1421:
	s_andn2_b64 vcc, exec, s[0:1]
	s_cbranch_vccnz .LBB0_1423
	v_readlane_b32 s0, v253, 31
	s_nop 1
	v_mov_b32_e32 v2, s0
	ds_read_b64 v[6:7], v2
	s_waitcnt lgkmcnt(0)
	v_readfirstlane_b32 s3, v6
	v_readfirstlane_b32 s29, v7
.LBB0_1423:
	s_ashr_i32 s0, s8, 31
	s_lshr_b32 s0, s0, 17
	s_add_i32 s42, s8, s0
	s_and_b32 s0, s42, 0xffff8000
	s_sub_i32 s0, s8, s0
	s_ashr_i32 s0, s0, 11
	s_lshl_b32 s1, s6, 4
	s_add_i32 s6, s0, s1
	s_ashr_i32 s7, s6, 31
	s_cmp_lt_i32 s8, 0x10000
	s_cselect_b64 s[0:1], -1, 0
	s_cmp_gt_i32 s8, 0xffff
	s_mov_b64 s[8:9], -1
	s_cbranch_scc0 .LBB0_1425
	s_lshl_b64 s[8:9], s[6:7], 23
	s_add_u32 s36, s25, s8
	s_addc_u32 s37, s26, s9
	s_lshl_b64 s[38:39], s[6:7], 24
	s_mov_b64 s[8:9], 0
.LBB0_1425:
	s_andn2_b64 vcc, exec, s[8:9]
	s_ashr_i32 s8, s42, 15
	s_cbranch_vccnz .LBB0_1392
	s_lshl_b64 s[38:39], s[6:7], 24
	s_add_u32 s36, s27, s38
	s_addc_u32 s37, s28, s39
	s_branch .LBB0_1392
.LBB0_1427:
	s_waitcnt vmcnt(0)
	v_readlane_b32 s26, v254, 28
	v_readlane_b32 s27, v254, 29
.LBB0_1428:
	s_waitcnt vmcnt(0)
	s_barrier

.LBB0_1431:
	s_ashr_i32 s69, s65, 3
	s_or_b32 s66, s64, 0x800
	s_lshl_b32 s16, s69, 1
	s_lshl_b32 s68, s12, 6
	s_add_u32 s70, s40, 0x4ac00000
	s_addc_u32 s71, s41, 0
	s_add_u32 s72, s40, 0x4c580000
	s_addc_u32 s73, s41, 0
	s_add_u32 s74, s40, 0x4d680000
	s_addc_u32 s75, s41, 0
	s_add_u32 s76, s40, 0x4df00000
	s_addc_u32 s77, s41, 0
	s_cmp_lt_i32 s17, 1
	s_cbranch_scc1 .LBB0_1536
	s_cmp_eq_u32 s18, 64
	s_cselect_b64 s[38:39], -1, 0
	s_and_b32 s0, s65, 0x78
	v_readlane_b32 s1, v254, 62
	s_add_i32 s6, s1, s0
	s_add_i32 s0, s6, s68
	s_add_i32 s18, s0, s66
	s_cmp_lt_u32 s18, s15
	s_mul_hi_u32 s1, s18, 0xaaaaaaab
	s_cselect_b64 s[42:43], -1, 0
	s_lshr_b32 s1, s1, 16
	s_mul_i32 s2, s1, 0xfffe8000
	s_add_i32 s7, s2, s18
	s_ashr_i32 s2, s7, 31
	s_lshr_b32 s2, s2, 17
	s_add_i32 s2, s7, s2
	s_ashr_i32 s8, s2, 15
	s_and_b32 s2, s2, 0xffff8000
	s_sub_i32 s2, s7, s2
	s_ashr_i32 s2, s2, 11
	s_add_i32 s3, s7, 0x7fff
	s_cmpk_gt_u32 s3, 0xfffe
	s_cselect_b64 s[44:45], -1, 0
	s_and_b32 s3, s7, 0xffff8000
	s_cmpk_lg_u32 s3, 0x8000
	s_cselect_b64 s[46:47], -1, 0
	s_lshl_b32 s1, s1, 4
	s_add_i32 s2, s2, s1
	s_ashr_i32 s3, s2, 31
	s_add_u32 s19, s40, 0x23840000
	s_addc_u32 s20, s41, 0
	s_lshl_b64 s[48:49], s[2:3], 24
	s_add_u32 s21, s40, 0x3840000
	s_addc_u32 s22, s41, 0
	s_lshl_b32 s1, s6, 5
	s_and_b32 s23, s1, 0x7e0
	s_and_b32 s9, s0, 0x7c0
	s_add_i32 s24, s18, 0x200
	s_cmp_lt_u32 s24, s15
	s_cselect_b64 s[50:51], -1, 0
	s_cmp_ge_u32 s24, s15
	s_mul_hi_u32 s0, s24, 0xaaaaaaab
	s_cselect_b64 s[52:53], -1, 0
	s_lshr_b32 s0, s0, 16
	s_mul_i32 s1, s0, 0xfffe8000
	s_add_i32 s25, s1, s24
	s_ashr_i32 s1, s25, 31
	s_lshr_b32 s1, s1, 17
	s_add_i32 s1, s25, s1
	s_ashr_i32 s26, s1, 15
	s_and_b32 s1, s1, 0xffff8000
	s_sub_i32 s1, s25, s1
	s_ashr_i32 s1, s1, 11
	s_add_i32 s27, s25, 0x7fff
	s_cmpk_gt_u32 s27, 0xfffe
	s_cselect_b64 s[54:55], -1, 0
	s_and_b32 s27, s25, 0xffff8000
	s_cmpk_lg_u32 s27, 0x8000
	s_cselect_b64 s[56:57], -1, 0
	s_lshl_b32 s0, s0, 4
	s_add_i32 s0, s1, s0
	s_ashr_i32 s1, s0, 31
	s_lshl_b64 s[58:59], s[0:1], 24
	s_and_b32 s27, s24, 0x7c0
	v_lshrrev_b32_e32 v143, 3, v8
	s_cmp_lt_i32 s25, 0x10000
	v_or_b32_e32 v2, s9, v143
	s_cselect_b64 vcc, -1, 0
	s_lshl_b32 s6, s6, 6
	v_lshlrev_b32_e32 v140, 13, v2
	v_and_b32_e32 v2, 7, v154
	v_or_b32_e32 v4, s27, v143
	s_lshl_b32 s25, s26, 7
	s_and_b32 s6, s6, 0xf00
	v_lshlrev_b32_e32 v146, 13, v4
	v_mul_u32_u24_e32 v4, 0x410, v2
	v_lshlrev_b32_e32 v5, 2, v143
	s_add_i32 s25, s25, s6
	v_bitop3_b32 v7, s23, v209, v143 bitop3:0xc8
	v_add3_u32 v145, s94, v4, v5
	v_or_b32_e32 v4, s25, v7
	s_add_u32 s25, s21, s58
	s_addc_u32 s26, s22, s59
	s_lshl_b64 s[0:1], s[0:1], 23
	s_add_u32 s28, s19, s0
	s_addc_u32 s29, s20, s1
	s_cmp_lt_i32 s7, 0x10000
	s_cselect_b64 s[0:1], -1, 0
	s_lshl_b32 s7, s8, 7
	s_add_i32 s7, s7, s6
	s_add_u32 s6, s21, s48
	v_or_b32_e32 v7, s7, v7
	s_addc_u32 s7, s22, s49
	s_lshl_b64 s[2:3], s[2:3], 23
	v_or_b32_e32 v6, s23, v143
	s_add_u32 s2, s19, s2
	v_cndmask_b32_e32 v4, v6, v4, vcc
	v_cndmask_b32_e64 v6, v6, v7, s[0:1]
	s_addc_u32 s3, s20, s3
	v_ashrrev_i32_e32 v7, 31, v6
	s_and_b64 s[0:1], s[0:1], exec
	v_lshlrev_b64 v[6:7], 12, v[6:7]
	s_cselect_b32 s1, s7, s3
	s_cselect_b32 s0, s6, s2
	s_lshl_b32 s92, s9, 1
	v_ashrrev_i32_e32 v5, 31, v4
	v_lshl_add_u64 v[6:7], s[0:1], 0, v[6:7]
	s_and_b64 s[0:1], vcc, exec
	v_lshlrev_b32_e32 v142, 2, v2
	v_lshlrev_b32_e32 v144, 3, v2
	v_lshlrev_b64 v[4:5], 12, v[4:5]
	v_lshl_add_u64 v[6:7], v[6:7], 0, s[92:93]
	v_lshlrev_b32_e32 v2, 4, v2
	s_cselect_b32 s1, s26, s29
	s_cselect_b32 s0, s25, s28
	v_lshl_add_u64 v[148:149], v[6:7], 0, v[2:3]
	v_lshl_add_u64 v[4:5], s[0:1], 0, v[4:5]
	s_mov_b64 s[0:1], 0x8000
	s_lshl_b32 s92, s27, 1
	v_lshl_add_u64 v[152:153], v[148:149], 0, s[0:1]
	s_mov_b64 s[0:1], 0x10000
	v_lshl_add_u64 v[4:5], v[4:5], 0, s[92:93]
	v_lshl_add_u64 v[154:155], v[148:149], 0, s[0:1]
	s_mov_b64 s[0:1], 0x18000
	v_mov_b32_e32 v141, v3
	v_mov_b32_e32 v147, v3
	v_lshl_add_u64 v[150:151], v[4:5], 0, v[2:3]
	v_lshl_add_u64 v[156:157], v[148:149], 0, s[0:1]
	s_mov_b32 s25, 0
	s_branch .LBB0_1437
.LBB0_1433:
	s_waitcnt vmcnt(0)
.LBB0_1434:
	v_readlane_b32 s80, v253, 20
	v_readlane_b32 s81, v253, 21
	v_readlane_b32 s81, v252, 44
	s_barrier

.LBB0_1472:
	v_mov_b32_e32 v2, v171
	s_nop 1
	v_permlane32_swap_b32_e32 v171, v2
	s_and_saveexec_b64 s[0:1], s[36:37]
	v_add_f32_e32 v2, v171, v2
	ds_write_b32 v170, v2 offset:128
	s_or_b64 exec, exec, s[0:1]
	s_waitcnt lgkmcnt(0)
	v_add_u32_e32 v2, s28, v169
	ds_read_b128 v[36:39], v2 offset:128
	ds_read_b128 v[40:43], v2 offset:160
	s_lshl_b64 s[0:1], s[60:61], 12
	s_add_u32 s0, s40, s0
	s_addc_u32 s1, s41, s1
	s_waitcnt lgkmcnt(1)
	v_rcp_f32_e32 v44, v36
	v_rcp_f32_e32 v45, v37
	v_rcp_f32_e32 v46, v38
	v_rcp_f32_e32 v47, v39
	s_waitcnt lgkmcnt(0)
	v_rcp_f32_e32 v48, v40
	ds_read_b128 v[36:39], v2 offset:192
	v_rcp_f32_e32 v49, v41
	v_rcp_f32_e32 v50, v42
	v_rcp_f32_e32 v51, v43
	ds_read_b128 v[40:43], v2 offset:224
	s_lshl_b32 s2, s29, 1
	s_add_u32 s0, s0, s2
	s_addc_u32 s1, s1, 0
	s_lshl_b32 s2, s8, 12
	s_add_i32 s2, s2, 0
	s_waitcnt lgkmcnt(1)
	v_rcp_f32_e32 v2, v36
	v_rcp_f32_e32 v36, v37
	v_rcp_f32_e32 v37, v38
	v_rcp_f32_e32 v38, v39
	s_waitcnt lgkmcnt(0)
	v_rcp_f32_e32 v39, v40
	v_rcp_f32_e32 v40, v41
	v_rcp_f32_e32 v41, v42
	v_rcp_f32_e32 v42, v43
	s_add_i32 s2, s2, 0x14800
	v_lshlrev_b32_e32 v43, 9, v167
	v_lshlrev_b32_e32 v52, 1, v166
	v_mul_f32_e32 v4, v4, v44
	v_add3_u32 v43, s2, v43, v52
	v_cvt_pk_bf16_f32 v4, v4, s0
	ds_write_b16 v43, v4
	v_mul_f32_e32 v4, v20, v44
	v_cvt_pk_bf16_f32 v4, v4, s0
	ds_write_b16 v43, v4 offset:64
	v_mul_f32_e32 v4, v5, v45
	v_cvt_pk_bf16_f32 v4, v4, s0
	ds_write_b16 v43, v4 offset:128
	v_mul_f32_e32 v4, v21, v45
	v_cvt_pk_bf16_f32 v4, v4, s0
	ds_write_b16 v43, v4 offset:192
	v_mul_f32_e32 v4, v6, v46
	v_cvt_pk_bf16_f32 v4, v4, s0
	ds_write_b16 v43, v4 offset:256
	v_mul_f32_e32 v4, v22, v46
	v_cvt_pk_bf16_f32 v4, v4, s0
	ds_write_b16 v43, v4 offset:320
	v_mul_f32_e32 v4, v7, v47
	v_cvt_pk_bf16_f32 v4, v4, s0
	ds_write_b16 v43, v4 offset:384
	v_mul_f32_e32 v4, v23, v47
	v_cvt_pk_bf16_f32 v4, v4, s0
	ds_write_b16 v43, v4 offset:448
	v_mul_f32_e32 v4, v8, v48
	v_cvt_pk_bf16_f32 v4, v4, s0
	ds_write_b16 v43, v4 offset:1024
	v_mul_f32_e32 v4, v24, v48
	v_cvt_pk_bf16_f32 v4, v4, s0
	ds_write_b16 v43, v4 offset:1088
	v_mul_f32_e32 v4, v9, v49
	v_cvt_pk_bf16_f32 v4, v4, s0
	ds_write_b16 v43, v4 offset:1152
	v_mul_f32_e32 v4, v25, v49
	v_cvt_pk_bf16_f32 v4, v4, s0
	ds_write_b16 v43, v4 offset:1216
	v_mul_f32_e32 v4, v10, v50
	v_cvt_pk_bf16_f32 v4, v4, s0
	ds_write_b16 v43, v4 offset:1280
	v_mul_f32_e32 v4, v26, v50
	v_cvt_pk_bf16_f32 v4, v4, s0
	ds_write_b16 v43, v4 offset:1344
	v_mul_f32_e32 v4, v11, v51
	v_cvt_pk_bf16_f32 v4, v4, s0
	ds_write_b16 v43, v4 offset:1408
	v_mul_f32_e32 v4, v27, v51
	v_cvt_pk_bf16_f32 v4, v4, s0
	ds_write_b16 v43, v4 offset:1472
	v_mul_f32_e32 v4, v12, v2
	v_mul_f32_e32 v2, v28, v2
	v_cvt_pk_bf16_f32 v2, v2, s0
	ds_write_b16 v43, v2 offset:2112
	v_mul_f32_e32 v2, v13, v36
	v_cvt_pk_bf16_f32 v2, v2, s0
	ds_write_b16 v43, v2 offset:2176
	v_mul_f32_e32 v2, v29, v36
	v_cvt_pk_bf16_f32 v2, v2, s0
	ds_write_b16 v43, v2 offset:2240
	v_mul_f32_e32 v2, v14, v37
	v_cvt_pk_bf16_f32 v2, v2, s0
	ds_write_b16 v43, v2 offset:2304
	v_mul_f32_e32 v2, v30, v37
	v_cvt_pk_bf16_f32 v2, v2, s0
	ds_write_b16 v43, v2 offset:2368
	v_mul_f32_e32 v2, v15, v38
	v_cvt_pk_bf16_f32 v2, v2, s0
	ds_write_b16 v43, v2 offset:2432
	v_mul_f32_e32 v2, v31, v38
	v_cvt_pk_bf16_f32 v2, v2, s0
	ds_write_b16 v43, v2 offset:2496
	v_mul_f32_e32 v2, v16, v39
	v_cvt_pk_bf16_f32 v2, v2, s0
	ds_write_b16 v43, v2 offset:3072
	v_mul_f32_e32 v2, v32, v39
	v_cvt_pk_bf16_f32 v2, v2, s0
	ds_write_b16 v43, v2 offset:3136
	v_mul_f32_e32 v2, v17, v40
	v_cvt_pk_bf16_f32 v2, v2, s0
	ds_write_b16 v43, v2 offset:3200
	v_mul_f32_e32 v2, v33, v40
	v_cvt_pk_bf16_f32 v2, v2, s0
	ds_write_b16 v43, v2 offset:3264
	v_mul_f32_e32 v2, v18, v41
	v_cvt_pk_bf16_f32 v2, v2, s0
	ds_write_b16 v43, v2 offset:3328
	v_mul_f32_e32 v2, v34, v41
	v_cvt_pk_bf16_f32 v2, v2, s0
	ds_write_b16 v43, v2 offset:3392
	v_mul_f32_e32 v2, v19, v42
	v_cvt_pk_bf16_f32 v2, v2, s0
	ds_write_b16 v43, v2 offset:3456
	v_mul_f32_e32 v2, v35, v42
	v_cvt_pk_bf16_f32 v2, v2, s0
	ds_write_b16 v43, v2 offset:3520
	v_lshlrev_b32_e32 v2, 1, v165
	v_cvt_pk_bf16_f32 v4, v4, s0
	v_and_b32_e32 v2, 0x70, v2
	ds_write_b16 v43, v4 offset:2048
	v_lshrrev_b32_e32 v16, 3, v164
	v_add_u32_e32 v17, s2, v2
	s_waitcnt lgkmcnt(0)
	v_lshl_add_u64 v[4:5], s[0:1], 0, v[2:3]
	s_mov_b64 s[0:1], 0x51200c00
	v_lshl_add_u32 v2, v16, 7, v17
	v_or_b32_e32 v18, 8, v16
	v_lshl_add_u64 v[12:13], v[4:5], 0, s[0:1]
	ds_read_b128 v[4:7], v2
	v_lshl_add_u32 v8, v18, 7, v17
	ds_read_b128 v[8:11], v8
	v_lshlrev_b32_e32 v2, 12, v16
	v_lshl_add_u64 v[14:15], v[12:13], 0, v[2:3]
	v_lshlrev_b32_e32 v2, 12, v18
	s_waitcnt lgkmcnt(1)
	global_store_dwordx4 v[14:15], v[4:7], off
	s_nop 1
	v_lshl_add_u64 v[4:5], v[12:13], 0, v[2:3]
	v_or_b32_e32 v2, 16, v16
	s_waitcnt lgkmcnt(0)
	global_store_dwordx4 v[4:5], v[8:11], off
	v_lshl_add_u32 v4, v2, 7, v17
	v_or_b32_e32 v16, 24, v16
	ds_read_b128 v[4:7], v4
	v_lshl_add_u32 v8, v16, 7, v17
	ds_read_b128 v[8:11], v8
	v_lshlrev_b32_e32 v2, 12, v2
	v_lshl_add_u64 v[14:15], v[12:13], 0, v[2:3]
	v_lshlrev_b32_e32 v2, 12, v16
	s_waitcnt lgkmcnt(1)
	global_store_dwordx4 v[14:15], v[4:7], off
	s_nop 1
	v_lshl_add_u64 v[4:5], v[12:13], 0, v[2:3]
	s_waitcnt lgkmcnt(0)
	global_store_dwordx4 v[4:5], v[8:11], off
	s_setprio 0
	s_cmp_eq_u32 s25, 0
	v_readlane_b32 s2, v253, 11
	s_cselect_b64 s[0:1], -1, 0
	v_readlane_b32 s3, v253, 12
	s_and_b64 s[0:1], s[2:3], s[0:1]
	s_waitcnt lgkmcnt(0)
	s_barrier
	s_and_b64 s[0:1], s[0:1], s[38:39]
	s_andn2_b64 vcc, exec, s[0:1]
	s_cbranch_vccnz .LBB0_1435
	s_andn2_b64 vcc, exec, s[42:43]
	s_cbranch_vccnz .LBB0_1434
	s_mov_b64 s[0:1], -1
	s_and_b64 vcc, exec, s[44:45]
	s_cbranch_vccz .LBB0_1482
	s_and_b64 vcc, exec, s[46:47]
	s_cbranch_vccz .LBB0_1479
	v_readlane_b32 s0, v253, 6
	s_nop 1
	v_mov_b32_e32 v2, s0
	ds_read_b64 v[4:5], v2
	s_mov_b64 s[0:1], 0
	s_waitcnt lgkmcnt(0)
	v_readfirstlane_b32 s2, v4
	v_readfirstlane_b32 s3, v5

.LBB0_1484:
	s_add_u32 s0, s2, s48
	s_addc_u32 s1, s3, s49
	v_lshl_add_u64 v[4:5], s[0:1], 0, v[140:141]
	s_lshl_b32 s92, s23, 2
	v_lshl_add_u64 v[6:7], v[4:5], 0, s[92:93]
	v_lshlrev_b32_e32 v4, 2, v142
	v_mov_b32_e32 v5, v3
	v_lshl_add_u64 v[6:7], v[6:7], 0, v[4:5]
	s_mov_b32 s0, m0
	s_mov_b32 m0, s94
	s_nop 0
	global_load_lds_dwordx4 v[6:7], off nt
	s_mov_b32 m0, s0
	s_mov_b64 s[0:1], 0x10000
	v_lshl_add_u64 v[8:9], v[6:7], 0, s[0:1]
	s_add_i32 s26, s94, 0x410
	s_mov_b32 s0, m0
	s_mov_b32 m0, s26
	s_nop 0
	global_load_lds_dwordx4 v[8:9], off nt
	s_mov_b32 m0, s0
	v_lshl_add_u64 v[8:9], v[6:7], 0, s[84:85]
	s_add_i32 s27, s94, 0x820
	s_mov_b32 s0, m0
	s_mov_b32 m0, s27
	s_nop 0
	global_load_lds_dwordx4 v[8:9], off nt
	s_mov_b32 m0, s0
	s_mov_b64 s[0:1], 0x30000
	v_lshl_add_u64 v[8:9], v[6:7], 0, s[0:1]
	s_add_i32 s28, s94, 0xc30
	s_mov_b32 s0, m0
	s_mov_b32 m0, s28
	s_nop 0
	global_load_lds_dwordx4 v[8:9], off nt
	s_mov_b32 m0, s0
	s_mov_b64 s[0:1], 0x40000
	v_lshl_add_u64 v[8:9], v[6:7], 0, s[0:1]
	s_add_i32 s29, s94, 0x1040
	s_mov_b32 s0, m0
	s_mov_b32 m0, s29
	s_nop 0
	global_load_lds_dwordx4 v[8:9], off nt
	s_mov_b32 m0, s0
	s_mov_b64 s[0:1], 0x50000
	v_lshl_add_u64 v[8:9], v[6:7], 0, s[0:1]
	s_add_i32 s78, s94, 0x1450
	s_mov_b32 s0, m0
	s_mov_b32 m0, s78
	s_nop 0
	global_load_lds_dwordx4 v[8:9], off nt
	s_mov_b32 m0, s0
	s_mov_b64 s[0:1], 0x60000
	v_lshl_add_u64 v[8:9], v[6:7], 0, s[0:1]
	s_add_i32 s79, s94, 0x1860
	s_mov_b32 s0, m0
	s_mov_b32 m0, s79
	s_nop 0
	global_load_lds_dwordx4 v[8:9], off nt
	s_mov_b32 m0, s0
	s_mov_b64 s[0:1], 0x70000
	v_lshl_add_u64 v[6:7], v[6:7], 0, s[0:1]
	s_add_i32 s80, s94, 0x1c70
	s_mov_b32 s0, m0
	s_mov_b32 m0, s80
	s_nop 0
	global_load_lds_dwordx4 v[6:7], off nt
	s_mov_b32 m0, s0
	s_mov_b64 s[0:1], -1
	s_and_b64 vcc, exec, s[52:53]
	s_cbranch_vccz .LBB0_1486
	s_waitcnt vmcnt(0)
	s_mov_b64 s[0:1], 0
.LBB0_1486:
	s_andn2_b64 vcc, exec, s[0:1]
	v_mov_b64_e32 v[6:7], v[148:149]
	s_cbranch_vccnz .LBB0_1496
	s_mov_b64 s[0:1], -1
	s_and_b64 vcc, exec, s[54:55]
	s_cbranch_vccz .LBB0_1493
	s_and_b64 vcc, exec, s[56:57]
	s_cbranch_vccz .LBB0_1490
	v_readlane_b32 s0, v253, 6
	s_nop 1
	v_mov_b32_e32 v2, s0
	ds_read_b64 v[6:7], v2
	s_mov_b64 s[0:1], 0
	s_waitcnt lgkmcnt(0)
	v_readfirstlane_b32 s2, v6
	v_readfirstlane_b32 s3, v7
.LBB0_1490:
	s_andn2_b64 vcc, exec, s[0:1]
	s_cbranch_vccnz .LBB0_1492
	v_readlane_b32 s0, v252, 36
	s_nop 1
	v_mov_b32_e32 v2, s0
	ds_read_b64 v[6:7], v2
	s_waitcnt lgkmcnt(0)
	v_readfirstlane_b32 s2, v6
	v_readfirstlane_b32 s3, v7

.LBB0_1493:
	s_andn2_b64 vcc, exec, s[0:1]
	s_cbranch_vccnz .LBB0_1495
	v_readlane_b32 s0, v253, 31
	s_nop 1
	v_mov_b32_e32 v2, s0
	ds_read_b64 v[6:7], v2
	s_waitcnt lgkmcnt(0)
	v_readfirstlane_b32 s2, v6
	v_readfirstlane_b32 s3, v7
.LBB0_1495:
	s_add_u32 s0, s2, s58
	s_addc_u32 s1, s3, s59
	v_lshl_add_u64 v[6:7], s[0:1], 0, v[146:147]
	v_lshl_add_u64 v[6:7], v[6:7], 0, s[92:93]
	v_mov_b32_e32 v5, v3
	v_lshl_add_u64 v[6:7], v[6:7], 0, v[4:5]
	s_add_i32 s0, s94, 0x2080
	s_mov_b32 s1, m0
	s_mov_b32 m0, s0
	s_nop 0
	global_load_lds_dwordx4 v[6:7], off nt
	s_mov_b32 m0, s1
	s_mov_b64 s[0:1], 0x10000
	v_lshl_add_u64 v[8:9], v[6:7], 0, s[0:1]
	s_add_i32 s0, s94, 0x2490
	s_mov_b32 s1, m0
	s_mov_b32 m0, s0
	s_nop 0
	global_load_lds_dwordx4 v[8:9], off nt
	s_mov_b32 m0, s1
	v_lshl_add_u64 v[8:9], v[6:7], 0, s[84:85]
	s_add_i32 s0, s94, 0x28a0
	s_mov_b32 s1, m0
	s_mov_b32 m0, s0
	s_nop 0
	global_load_lds_dwordx4 v[8:9], off nt
	s_mov_b32 m0, s1
	s_mov_b64 s[0:1], 0x30000
	v_lshl_add_u64 v[8:9], v[6:7], 0, s[0:1]
	s_add_i32 s0, s94, 0x2cb0
	s_mov_b32 s1, m0
	s_mov_b32 m0, s0
	s_nop 0
	global_load_lds_dwordx4 v[8:9], off nt
	s_mov_b32 m0, s1
	s_mov_b64 s[0:1], 0x40000
	v_lshl_add_u64 v[8:9], v[6:7], 0, s[0:1]
	s_add_i32 s0, s94, 0x30c0
	s_mov_b32 s1, m0
	s_mov_b32 m0, s0
	s_nop 0
	global_load_lds_dwordx4 v[8:9], off nt
	s_mov_b32 m0, s1
	s_mov_b64 s[0:1], 0x50000
	v_lshl_add_u64 v[8:9], v[6:7], 0, s[0:1]
	s_add_i32 s0, s94, 0x34d0
	s_mov_b32 s1, m0
	s_mov_b32 m0, s0
	s_nop 0
	global_load_lds_dwordx4 v[8:9], off nt
	s_mov_b32 m0, s1
	s_mov_b64 s[0:1], 0x60000
	v_lshl_add_u64 v[8:9], v[6:7], 0, s[0:1]
	s_add_i32 s0, s94, 0x38e0
	s_mov_b32 s1, m0
	s_mov_b32 m0, s0
	s_nop 0
	global_load_lds_dwordx4 v[8:9], off nt
	s_mov_b32 m0, s1
	s_mov_b64 s[0:1], 0x70000
	v_lshl_add_u64 v[6:7], v[6:7], 0, s[0:1]
	s_add_i32 s0, s94, 0x3cf0
	s_mov_b32 s1, m0
	s_mov_b32 m0, s0
	s_nop 0
	global_load_lds_dwordx4 v[6:7], off nt
	s_mov_b32 m0, s1
	s_waitcnt vmcnt(8)
	v_mov_b64_e32 v[6:7], v[150:151]
.LBB0_1496:
	ds_read2_b32 v[12:13], v145 offset0:32 offset1:40
	ds_read2_b32 v[14:15], v145 offset1:8
	ds_read2_b32 v[16:17], v145 offset0:64 offset1:72
	ds_read2_b32 v[18:19], v145 offset0:96 offset1:104
	ds_read2_b32 v[20:21], v145 offset0:128 offset1:136
	ds_read2_b32 v[22:23], v145 offset0:160 offset1:168
	ds_read2_b32 v[24:25], v145 offset0:192 offset1:200
	ds_read2_b32 v[26:27], v145 offset0:224 offset1:232
	s_andn2_b64 vcc, exec, s[52:53]
	s_waitcnt lgkmcnt(6)
	v_cvt_pk_bf16_f32 v8, v14, v12
	s_waitcnt lgkmcnt(4)
	v_cvt_pk_bf16_f32 v9, v16, v18
	s_waitcnt lgkmcnt(2)
	v_cvt_pk_bf16_f32 v10, v20, v22
	s_waitcnt lgkmcnt(0)
	v_cvt_pk_bf16_f32 v11, v24, v26
	global_store_dwordx4 v[148:149], v[8:11], off nt
	s_mov_b32 s81, s24
	s_nop 0
	v_cvt_pk_bf16_f32 v8, v15, v13
	v_cvt_pk_bf16_f32 v9, v17, v19
	v_cvt_pk_bf16_f32 v10, v21, v23
	v_cvt_pk_bf16_f32 v11, v25, v27
	global_store_dwordx4 v[152:153], v[8:11], off nt
	ds_read2_b32 v[12:13], v145 offset0:48 offset1:56
	ds_read2_b32 v[14:15], v145 offset0:16 offset1:24
	ds_read2_b32 v[16:17], v145 offset0:80 offset1:88
	ds_read2_b32 v[18:19], v145 offset0:112 offset1:120
	ds_read2_b32 v[20:21], v145 offset0:144 offset1:152
	ds_read2_b32 v[22:23], v145 offset0:176 offset1:184
	ds_read2_b32 v[24:25], v145 offset0:208 offset1:216
	ds_read2_b32 v[26:27], v145 offset0:240 offset1:248
	s_waitcnt lgkmcnt(6)
	v_cvt_pk_bf16_f32 v8, v14, v12
	s_waitcnt lgkmcnt(4)
	v_cvt_pk_bf16_f32 v9, v16, v18
	s_waitcnt lgkmcnt(2)
	v_cvt_pk_bf16_f32 v10, v20, v22
	s_waitcnt lgkmcnt(0)
	v_cvt_pk_bf16_f32 v11, v24, v26
	global_store_dwordx4 v[154:155], v[8:11], off nt
	s_nop 1
	v_cvt_pk_bf16_f32 v8, v15, v13
	v_cvt_pk_bf16_f32 v9, v17, v19
	v_cvt_pk_bf16_f32 v10, v21, v23
	v_cvt_pk_bf16_f32 v11, v25, v27
	global_store_dwordx4 v[156:157], v[8:11], off nt
	s_waitcnt lgkmcnt(0)
	s_cbranch_vccnz .LBB0_1498
	s_waitcnt vmcnt(0)
	s_mov_b32 s81, s18
.LBB0_1498:
	s_andn2_b64 vcc, exec, s[50:51]
	v_mov_b64_e32 v[8:9], v[148:149]
	s_cbranch_vccz .LBB0_1502
	s_branch .LBB0_1434
.LBB0_1499:
	s_lshl_b32 s6, s81, 5
	s_lshl_b32 s7, s81, 6
	s_and_b32 s6, s6, 0x7e0
	s_and_b32 s7, s7, 0xf00
	s_lshl_b32 s8, s8, 7
	s_add_i32 s8, s8, s7
	v_bitop3_b32 v5, s6, v209, v143 bitop3:0xc8
	v_or_b32_e32 v2, s6, v143
	v_or_b32_e32 v5, s8, v5
	s_and_b32 s7, s2, 0x7c0
	v_cndmask_b32_e64 v6, v2, v5, s[0:1]
	v_or_b32_e32 v2, s7, v143
	s_add_u32 s0, s3, s62
	v_lshlrev_b32_e32 v2, 13, v2
	s_addc_u32 s1, s82, s63
	v_lshl_add_u64 v[10:11], s[0:1], 0, v[2:3]
	s_lshl_b32 s92, s6, 2
	v_lshl_add_u64 v[10:11], v[10:11], 0, s[92:93]
	v_mov_b32_e32 v5, v3
	v_lshl_add_u64 v[10:11], v[10:11], 0, v[4:5]
	s_add_i32 s0, s94, 0x2080
	s_mov_b32 s1, m0
	s_mov_b32 m0, s0
	s_nop 0
	global_load_lds_dwordx4 v[10:11], off nt
	s_mov_b32 m0, s1
	s_mov_b64 s[0:1], 0x10000
	v_lshl_add_u64 v[12:13], v[10:11], 0, s[0:1]
	s_add_i32 s0, s94, 0x2490
	s_mov_b32 s1, m0
	s_mov_b32 m0, s0
	s_nop 0
	global_load_lds_dwordx4 v[12:13], off nt
	s_mov_b32 m0, s1
	v_lshl_add_u64 v[12:13], v[10:11], 0, s[84:85]
	s_add_i32 s0, s94, 0x28a0
	s_mov_b32 s1, m0
	s_mov_b32 m0, s0
	s_nop 0
	global_load_lds_dwordx4 v[12:13], off nt
	s_mov_b32 m0, s1
	s_mov_b64 s[0:1], 0x30000
	v_lshl_add_u64 v[12:13], v[10:11], 0, s[0:1]
	s_add_i32 s0, s94, 0x2cb0
	s_mov_b32 s1, m0
	s_mov_b32 m0, s0
	s_nop 0
	global_load_lds_dwordx4 v[12:13], off nt
	s_mov_b32 m0, s1
	s_mov_b64 s[0:1], 0x40000
	v_lshl_add_u64 v[12:13], v[10:11], 0, s[0:1]
	s_add_i32 s0, s94, 0x30c0
	s_mov_b32 s1, m0
	s_mov_b32 m0, s0
	s_nop 0
	global_load_lds_dwordx4 v[12:13], off nt
	s_mov_b32 m0, s1
	s_mov_b64 s[0:1], 0x50000
	v_lshl_add_u64 v[12:13], v[10:11], 0, s[0:1]
	s_add_i32 s0, s94, 0x34d0
	s_mov_b32 s1, m0
	s_mov_b32 m0, s0
	s_nop 0
	global_load_lds_dwordx4 v[12:13], off nt
	s_mov_b32 m0, s1
	s_mov_b64 s[0:1], 0x60000
	v_lshl_add_u64 v[12:13], v[10:11], 0, s[0:1]
	s_add_i32 s0, s94, 0x38e0
	s_mov_b32 s1, m0
	s_mov_b32 m0, s0
	s_nop 0
	global_load_lds_dwordx4 v[12:13], off nt
	s_mov_b32 m0, s1
	v_ashrrev_i32_e32 v7, 31, v6
	s_mov_b64 s[0:1], 0x70000
	v_lshlrev_b64 v[6:7], 12, v[6:7]
	v_lshl_add_u64 v[10:11], v[10:11], 0, s[0:1]
	s_add_i32 s0, s94, 0x3cf0
	s_mov_b32 s1, m0
	s_mov_b32 m0, s0
	s_nop 0
	global_load_lds_dwordx4 v[10:11], off nt
	s_mov_b32 m0, s1
	v_lshl_add_u64 v[6:7], s[60:61], 0, v[6:7]
	s_lshl_b32 s92, s7, 1
	s_waitcnt vmcnt(12)
	v_lshl_add_u64 v[6:7], v[6:7], 0, s[92:93]
	v_lshlrev_b32_e32 v2, 1, v144
	v_lshl_add_u64 v[6:7], v[6:7], 0, v[2:3]
	s_mov_b32 s82, s2
.LBB0_1500:
	ds_read2_b32 v[14:15], v145 offset0:32 offset1:40
	ds_read2_b32 v[16:17], v145 offset1:8
	ds_read2_b32 v[18:19], v145 offset0:64 offset1:72
	ds_read2_b32 v[20:21], v145 offset0:96 offset1:104
	ds_read2_b32 v[22:23], v145 offset0:128 offset1:136
	ds_read2_b32 v[24:25], v145 offset0:160 offset1:168
	ds_read2_b32 v[26:27], v145 offset0:192 offset1:200
	ds_read2_b32 v[28:29], v145 offset0:224 offset1:232
	s_mov_b32 s0, 0x8000
	s_waitcnt lgkmcnt(6)
	v_cvt_pk_bf16_f32 v10, v16, v14
	s_waitcnt lgkmcnt(4)
	v_cvt_pk_bf16_f32 v11, v18, v20
	s_waitcnt lgkmcnt(2)
	v_cvt_pk_bf16_f32 v12, v22, v24
	s_waitcnt lgkmcnt(0)
	v_cvt_pk_bf16_f32 v13, v26, v28
	v_add_co_u32_e32 v14, vcc, s0, v8
	global_store_dwordx4 v[8:9], v[10:13], off nt
	s_mov_b32 s0, 0x10000
	s_nop 0
	v_cvt_pk_bf16_f32 v10, v17, v15
	v_cvt_pk_bf16_f32 v11, v19, v21
	v_cvt_pk_bf16_f32 v12, v23, v25
	v_cvt_pk_bf16_f32 v13, v27, v29
	v_addc_co_u32_e32 v15, vcc, 0, v9, vcc
	global_store_dwordx4 v[14:15], v[10:13], off nt
	ds_read2_b32 v[14:15], v145 offset0:48 offset1:56
	ds_read2_b32 v[16:17], v145 offset0:16 offset1:24
	ds_read2_b32 v[18:19], v145 offset0:80 offset1:88
	ds_read2_b32 v[20:21], v145 offset0:112 offset1:120
	ds_read2_b32 v[22:23], v145 offset0:144 offset1:152
	ds_read2_b32 v[24:25], v145 offset0:176 offset1:184
	ds_read2_b32 v[26:27], v145 offset0:208 offset1:216
	ds_read2_b32 v[28:29], v145 offset0:240 offset1:248
	v_add_co_u32_e32 v30, vcc, s0, v8
	s_waitcnt lgkmcnt(6)
	v_cvt_pk_bf16_f32 v10, v16, v14
	v_addc_co_u32_e32 v31, vcc, 0, v9, vcc
	s_waitcnt lgkmcnt(4)
	v_cvt_pk_bf16_f32 v11, v18, v20
	s_waitcnt lgkmcnt(2)
	v_cvt_pk_bf16_f32 v12, v22, v24
	s_waitcnt lgkmcnt(0)
	v_cvt_pk_bf16_f32 v13, v26, v28
	v_add_co_u32_e32 v14, vcc, 0x18000, v8
	global_store_dwordx4 v[30:31], v[10:13], off nt
	s_nop 1
	v_cvt_pk_bf16_f32 v10, v17, v15
	v_cvt_pk_bf16_f32 v11, v19, v21
	v_cvt_pk_bf16_f32 v12, v23, v25
	v_cvt_pk_bf16_f32 v13, v27, v29
	v_addc_co_u32_e32 v15, vcc, 0, v9, vcc
	global_store_dwordx4 v[14:15], v[10:13], off nt
	s_waitcnt lgkmcnt(0)
.LBB0_1501:
	s_and_b64 vcc, exec, s[36:37]
	s_mov_b32 s81, s82
	s_cbranch_vccnz .LBB0_1433
.LBB0_1502:
	s_add_i32 s82, s81, 0x200
	s_cmp_lt_i32 s82, s15
	s_cselect_b64 s[60:61], -1, 0
	s_cmp_ge_i32 s82, s15
	s_mov_b64 s[0:1], -1
	s_cbranch_scc0 .LBB0_1504
	s_waitcnt vmcnt(0)
	s_mov_b64 s[0:1], 0
.LBB0_1504:
	s_andn2_b64 vcc, exec, s[0:1]
	s_cbranch_vccnz .LBB0_1518
	s_mul_hi_u32 s0, s82, 0xaaaaaaab
	s_lshr_b32 s6, s0, 16
	s_mul_i32 s8, s6, 0xfffe8000
	s_add_i32 s8, s8, s82
	s_add_i32 s0, s8, 0x7fff
	s_cmpk_gt_u32 s0, 0xfffe
	s_mov_b64 s[0:1], -1
	s_cbranch_scc0 .LBB0_1511
	s_and_b32 s0, s8, 0xffff8000
	s_cmpk_lg_u32 s0, 0x8000
	s_mov_b64 s[0:1], -1
	s_cbranch_scc0 .LBB0_1508
	v_readlane_b32 s0, v253, 6
	s_nop 1
	v_mov_b32_e32 v2, s0
	ds_read_b64 v[8:9], v2
	s_mov_b64 s[0:1], 0
	s_waitcnt lgkmcnt(0)
	v_readfirstlane_b32 s2, v8
	v_readfirstlane_b32 s3, v9
.LBB0_1508:
	s_andn2_b64 vcc, exec, s[0:1]
	s_cbranch_vccnz .LBB0_1510
	v_readlane_b32 s0, v252, 36
	s_nop 1
	v_mov_b32_e32 v2, s0
	ds_read_b64 v[8:9], v2
	s_waitcnt lgkmcnt(0)
	v_readfirstlane_b32 s2, v8
	v_readfirstlane_b32 s3, v9

.LBB0_1511:
	s_andn2_b64 vcc, exec, s[0:1]
	s_cbranch_vccnz .LBB0_1513
	v_readlane_b32 s0, v253, 31
	s_nop 1
	v_mov_b32_e32 v2, s0
	ds_read_b64 v[8:9], v2
	s_waitcnt lgkmcnt(0)
	v_readfirstlane_b32 s2, v8
	v_readfirstlane_b32 s3, v9
.LBB0_1513:
	s_ashr_i32 s0, s8, 31
	s_lshr_b32 s0, s0, 17
	s_add_i32 s83, s8, s0
	s_and_b32 s0, s83, 0xffff8000
	s_sub_i32 s0, s8, s0
	s_ashr_i32 s0, s0, 11
	s_lshl_b32 s1, s6, 4
	s_add_i32 s6, s0, s1
	s_ashr_i32 s7, s6, 31
	s_cmp_lt_i32 s8, 0x10000
	s_cselect_b64 s[0:1], -1, 0
	s_cmp_gt_i32 s8, 0xffff
	s_mov_b64 s[8:9], -1
	s_cbranch_scc0 .LBB0_1515
	s_lshl_b64 s[8:9], s[6:7], 23
	s_add_u32 s36, s19, s8
	s_addc_u32 s37, s20, s9
	s_lshl_b64 s[62:63], s[6:7], 24
	s_mov_b64 s[8:9], 0
.LBB0_1515:
	s_andn2_b64 vcc, exec, s[8:9]
	s_ashr_i32 s8, s83, 15
	s_cbranch_vccnz .LBB0_1517
	s_lshl_b64 s[62:63], s[6:7], 24
	s_add_u32 s36, s21, s62
	s_addc_u32 s37, s22, s63
.LBB0_1517:
	s_lshl_b32 s6, s81, 5
	s_lshl_b32 s7, s81, 6
	s_and_b32 s6, s6, 0x7e0
	s_and_b32 s7, s7, 0xf00
	s_lshl_b32 s8, s8, 7
	s_add_i32 s8, s8, s7
	v_bitop3_b32 v5, s6, v209, v143 bitop3:0xc8
	v_or_b32_e32 v2, s6, v143
	v_or_b32_e32 v5, s8, v5
	s_and_b32 s7, s82, 0x7c0
	v_cndmask_b32_e64 v8, v2, v5, s[0:1]
	v_or_b32_e32 v2, s7, v143
	s_add_u32 s0, s2, s62
	v_lshlrev_b32_e32 v2, 13, v2
	s_addc_u32 s1, s3, s63
	v_lshl_add_u64 v[10:11], s[0:1], 0, v[2:3]
	s_lshl_b32 s92, s6, 2
	v_lshl_add_u64 v[10:11], v[10:11], 0, s[92:93]
	v_mov_b32_e32 v5, v3
	v_lshl_add_u64 v[10:11], v[10:11], 0, v[4:5]
	s_mov_b32 s0, m0
	s_mov_b32 m0, s94
	s_nop 0
	global_load_lds_dwordx4 v[10:11], off nt
	s_mov_b32 m0, s0
	s_mov_b64 s[0:1], 0x10000
	v_lshl_add_u64 v[12:13], v[10:11], 0, s[0:1]
	s_mov_b32 s0, m0
	s_mov_b32 m0, s26
	s_nop 0
	global_load_lds_dwordx4 v[12:13], off nt
	s_mov_b32 m0, s0
	v_lshl_add_u64 v[12:13], v[10:11], 0, s[84:85]
	s_mov_b32 s0, m0
	s_mov_b32 m0, s27
	s_nop 0
	global_load_lds_dwordx4 v[12:13], off nt
	s_mov_b32 m0, s0
	s_mov_b64 s[0:1], 0x30000
	v_lshl_add_u64 v[12:13], v[10:11], 0, s[0:1]
	s_mov_b32 s0, m0
	s_mov_b32 m0, s28
	s_nop 0
	global_load_lds_dwordx4 v[12:13], off nt
	s_mov_b32 m0, s0
	s_mov_b64 s[0:1], 0x40000
	v_lshl_add_u64 v[12:13], v[10:11], 0, s[0:1]
	s_mov_b32 s0, m0
	s_mov_b32 m0, s29
	s_nop 0
	global_load_lds_dwordx4 v[12:13], off nt
	s_mov_b32 m0, s0
	s_mov_b64 s[0:1], 0x50000
	v_lshl_add_u64 v[12:13], v[10:11], 0, s[0:1]
	s_mov_b32 s0, m0
	s_mov_b32 m0, s78
	s_nop 0
	global_load_lds_dwordx4 v[12:13], off nt
	s_mov_b32 m0, s0
	s_mov_b64 s[0:1], 0x60000
	v_lshl_add_u64 v[12:13], v[10:11], 0, s[0:1]
	s_mov_b32 s0, m0
	s_mov_b32 m0, s79
	s_nop 0
	global_load_lds_dwordx4 v[12:13], off nt
	s_mov_b32 m0, s0
	v_ashrrev_i32_e32 v9, 31, v8
	s_mov_b64 s[0:1], 0x70000
	v_lshlrev_b64 v[8:9], 12, v[8:9]
	v_lshl_add_u64 v[10:11], v[10:11], 0, s[0:1]
	s_mov_b32 s0, m0
	s_mov_b32 m0, s80
	s_nop 0
	global_load_lds_dwordx4 v[10:11], off nt
	s_mov_b32 m0, s0
	v_lshl_add_u64 v[8:9], s[36:37], 0, v[8:9]
	s_lshl_b32 s92, s7, 1
	s_waitcnt vmcnt(12)
	v_lshl_add_u64 v[8:9], v[8:9], 0, s[92:93]
	v_lshlrev_b32_e32 v2, 1, v144
	v_lshl_add_u64 v[8:9], v[8:9], 0, v[2:3]
.LBB0_1518:
	v_add_u32_e32 v2, 0x2000, v145
	v_add_u32_e32 v5, 0x2400, v145
	ds_read2_b32 v[14:15], v2 offset0:64 offset1:72
	ds_read2_b32 v[16:17], v2 offset0:32 offset1:40
	ds_read2_b32 v[18:19], v2 offset0:96 offset1:104
	ds_read2_b32 v[20:21], v2 offset0:128 offset1:136
	ds_read2_b32 v[22:23], v2 offset0:160 offset1:168
	ds_read2_b32 v[24:25], v2 offset0:192 offset1:200
	ds_read2_b32 v[26:27], v2 offset0:224 offset1:232
	ds_read2_b32 v[28:29], v5 offset1:8
	s_mov_b32 s0, 0x8000
	s_waitcnt lgkmcnt(6)
	v_cvt_pk_bf16_f32 v10, v16, v14
	s_waitcnt lgkmcnt(4)
	v_cvt_pk_bf16_f32 v11, v18, v20
	s_waitcnt lgkmcnt(2)
	v_cvt_pk_bf16_f32 v12, v22, v24
	s_waitcnt lgkmcnt(0)
	v_cvt_pk_bf16_f32 v13, v26, v28
	v_add_co_u32_e32 v14, vcc, s0, v6
	global_store_dwordx4 v[6:7], v[10:13], off nt
	s_mov_b32 s0, 0x10000
	s_mov_b64 s[36:37], -1
	v_cvt_pk_bf16_f32 v10, v17, v15
	v_cvt_pk_bf16_f32 v11, v19, v21
	v_cvt_pk_bf16_f32 v12, v23, v25
	v_cvt_pk_bf16_f32 v13, v27, v29
	v_addc_co_u32_e32 v15, vcc, 0, v7, vcc
	global_store_dwordx4 v[14:15], v[10:13], off nt
	ds_read2_b32 v[14:15], v2 offset0:80 offset1:88
	ds_read2_b32 v[16:17], v2 offset0:48 offset1:56
	ds_read2_b32 v[18:19], v2 offset0:112 offset1:120
	ds_read2_b32 v[20:21], v2 offset0:144 offset1:152
	ds_read2_b32 v[22:23], v2 offset0:176 offset1:184
	ds_read2_b32 v[24:25], v2 offset0:208 offset1:216
	ds_read2_b32 v[26:27], v2 offset0:240 offset1:248
	ds_read2_b32 v[28:29], v5 offset0:16 offset1:24
	v_add_co_u32_e32 v30, vcc, s0, v6
	s_waitcnt lgkmcnt(6)
	v_cvt_pk_bf16_f32 v10, v16, v14
	v_addc_co_u32_e32 v31, vcc, 0, v7, vcc
	s_waitcnt lgkmcnt(4)
	v_cvt_pk_bf16_f32 v11, v18, v20
	s_waitcnt lgkmcnt(2)
	v_cvt_pk_bf16_f32 v12, v22, v24
	s_waitcnt lgkmcnt(0)
	v_cvt_pk_bf16_f32 v13, v26, v28
	v_add_co_u32_e32 v14, vcc, 0x18000, v6
	global_store_dwordx4 v[30:31], v[10:13], off nt
	s_nop 1
	v_cvt_pk_bf16_f32 v10, v17, v15
	v_cvt_pk_bf16_f32 v11, v19, v21
	v_cvt_pk_bf16_f32 v12, v23, v25
	v_cvt_pk_bf16_f32 v13, v27, v29
	v_addc_co_u32_e32 v15, vcc, 0, v7, vcc
	global_store_dwordx4 v[14:15], v[10:13], off nt
	s_waitcnt lgkmcnt(0)
	s_andn2_b64 vcc, exec, s[60:61]
	s_cbranch_vccnz .LBB0_1501
	s_add_i32 s2, s81, 0x400
	s_cmp_ge_i32 s2, s15
	s_cselect_b64 s[36:37], -1, 0
	s_mov_b64 s[0:1], -1
	s_and_b64 vcc, exec, s[36:37]
	s_cbranch_vccz .LBB0_1521
	s_waitcnt vmcnt(0)
	s_mov_b64 s[0:1], 0
.LBB0_1521:
	s_andn2_b64 vcc, exec, s[0:1]
	s_cbranch_vccnz .LBB0_1500
	s_mul_hi_u32 s0, s2, 0xaaaaaaab
	s_lshr_b32 s6, s0, 16
	s_mul_i32 s8, s6, 0xfffe8000
	s_add_i32 s8, s8, s2
	s_add_i32 s0, s8, 0x7fff
	s_cmpk_gt_u32 s0, 0xfffe
	s_mov_b64 s[0:1], -1
	s_cbranch_scc0 .LBB0_1528
	s_and_b32 s0, s8, 0xffff8000
	s_cmpk_lg_u32 s0, 0x8000
	s_mov_b64 s[0:1], -1
	s_cbranch_scc0 .LBB0_1525
	v_readlane_b32 s0, v253, 6
	s_nop 1
	v_mov_b32_e32 v2, s0
	ds_read_b64 v[6:7], v2
	s_mov_b64 s[0:1], 0
	s_waitcnt lgkmcnt(0)
	v_readfirstlane_b32 s3, v6
	v_readfirstlane_b32 s82, v7
.LBB0_1525:
	s_andn2_b64 vcc, exec, s[0:1]
	s_cbranch_vccnz .LBB0_1527
	v_readlane_b32 s0, v252, 36
	s_nop 1
	v_mov_b32_e32 v2, s0
	ds_read_b64 v[6:7], v2
	s_waitcnt lgkmcnt(0)
	v_readfirstlane_b32 s3, v6
	v_readfirstlane_b32 s82, v7

.LBB0_1528:
	s_andn2_b64 vcc, exec, s[0:1]
	s_cbranch_vccnz .LBB0_1530
	v_readlane_b32 s0, v253, 31
	s_nop 1
	v_mov_b32_e32 v2, s0
	ds_read_b64 v[6:7], v2
	s_waitcnt lgkmcnt(0)
	v_readfirstlane_b32 s3, v6
	v_readfirstlane_b32 s82, v7
.LBB0_1530:
	s_ashr_i32 s0, s8, 31
	s_lshr_b32 s0, s0, 17
	s_add_i32 s83, s8, s0
	s_and_b32 s0, s83, 0xffff8000
	s_sub_i32 s0, s8, s0
	s_ashr_i32 s0, s0, 11
	s_lshl_b32 s1, s6, 4
	s_add_i32 s6, s0, s1
	s_ashr_i32 s7, s6, 31
	s_cmp_lt_i32 s8, 0x10000
	s_cselect_b64 s[0:1], -1, 0
	s_cmp_gt_i32 s8, 0xffff
	s_mov_b64 s[8:9], -1
	s_cbranch_scc0 .LBB0_1532
	s_lshl_b64 s[8:9], s[6:7], 23
	s_add_u32 s60, s19, s8
	s_addc_u32 s61, s20, s9
	s_lshl_b64 s[62:63], s[6:7], 24
	s_mov_b64 s[8:9], 0
.LBB0_1532:
	s_andn2_b64 vcc, exec, s[8:9]
	s_ashr_i32 s8, s83, 15
	s_cbranch_vccnz .LBB0_1499
	s_lshl_b64 s[62:63], s[6:7], 24
	s_add_u32 s60, s21, s62
	s_addc_u32 s61, s22, s63
	s_branch .LBB0_1499

.LBB0_1695:
	s_ashr_i32 s0, s2, 31
	s_lshr_b32 s0, s0, 17
	s_add_i32 s9, s2, s0
	s_and_b32 s0, s9, 0xffff8000
	s_sub_i32 s0, s2, s0
	s_ashr_i32 s0, s0, 11
	s_lshl_b32 s1, s7, 4
	s_add_i32 s0, s0, s1
	s_ashr_i32 s1, s0, 31
	s_lshl_b64 s[18:19], s[0:1], 23
	s_lshl_b64 s[20:21], s[0:1], 24
	s_add_i32 s26, s8, s80
	s_cmp_lt_i32 s26, s12
	s_cselect_b64 s[34:35], -1, 0
	s_cmp_ge_i32 s26, s12
	s_cselect_b64 s[38:39], -1, 0
	s_add_u32 s15, s36, 0x23840000
	s_addc_u32 s16, s37, 0
	s_add_u32 s7, s15, s18
	s_addc_u32 s19, s16, s19
	s_add_u32 s17, s36, 0x3840000
	s_addc_u32 s18, s37, 0
	s_add_u32 s24, s17, s20
	s_addc_u32 s25, s18, s21
	s_cmp_lt_i32 s2, 0x10000
	s_cselect_b64 s[0:1], -1, 0
	s_and_b64 s[22:23], s[0:1], exec
	v_lshrrev_b32_e32 v10, 3, v9
	v_readlane_b32 s2, v253, 10
	s_cselect_b32 s41, s25, s19
	s_cselect_b32 s40, s24, s7
	v_or_b32_e32 v2, s2, v10
	s_add_u32 s2, s3, s20
	v_lshlrev_b32_e32 v2, 13, v2
	s_addc_u32 s3, s6, s21
	v_lshl_add_u64 v[4:5], s[2:3], 0, v[2:3]
	v_readlane_b32 s2, v253, 8
	s_lshl_b32 s92, s2, 2
	v_and_b32_e32 v13, 7, v8
	v_lshl_add_u64 v[4:5], v[4:5], 0, s[92:93]
	v_lshlrev_b32_e32 v2, 4, v13
	v_lshl_add_u64 v[4:5], v[4:5], 0, v[2:3]
	s_mov_b32 s2, m0
	s_mov_b32 m0, s94
	s_nop 0
	global_load_lds_dwordx4 v[4:5], off
	s_mov_b32 m0, s2
	s_mov_b64 s[2:3], 0x10000
	v_lshl_add_u64 v[6:7], v[4:5], 0, s[2:3]
	s_add_i32 s19, s94, 0x410
	s_mov_b32 s2, m0
	s_mov_b32 m0, s19
	s_nop 0
	global_load_lds_dwordx4 v[6:7], off nt
	s_mov_b32 m0, s2
	v_lshl_add_u64 v[6:7], v[4:5], 0, s[84:85]
	s_add_i32 s20, s94, 0x820
	s_mov_b32 s2, m0
	s_mov_b32 m0, s20
	s_nop 0
	global_load_lds_dwordx4 v[6:7], off nt
	s_mov_b32 m0, s2
	s_mov_b64 s[2:3], 0x30000
	v_lshl_add_u64 v[6:7], v[4:5], 0, s[2:3]
	s_add_i32 s21, s94, 0xc30
	s_mov_b32 s2, m0
	s_mov_b32 m0, s21
	s_nop 0
	global_load_lds_dwordx4 v[6:7], off nt
	s_mov_b32 m0, s2
	s_mov_b64 s[2:3], 0x40000
	v_lshl_add_u64 v[6:7], v[4:5], 0, s[2:3]
	s_add_i32 s22, s94, 0x1040
	s_mov_b32 s2, m0
	s_mov_b32 m0, s22
	s_nop 0
	global_load_lds_dwordx4 v[6:7], off nt
	s_mov_b32 m0, s2
	s_mov_b64 s[2:3], 0x50000
	v_lshl_add_u64 v[6:7], v[4:5], 0, s[2:3]
	s_add_i32 s23, s94, 0x1450
	s_mov_b32 s2, m0
	s_mov_b32 m0, s23
	s_nop 0
	global_load_lds_dwordx4 v[6:7], off nt
	s_mov_b32 m0, s2
	s_mov_b64 s[2:3], 0x60000
	v_lshl_add_u64 v[6:7], v[4:5], 0, s[2:3]
	s_add_i32 s24, s94, 0x1860
	s_mov_b32 s2, m0
	s_mov_b32 m0, s24
	s_nop 0
	global_load_lds_dwordx4 v[6:7], off nt
	s_mov_b32 m0, s2
	s_mov_b64 s[2:3], 0x70000
	v_lshl_add_u64 v[4:5], v[4:5], 0, s[2:3]
	s_add_i32 s25, s94, 0x1c70
	s_mov_b32 s2, m0
	s_mov_b32 m0, s25
	s_nop 0
	global_load_lds_dwordx4 v[4:5], off nt
	s_mov_b32 m0, s2
	s_mov_b64 s[6:7], -1
	s_and_b64 vcc, exec, s[38:39]
	s_cbranch_vccz .LBB0_1697
	s_waitcnt vmcnt(0)
	s_mov_b64 s[6:7], 0

.LBB0_1706:
	s_ashr_i32 s0, s3, 31
	s_lshr_b32 s0, s0, 17
	s_add_i32 s0, s3, s0
	s_ashr_i32 s9, s0, 15
	s_and_b32 s0, s0, 0xffff8000
	s_sub_i32 s0, s3, s0
	s_ashr_i32 s0, s0, 11
	s_lshl_b32 s1, s7, 4
	s_add_i32 s0, s0, s1
	s_lshl_b32 s27, s26, 6
	s_ashr_i32 s1, s0, 31
	s_lshl_b32 s7, s26, 5
	s_and_b32 s27, s27, 0xf00
	s_lshl_b32 s9, s9, 7
	s_lshl_b64 s[28:29], s[0:1], 23
	s_lshl_b64 s[0:1], s[0:1], 24
	s_and_b32 s7, s7, 0x7e0
	s_add_i32 s9, s9, s27
	s_and_b32 s27, s26, 0x7c0
	s_add_u32 s40, s15, s28
	s_addc_u32 s41, s16, s29
	s_add_u32 s44, s17, s0
	s_addc_u32 s45, s18, s1
	s_cmp_lt_i32 s3, 0x10000
	v_mov_b32_e32 v6, s7
	s_movk_i32 s3, 0x67
	v_bitop3_b32 v6, v10, s3, v6 bitop3:0xc8
	s_cselect_b64 vcc, -1, 0
	v_or_b32_e32 v2, s7, v10
	v_or_b32_e32 v6, s9, v6
	s_and_b64 s[28:29], vcc, exec
	v_cndmask_b32_e32 v6, v2, v6, vcc
	s_cselect_b32 s29, s45, s41
	s_cselect_b32 s28, s44, s40
	v_or_b32_e32 v2, s27, v10
	s_add_u32 s0, s2, s0
	v_lshlrev_b32_e32 v2, 13, v2
	s_addc_u32 s1, s6, s1
	v_lshl_add_u64 v[14:15], s[0:1], 0, v[2:3]
	s_lshl_b32 s92, s7, 2
	v_lshl_add_u64 v[14:15], v[14:15], 0, s[92:93]
	v_lshlrev_b32_e32 v2, 2, v11
	v_lshl_add_u64 v[14:15], v[14:15], 0, v[2:3]
	s_add_i32 s0, s94, 0x2080
	s_mov_b32 s1, m0
	s_mov_b32 m0, s0
	s_nop 0
	global_load_lds_dwordx4 v[14:15], off nt
	s_mov_b32 m0, s1
	s_mov_b64 s[0:1], 0x10000
	v_lshl_add_u64 v[16:17], v[14:15], 0, s[0:1]
	s_add_i32 s0, s94, 0x2490
	s_mov_b32 s1, m0
	s_mov_b32 m0, s0
	s_nop 0
	global_load_lds_dwordx4 v[16:17], off nt
	s_mov_b32 m0, s1
	v_lshl_add_u64 v[16:17], v[14:15], 0, s[84:85]
	s_add_i32 s0, s94, 0x28a0
	s_mov_b32 s1, m0
	s_mov_b32 m0, s0
	s_nop 0
	global_load_lds_dwordx4 v[16:17], off nt
	s_mov_b32 m0, s1
	s_mov_b64 s[0:1], 0x30000
	v_lshl_add_u64 v[16:17], v[14:15], 0, s[0:1]
	s_add_i32 s0, s94, 0x2cb0
	s_mov_b32 s1, m0
	s_mov_b32 m0, s0
	s_nop 0
	global_load_lds_dwordx4 v[16:17], off nt
	s_mov_b32 m0, s1
	s_mov_b64 s[0:1], 0x40000
	v_lshl_add_u64 v[16:17], v[14:15], 0, s[0:1]
	s_add_i32 s0, s94, 0x30c0
	s_mov_b32 s1, m0
	s_mov_b32 m0, s0
	s_nop 0
	global_load_lds_dwordx4 v[16:17], off nt
	s_mov_b32 m0, s1
	s_mov_b64 s[0:1], 0x50000
	v_lshl_add_u64 v[16:17], v[14:15], 0, s[0:1]
	s_add_i32 s0, s94, 0x34d0
	s_mov_b32 s1, m0
	s_mov_b32 m0, s0
	s_nop 0
	global_load_lds_dwordx4 v[16:17], off nt
	s_mov_b32 m0, s1
	s_mov_b64 s[0:1], 0x60000
	v_lshl_add_u64 v[16:17], v[14:15], 0, s[0:1]
	s_add_i32 s0, s94, 0x38e0
	s_mov_b32 s1, m0
	s_mov_b32 m0, s0
	s_nop 0
	global_load_lds_dwordx4 v[16:17], off nt
	s_mov_b32 m0, s1
	v_ashrrev_i32_e32 v7, 31, v6
	s_mov_b64 s[0:1], 0x70000
	v_lshlrev_b64 v[6:7], 12, v[6:7]
	v_lshl_add_u64 v[14:15], v[14:15], 0, s[0:1]
	s_add_i32 s0, s94, 0x3cf0
	s_mov_b32 s1, m0
	s_mov_b32 m0, s0
	s_nop 0
	global_load_lds_dwordx4 v[14:15], off nt
	s_mov_b32 m0, s1
	v_lshl_add_u64 v[6:7], s[28:29], 0, v[6:7]
	s_lshl_b32 s92, s27, 1
	s_waitcnt vmcnt(8)
	v_lshl_add_u64 v[6:7], v[6:7], 0, s[92:93]
	v_lshlrev_b32_e32 v2, 1, v12
	v_lshl_add_u64 v[6:7], v[6:7], 0, v[2:3]
.LBB0_1707:
	v_mul_u32_u24_e32 v2, 0x410, v13
	v_lshlrev_b32_e32 v13, 2, v10
	v_add3_u32 v13, s94, v2, v13
	ds_read2_b32 v[18:19], v13 offset0:32 offset1:40
	ds_read2_b32 v[20:21], v13 offset1:8
	ds_read2_b32 v[22:23], v13 offset0:64 offset1:72
	ds_read2_b32 v[24:25], v13 offset0:96 offset1:104
	ds_read2_b32 v[26:27], v13 offset0:128 offset1:136
	ds_read2_b32 v[28:29], v13 offset0:160 offset1:168
	ds_read2_b32 v[30:31], v13 offset0:192 offset1:200
	ds_read2_b32 v[32:33], v13 offset0:224 offset1:232
	s_mov_b32 s0, 0x8000
	s_waitcnt lgkmcnt(0)
	v_cvt_pk_bf16_f32 v14, v20, v18
	v_cvt_pk_bf16_f32 v15, v22, v24
	v_cvt_pk_bf16_f32 v16, v26, v28
	v_cvt_pk_bf16_f32 v17, v30, v32
	v_add_co_u32_e32 v18, vcc, s0, v4
	global_store_dwordx4 v[4:5], v[14:17], off nt
	s_mov_b32 s0, 0x10000
	s_nop 0
	v_cvt_pk_bf16_f32 v14, v21, v19
	v_cvt_pk_bf16_f32 v15, v23, v25
	v_cvt_pk_bf16_f32 v16, v27, v29
	v_cvt_pk_bf16_f32 v17, v31, v33
	v_addc_co_u32_e32 v19, vcc, 0, v5, vcc
	global_store_dwordx4 v[18:19], v[14:17], off nt
	ds_read2_b32 v[18:19], v13 offset0:48 offset1:56
	ds_read2_b32 v[20:21], v13 offset0:16 offset1:24
	ds_read2_b32 v[22:23], v13 offset0:80 offset1:88
	ds_read2_b32 v[24:25], v13 offset0:112 offset1:120
	ds_read2_b32 v[26:27], v13 offset0:144 offset1:152
	ds_read2_b32 v[28:29], v13 offset0:176 offset1:184
	ds_read2_b32 v[30:31], v13 offset0:208 offset1:216
	ds_read2_b32 v[32:33], v13 offset0:240 offset1:248
	v_add_co_u32_e32 v34, vcc, s0, v4
	s_waitcnt lgkmcnt(0)
	v_cvt_pk_bf16_f32 v14, v20, v18
	v_addc_co_u32_e32 v35, vcc, 0, v5, vcc
	v_cvt_pk_bf16_f32 v15, v22, v24
	v_cvt_pk_bf16_f32 v16, v26, v28
	v_cvt_pk_bf16_f32 v17, v30, v32
	v_add_co_u32_e32 v18, vcc, 0x18000, v4
	global_store_dwordx4 v[34:35], v[14:17], off nt
	s_nop 1
	v_cvt_pk_bf16_f32 v14, v21, v19
	v_cvt_pk_bf16_f32 v15, v23, v25
	v_cvt_pk_bf16_f32 v16, v27, v29
	v_cvt_pk_bf16_f32 v17, v31, v33
	v_addc_co_u32_e32 v19, vcc, 0, v5, vcc
	global_store_dwordx4 v[18:19], v[14:17], off nt
	s_waitcnt lgkmcnt(0)
	s_andn2_b64 vcc, exec, s[38:39]
	s_cbranch_vccnz .LBB0_1709
	s_waitcnt vmcnt(0)
	s_mov_b32 s26, s8

.LBB0_1710:
	s_lshl_b32 s6, s2, 5
	s_lshl_b32 s7, s2, 6
	s_and_b32 s6, s6, 0x7e0
	s_and_b32 s7, s7, 0xf00
	s_lshl_b32 s8, s8, 7
	s_add_i32 s8, s8, s7
	v_bitop3_b32 v6, s6, v209, v10 bitop3:0xc8
	v_or_b32_e32 v2, s6, v10
	v_or_b32_e32 v6, s8, v6
	s_and_b32 s7, s2, 0x7c0
	v_cndmask_b32_e64 v6, v2, v6, s[0:1]
	v_or_b32_e32 v2, s7, v10
	s_add_u32 s0, s3, s40
	v_lshlrev_b32_e32 v2, 13, v2
	s_addc_u32 s1, s26, s41
	v_lshl_add_u64 v[14:15], s[0:1], 0, v[2:3]
	s_lshl_b32 s92, s6, 2
	v_lshl_add_u64 v[14:15], v[14:15], 0, s[92:93]
	v_lshlrev_b32_e32 v2, 2, v11
	v_lshl_add_u64 v[14:15], v[14:15], 0, v[2:3]
	s_add_i32 s0, s94, 0x2080
	s_mov_b32 s1, m0
	s_mov_b32 m0, s0
	s_nop 0
	global_load_lds_dwordx4 v[14:15], off nt
	s_mov_b32 m0, s1
	s_mov_b64 s[0:1], 0x10000
	v_lshl_add_u64 v[16:17], v[14:15], 0, s[0:1]
	s_add_i32 s0, s94, 0x2490
	s_mov_b32 s1, m0
	s_mov_b32 m0, s0
	s_nop 0
	global_load_lds_dwordx4 v[16:17], off nt
	s_mov_b32 m0, s1
	v_lshl_add_u64 v[16:17], v[14:15], 0, s[84:85]
	s_add_i32 s0, s94, 0x28a0
	s_mov_b32 s1, m0
	s_mov_b32 m0, s0
	s_nop 0
	global_load_lds_dwordx4 v[16:17], off nt
	s_mov_b32 m0, s1
	s_mov_b64 s[0:1], 0x30000
	v_lshl_add_u64 v[16:17], v[14:15], 0, s[0:1]
	s_add_i32 s0, s94, 0x2cb0
	s_mov_b32 s1, m0
	s_mov_b32 m0, s0
	s_nop 0
	global_load_lds_dwordx4 v[16:17], off nt
	s_mov_b32 m0, s1
	s_mov_b64 s[0:1], 0x40000
	v_lshl_add_u64 v[16:17], v[14:15], 0, s[0:1]
	s_add_i32 s0, s94, 0x30c0
	s_mov_b32 s1, m0
	s_mov_b32 m0, s0
	s_nop 0
	global_load_lds_dwordx4 v[16:17], off nt
	s_mov_b32 m0, s1
	s_mov_b64 s[0:1], 0x50000
	v_lshl_add_u64 v[16:17], v[14:15], 0, s[0:1]
	s_add_i32 s0, s94, 0x34d0
	s_mov_b32 s1, m0
	s_mov_b32 m0, s0
	s_nop 0
	global_load_lds_dwordx4 v[16:17], off nt
	s_mov_b32 m0, s1
	s_mov_b64 s[0:1], 0x60000
	v_lshl_add_u64 v[16:17], v[14:15], 0, s[0:1]
	s_add_i32 s0, s94, 0x38e0
	s_mov_b32 s1, m0
	s_mov_b32 m0, s0
	s_nop 0
	global_load_lds_dwordx4 v[16:17], off nt
	s_mov_b32 m0, s1
	v_ashrrev_i32_e32 v7, 31, v6
	s_mov_b64 s[0:1], 0x70000
	v_lshlrev_b64 v[6:7], 12, v[6:7]
	v_lshl_add_u64 v[14:15], v[14:15], 0, s[0:1]
	s_add_i32 s0, s94, 0x3cf0
	s_mov_b32 s1, m0
	s_mov_b32 m0, s0
	s_nop 0
	global_load_lds_dwordx4 v[14:15], off nt
	s_mov_b32 m0, s1
	v_lshl_add_u64 v[6:7], s[38:39], 0, v[6:7]
	s_lshl_b32 s92, s7, 1
	s_waitcnt vmcnt(12)
	v_lshl_add_u64 v[6:7], v[6:7], 0, s[92:93]
	v_lshlrev_b32_e32 v2, 1, v12
	v_lshl_add_u64 v[6:7], v[6:7], 0, v[2:3]
	s_mov_b32 s26, s2
.LBB0_1711:
	ds_read2_b32 v[18:19], v13 offset0:32 offset1:40
	ds_read2_b32 v[20:21], v13 offset1:8
	ds_read2_b32 v[22:23], v13 offset0:64 offset1:72
	ds_read2_b32 v[24:25], v13 offset0:96 offset1:104
	ds_read2_b32 v[26:27], v13 offset0:128 offset1:136
	ds_read2_b32 v[28:29], v13 offset0:160 offset1:168
	ds_read2_b32 v[30:31], v13 offset0:192 offset1:200
	ds_read2_b32 v[32:33], v13 offset0:224 offset1:232
	s_mov_b32 s0, 0x8000
	s_waitcnt lgkmcnt(0)
	v_cvt_pk_bf16_f32 v14, v20, v18
	v_cvt_pk_bf16_f32 v15, v22, v24
	v_cvt_pk_bf16_f32 v16, v26, v28
	v_cvt_pk_bf16_f32 v17, v30, v32
	v_add_co_u32_e32 v18, vcc, s0, v4
	global_store_dwordx4 v[4:5], v[14:17], off nt
	s_mov_b32 s0, 0x10000
	s_nop 0
	v_cvt_pk_bf16_f32 v14, v21, v19
	v_cvt_pk_bf16_f32 v15, v23, v25
	v_cvt_pk_bf16_f32 v16, v27, v29
	v_cvt_pk_bf16_f32 v17, v31, v33
	v_addc_co_u32_e32 v19, vcc, 0, v5, vcc
	global_store_dwordx4 v[18:19], v[14:17], off nt
	ds_read2_b32 v[18:19], v13 offset0:48 offset1:56
	ds_read2_b32 v[20:21], v13 offset0:16 offset1:24
	ds_read2_b32 v[22:23], v13 offset0:80 offset1:88
	ds_read2_b32 v[24:25], v13 offset0:112 offset1:120
	ds_read2_b32 v[26:27], v13 offset0:144 offset1:152
	ds_read2_b32 v[28:29], v13 offset0:176 offset1:184
	ds_read2_b32 v[30:31], v13 offset0:208 offset1:216
	ds_read2_b32 v[32:33], v13 offset0:240 offset1:248
	v_add_co_u32_e32 v34, vcc, s0, v4
	s_waitcnt lgkmcnt(0)
	v_cvt_pk_bf16_f32 v14, v20, v18
	v_addc_co_u32_e32 v35, vcc, 0, v5, vcc
	v_cvt_pk_bf16_f32 v15, v22, v24
	v_cvt_pk_bf16_f32 v16, v26, v28
	v_cvt_pk_bf16_f32 v17, v30, v32
	v_add_co_u32_e32 v18, vcc, 0x18000, v4
	global_store_dwordx4 v[34:35], v[14:17], off nt
	s_nop 1
	v_cvt_pk_bf16_f32 v14, v21, v19
	v_cvt_pk_bf16_f32 v15, v23, v25
	v_cvt_pk_bf16_f32 v16, v27, v29
	v_cvt_pk_bf16_f32 v17, v31, v33
	v_addc_co_u32_e32 v19, vcc, 0, v5, vcc
	global_store_dwordx4 v[18:19], v[14:17], off nt
	s_waitcnt lgkmcnt(0)

.LBB0_1728:
	s_lshl_b32 s6, s26, 5
	s_lshl_b32 s7, s26, 6
	s_and_b32 s6, s6, 0x7e0
	s_and_b32 s7, s7, 0xf00
	s_lshl_b32 s8, s8, 7
	s_add_i32 s8, s8, s7
	v_bitop3_b32 v4, s6, v209, v10 bitop3:0xc8
	v_or_b32_e32 v2, s6, v10
	v_or_b32_e32 v4, s8, v4
	s_and_b32 s7, s26, 0x7c0
	v_cndmask_b32_e64 v4, v2, v4, s[0:1]
	v_or_b32_e32 v2, s7, v10
	s_add_u32 s0, s2, s40
	v_lshlrev_b32_e32 v2, 13, v2
	s_addc_u32 s1, s3, s41
	v_lshl_add_u64 v[14:15], s[0:1], 0, v[2:3]
	s_lshl_b32 s92, s6, 2
	v_lshl_add_u64 v[14:15], v[14:15], 0, s[92:93]
	v_lshlrev_b32_e32 v2, 2, v11
	v_lshl_add_u64 v[14:15], v[14:15], 0, v[2:3]
	s_mov_b32 s0, m0
	s_mov_b32 m0, s94
	s_nop 0
	global_load_lds_dwordx4 v[14:15], off nt
	s_mov_b32 m0, s0
	s_mov_b64 s[0:1], 0x10000
	v_lshl_add_u64 v[16:17], v[14:15], 0, s[0:1]
	s_mov_b32 s0, m0
	s_mov_b32 m0, s19
	s_nop 0
	global_load_lds_dwordx4 v[16:17], off nt
	s_mov_b32 m0, s0
	v_lshl_add_u64 v[16:17], v[14:15], 0, s[84:85]
	s_mov_b32 s0, m0
	s_mov_b32 m0, s20
	s_nop 0
	global_load_lds_dwordx4 v[16:17], off nt
	s_mov_b32 m0, s0
	s_mov_b64 s[0:1], 0x30000
	v_lshl_add_u64 v[16:17], v[14:15], 0, s[0:1]
	s_mov_b32 s0, m0
	s_mov_b32 m0, s21
	s_nop 0
	global_load_lds_dwordx4 v[16:17], off nt
	s_mov_b32 m0, s0
	s_mov_b64 s[0:1], 0x40000
	v_lshl_add_u64 v[16:17], v[14:15], 0, s[0:1]
	s_mov_b32 s0, m0
	s_mov_b32 m0, s22
	s_nop 0
	global_load_lds_dwordx4 v[16:17], off nt
	s_mov_b32 m0, s0
	s_mov_b64 s[0:1], 0x50000
	v_lshl_add_u64 v[16:17], v[14:15], 0, s[0:1]
	s_mov_b32 s0, m0
	s_mov_b32 m0, s23
	s_nop 0
	global_load_lds_dwordx4 v[16:17], off nt
	s_mov_b32 m0, s0
	s_mov_b64 s[0:1], 0x60000
	v_lshl_add_u64 v[16:17], v[14:15], 0, s[0:1]
	s_mov_b32 s0, m0
	s_mov_b32 m0, s24
	s_nop 0
	global_load_lds_dwordx4 v[16:17], off nt
	s_mov_b32 m0, s0
	v_ashrrev_i32_e32 v5, 31, v4
	s_mov_b64 s[0:1], 0x70000
	v_lshlrev_b64 v[4:5], 12, v[4:5]
	v_lshl_add_u64 v[14:15], v[14:15], 0, s[0:1]
	s_mov_b32 s0, m0
	s_mov_b32 m0, s25
	s_nop 0
	global_load_lds_dwordx4 v[14:15], off nt
	s_mov_b32 m0, s0
	v_lshl_add_u64 v[4:5], s[34:35], 0, v[4:5]
	s_lshl_b32 s92, s7, 1
	s_waitcnt vmcnt(12)
	v_lshl_add_u64 v[4:5], v[4:5], 0, s[92:93]
	v_lshlrev_b32_e32 v2, 1, v12
	v_lshl_add_u64 v[4:5], v[4:5], 0, v[2:3]
.LBB0_1729:
	v_add_u32_e32 v2, 0x2000, v13
	v_add_u32_e32 v34, 0x2400, v13
	ds_read2_b32 v[18:19], v2 offset0:64 offset1:72
	ds_read2_b32 v[20:21], v2 offset0:32 offset1:40
	ds_read2_b32 v[22:23], v2 offset0:96 offset1:104
	ds_read2_b32 v[24:25], v2 offset0:128 offset1:136
	ds_read2_b32 v[26:27], v2 offset0:160 offset1:168
	ds_read2_b32 v[28:29], v2 offset0:192 offset1:200
	ds_read2_b32 v[30:31], v2 offset0:224 offset1:232
	ds_read2_b32 v[32:33], v34 offset1:8
	s_mov_b32 s0, 0x8000
	s_waitcnt lgkmcnt(0)
	v_cvt_pk_bf16_f32 v14, v20, v18
	v_cvt_pk_bf16_f32 v15, v22, v24
	v_cvt_pk_bf16_f32 v16, v26, v28
	v_cvt_pk_bf16_f32 v17, v30, v32
	v_add_co_u32_e32 v18, vcc, s0, v6
	global_store_dwordx4 v[6:7], v[14:17], off nt
	s_mov_b32 s0, 0x10000
	s_mov_b64 s[34:35], -1
	v_cvt_pk_bf16_f32 v14, v21, v19
	v_cvt_pk_bf16_f32 v15, v23, v25
	v_cvt_pk_bf16_f32 v16, v27, v29
	v_cvt_pk_bf16_f32 v17, v31, v33
	v_addc_co_u32_e32 v19, vcc, 0, v7, vcc
	global_store_dwordx4 v[18:19], v[14:17], off nt
	ds_read2_b32 v[18:19], v2 offset0:80 offset1:88
	ds_read2_b32 v[20:21], v2 offset0:48 offset1:56
	ds_read2_b32 v[22:23], v2 offset0:112 offset1:120
	ds_read2_b32 v[24:25], v2 offset0:144 offset1:152
	ds_read2_b32 v[26:27], v2 offset0:176 offset1:184
	ds_read2_b32 v[28:29], v2 offset0:208 offset1:216
	ds_read2_b32 v[30:31], v2 offset0:240 offset1:248
	ds_read2_b32 v[32:33], v34 offset0:16 offset1:24
	v_add_co_u32_e32 v34, vcc, s0, v6
	s_waitcnt lgkmcnt(0)
	v_cvt_pk_bf16_f32 v14, v20, v18
	v_addc_co_u32_e32 v35, vcc, 0, v7, vcc
	v_cvt_pk_bf16_f32 v15, v22, v24
	v_cvt_pk_bf16_f32 v16, v26, v28
	v_cvt_pk_bf16_f32 v17, v30, v32
	v_add_co_u32_e32 v18, vcc, 0x18000, v6
	global_store_dwordx4 v[34:35], v[14:17], off nt
	s_nop 1
	v_cvt_pk_bf16_f32 v14, v21, v19
	v_cvt_pk_bf16_f32 v15, v23, v25
	v_cvt_pk_bf16_f32 v16, v27, v29
	v_cvt_pk_bf16_f32 v17, v31, v33
	v_addc_co_u32_e32 v19, vcc, 0, v7, vcc
	global_store_dwordx4 v[18:19], v[14:17], off nt
	s_waitcnt lgkmcnt(0)
	s_andn2_b64 vcc, exec, s[38:39]
	s_cbranch_vccnz .LBB0_1712
	s_add_i32 s2, s26, s80
	s_cmp_ge_i32 s2, s12
	s_cselect_b64 s[34:35], -1, 0
	s_mov_b64 s[0:1], -1
	s_and_b64 vcc, exec, s[34:35]
	s_cbranch_vccz .LBB0_1732
	s_waitcnt vmcnt(0)
	s_mov_b64 s[0:1], 0

.LBB0_1747:
	s_andn2_b64 vcc, exec, s[0:1]
	v_readlane_b32 s34, v253, 18
	s_mov_b32 s0, s80
	v_readlane_b32 s35, v253, 19
	s_cbranch_vccnz .LBB0_1891
	v_readlane_b32 s0, v252, 4
	v_readlane_b32 s1, v252, 5
	s_and_b64 s[0:1], s[0:1], exec
	v_readlane_b32 s0, v252, 7
	s_cselect_b32 s34, s0, s86
	s_mov_b64 s[0:1], -1
	s_and_b64 vcc, exec, s[42:43]
	s_cbranch_vccz .LBB0_1820
	s_cmp_lt_i32 s69, 24
	s_cbranch_scc1 .LBB0_1819
	s_and_b32 s0, s65, -8
	v_readlane_b32 s1, v252, 3
	s_add_i32 s2, s1, s0
	s_add_i32 s0, s2, s68
	s_add_i32 s23, s67, s0
	s_cmp_ge_i32 s23, s12
	s_cbranch_scc1 .LBB0_1819
	s_mul_hi_i32 s0, s23, 0x2aaaaaab
	s_lshr_b32 s1, s0, 31
	s_ashr_i32 s7, s0, 14
	s_add_i32 s7, s7, s1
	s_mul_i32 s6, s7, 0xfffe8000
	s_add_i32 s6, s6, s23
	s_add_i32 s0, s6, 0x7fff
	s_cmpk_gt_u32 s0, 0xfffe
	s_mov_b64 s[0:1], -1
	s_cbranch_scc0 .LBB0_1757
	s_and_b32 s0, s6, 0xffff8000
	s_cmpk_lg_u32 s0, 0x8000
	s_mov_b64 s[0:1], -1
	s_cbranch_scc0 .LBB0_1754
	v_readlane_b32 s0, v253, 6
	s_nop 1
	v_mov_b32_e32 v2, s0
	ds_read_b64 v[4:5], v2
	s_mov_b64 s[0:1], 0
	s_waitcnt lgkmcnt(0)
	v_readfirstlane_b32 s3, v4
	v_readfirstlane_b32 s15, v5
.LBB0_1754:
	s_andn2_b64 vcc, exec, s[0:1]
	s_cbranch_vccnz .LBB0_1756
	v_readlane_b32 s0, v252, 36
	s_nop 1
	v_mov_b32_e32 v2, s0
	ds_read_b64 v[4:5], v2
	s_waitcnt lgkmcnt(0)
	v_readfirstlane_b32 s3, v4
	v_readfirstlane_b32 s15, v5

.LBB0_1757:
	s_andn2_b64 vcc, exec, s[0:1]
	s_cbranch_vccnz .LBB0_1759
	v_readlane_b32 s0, v253, 31
	s_nop 1
	v_mov_b32_e32 v2, s0
	ds_read_b64 v[4:5], v2
	s_waitcnt lgkmcnt(0)
	v_readfirstlane_b32 s3, v4
	v_readfirstlane_b32 s15, v5
.LBB0_1759:
	s_ashr_i32 s0, s6, 31
	s_lshr_b32 s0, s0, 17
	s_add_i32 s24, s6, s0
	s_and_b32 s0, s24, 0xffff8000
	s_sub_i32 s0, s6, s0
	s_ashr_i32 s0, s0, 11
	s_lshl_b32 s1, s7, 4
	s_add_i32 s38, s0, s1
	s_ashr_i32 s39, s38, 31
	s_cmp_lt_i32 s6, 0x10000
	s_cselect_b64 s[0:1], -1, 0
	s_cmp_gt_i32 s6, 0xffff
	s_mov_b64 s[8:9], -1
	s_cbranch_scc0 .LBB0_1761
	s_lshl_b64 s[6:7], s[38:39], 23
	s_add_u32 s6, s36, s6
	s_addc_u32 s7, s37, s7
	s_add_u32 s42, s6, 0x23840000
	s_addc_u32 s43, s7, 0
	s_lshl_b64 s[6:7], s[38:39], 24
	s_mov_b64 s[8:9], 0
.LBB0_1761:
	s_andn2_b64 vcc, exec, s[8:9]
	s_cbranch_vccnz .LBB0_1763
	s_lshl_b64 s[6:7], s[38:39], 24
	s_add_u32 s8, s36, s6
	s_addc_u32 s9, s37, s7
	s_add_u32 s42, s8, 0x3840000
	s_addc_u32 s43, s9, 0
.LBB0_1763:
	s_lshl_b32 s8, s2, 5
	s_and_b32 s9, s8, 0x7e0
	v_lshrrev_b32_e32 v10, 3, v9
	s_and_b32 s8, s23, 0x7c0
	v_or_b32_e32 v2, s8, v10
	s_add_u32 s6, s3, s6
	v_lshlrev_b32_e32 v2, 13, v2
	s_addc_u32 s7, s15, s7
	v_lshl_add_u64 v[4:5], s[6:7], 0, v[2:3]
	s_lshl_b32 s92, s9, 2
	v_and_b32_e32 v13, 7, v8
	v_lshl_add_u64 v[4:5], v[4:5], 0, s[92:93]
	v_lshlrev_b32_e32 v2, 4, v13
	v_lshl_add_u64 v[4:5], v[4:5], 0, v[2:3]
	s_mov_b32 s3, m0
	s_mov_b32 m0, s94
	s_nop 0
	global_load_lds_dwordx4 v[4:5], off nt
	s_mov_b32 m0, s3
	s_mov_b64 s[6:7], 0x10000
	v_lshl_add_u64 v[6:7], v[4:5], 0, s[6:7]
	s_add_i32 s15, s94, 0x410
	s_mov_b32 s3, m0
	s_mov_b32 m0, s15
	s_nop 0
	global_load_lds_dwordx4 v[6:7], off nt
	s_mov_b32 m0, s3
	v_lshl_add_u64 v[6:7], v[4:5], 0, s[84:85]
	s_add_i32 s16, s94, 0x820
	s_mov_b32 s3, m0
	s_mov_b32 m0, s16
	s_nop 0
	global_load_lds_dwordx4 v[6:7], off nt
	s_mov_b32 m0, s3
	s_mov_b64 s[6:7], 0x30000
	v_lshl_add_u64 v[6:7], v[4:5], 0, s[6:7]
	s_add_i32 s17, s94, 0xc30
	s_mov_b32 s3, m0
	s_mov_b32 m0, s17
	s_nop 0
	global_load_lds_dwordx4 v[6:7], off nt
	s_mov_b32 m0, s3
	s_mov_b64 s[6:7], 0x40000
	v_lshl_add_u64 v[6:7], v[4:5], 0, s[6:7]
	s_add_i32 s18, s94, 0x1040
	s_mov_b32 s3, m0
	s_mov_b32 m0, s18
	s_nop 0
	global_load_lds_dwordx4 v[6:7], off nt
	s_mov_b32 m0, s3
	s_mov_b64 s[6:7], 0x50000
	v_lshl_add_u64 v[6:7], v[4:5], 0, s[6:7]
	s_add_i32 s19, s94, 0x1450
	s_mov_b32 s3, m0
	s_mov_b32 m0, s19
	s_nop 0
	global_load_lds_dwordx4 v[6:7], off nt
	s_mov_b32 m0, s3
	s_mov_b64 s[6:7], 0x60000
	s_add_i32 s20, s94, 0x1860
	s_add_i32 s21, s94, 0x1c70
	s_add_i32 s22, s23, 0x200
	v_lshl_add_u64 v[6:7], v[4:5], 0, s[6:7]
	s_mov_b32 s3, m0
	s_mov_b32 m0, s20
	s_nop 0
	global_load_lds_dwordx4 v[6:7], off nt
	s_mov_b32 m0, s3
	s_mov_b64 s[6:7], 0x70000
	s_cmp_lt_i32 s22, s12
	v_lshl_add_u64 v[4:5], v[4:5], 0, s[6:7]
	s_mov_b32 s3, m0
	s_mov_b32 m0, s21
	s_nop 0
	global_load_lds_dwordx4 v[4:5], off nt
	s_mov_b32 m0, s3
	s_cselect_b64 s[38:39], -1, 0
	s_cmp_ge_i32 s22, s12
	s_cselect_b64 s[40:41], -1, 0
	s_mov_b64 s[6:7], -1
	s_and_b64 vcc, exec, s[40:41]
	s_cbranch_vccz .LBB0_1765
	s_waitcnt vmcnt(0)
	s_mov_b64 s[6:7], 0
.LBB0_1765:
	s_ashr_i32 s3, s24, 15
	s_lshl_b32 s2, s2, 6
	v_or_b32_e32 v14, s9, v10
	s_and_b32 s2, s2, 0xf00
	s_lshl_b32 s3, s3, 7
	v_mov_b32_e32 v4, s9
	s_movk_i32 s9, 0x67
	s_add_i32 s3, s3, s2
	v_bitop3_b32 v15, v10, s9, v4 bitop3:0xc8
	v_or_b32_e32 v4, s3, v15
	v_cndmask_b32_e64 v4, v14, v4, s[0:1]
	v_ashrrev_i32_e32 v5, 31, v4
	v_lshlrev_b64 v[4:5], 12, v[4:5]
	v_lshl_add_u64 v[4:5], s[42:43], 0, v[4:5]
	s_lshl_b32 s0, s8, 1
	s_mov_b32 s1, s93
	v_lshl_add_u64 v[4:5], v[4:5], 0, s[0:1]
	v_lshl_add_u64 v[4:5], v[4:5], 0, v[2:3]
	v_lshlrev_b32_e32 v11, 2, v13
	v_lshlrev_b32_e32 v12, 3, v13
	s_andn2_b64 vcc, exec, s[6:7]
	v_mov_b64_e32 v[6:7], v[4:5]
	s_cbranch_vccnz .LBB0_1779
	s_mul_hi_i32 s0, s22, 0x2aaaaaab
	s_lshr_b32 s1, s0, 31
	s_ashr_i32 s7, s0, 14
	s_add_i32 s7, s7, s1
	s_mul_i32 s6, s7, 0xfffe8000
	s_add_i32 s6, s6, s22
	s_add_i32 s0, s6, 0x7fff
	s_cmpk_gt_u32 s0, 0xfffe
	s_mov_b64 s[0:1], -1
	s_cbranch_scc0 .LBB0_1772
	s_and_b32 s0, s6, 0xffff8000
	s_cmpk_lg_u32 s0, 0x8000
	s_mov_b64 s[0:1], -1
	s_cbranch_scc0 .LBB0_1769
	v_readlane_b32 s0, v253, 6
	s_nop 1
	v_mov_b32_e32 v2, s0
	ds_read_b64 v[6:7], v2
	s_mov_b64 s[0:1], 0
	s_waitcnt lgkmcnt(0)
	v_readfirstlane_b32 s3, v6
	v_readfirstlane_b32 s24, v7
.LBB0_1769:
	s_andn2_b64 vcc, exec, s[0:1]
	s_cbranch_vccnz .LBB0_1771
	v_readlane_b32 s0, v252, 36
	s_nop 1
	v_mov_b32_e32 v2, s0
	ds_read_b64 v[6:7], v2
	s_waitcnt lgkmcnt(0)
	v_readfirstlane_b32 s3, v6
	v_readfirstlane_b32 s24, v7

.LBB0_1772:
	s_andn2_b64 vcc, exec, s[0:1]
	s_cbranch_vccnz .LBB0_1774
	v_readlane_b32 s0, v253, 31
	s_nop 1
	v_mov_b32_e32 v2, s0
	ds_read_b64 v[6:7], v2
	s_waitcnt lgkmcnt(0)
	v_readfirstlane_b32 s3, v6
	v_readfirstlane_b32 s24, v7
.LBB0_1774:
	s_ashr_i32 s0, s6, 31
	s_lshr_b32 s0, s0, 17
	s_add_i32 s25, s6, s0
	s_and_b32 s0, s25, 0xffff8000
	s_sub_i32 s0, s6, s0
	s_ashr_i32 s0, s0, 11
	s_lshl_b32 s1, s7, 4
	s_add_i32 s44, s0, s1
	s_ashr_i32 s45, s44, 31
	s_cmp_lt_i32 s6, 0x10000
	s_cselect_b64 s[0:1], -1, 0
	s_cmp_gt_i32 s6, 0xffff
	s_mov_b64 s[8:9], -1
	s_cbranch_scc0 .LBB0_1776
	s_lshl_b64 s[6:7], s[44:45], 23
	s_add_u32 s6, s36, s6
	s_addc_u32 s7, s37, s7
	s_add_u32 s42, s6, 0x23840000
	s_addc_u32 s43, s7, 0
	s_lshl_b64 s[6:7], s[44:45], 24
	s_mov_b64 s[8:9], 0
.LBB0_1776:
	s_andn2_b64 vcc, exec, s[8:9]
	s_ashr_i32 s8, s25, 15
	s_cbranch_vccnz .LBB0_1778
	s_lshl_b64 s[6:7], s[44:45], 24
	s_add_u32 s9, s36, s6
	s_addc_u32 s25, s37, s7
	s_add_u32 s42, s9, 0x3840000
	s_addc_u32 s43, s25, 0
.LBB0_1778:
	s_lshl_b32 s8, s8, 7
	s_add_i32 s8, s8, s2
	v_or_b32_e32 v2, s8, v15
	s_and_b32 s2, s22, 0x7c0
	v_cndmask_b32_e64 v6, v14, v2, s[0:1]
	v_or_b32_e32 v2, s2, v10
	s_add_u32 s0, s3, s6
	v_lshlrev_b32_e32 v2, 13, v2
	s_addc_u32 s1, s24, s7
	v_lshl_add_u64 v[14:15], s[0:1], 0, v[2:3]
	v_lshl_add_u64 v[14:15], v[14:15], 0, s[92:93]
	v_lshlrev_b32_e32 v2, 2, v11
	v_lshl_add_u64 v[14:15], v[14:15], 0, v[2:3]
	s_add_i32 s0, s94, 0x2080
	s_mov_b32 s1, m0
	s_mov_b32 m0, s0
	s_nop 0
	global_load_lds_dwordx4 v[14:15], off nt
	s_mov_b32 m0, s1
	s_mov_b64 s[0:1], 0x10000
	v_lshl_add_u64 v[16:17], v[14:15], 0, s[0:1]
	s_add_i32 s0, s94, 0x2490
	s_mov_b32 s1, m0
	s_mov_b32 m0, s0
	s_nop 0
	global_load_lds_dwordx4 v[16:17], off nt
	s_mov_b32 m0, s1
	v_lshl_add_u64 v[16:17], v[14:15], 0, s[84:85]
	s_add_i32 s0, s94, 0x28a0
	s_mov_b32 s1, m0
	s_mov_b32 m0, s0
	s_nop 0
	global_load_lds_dwordx4 v[16:17], off nt
	s_mov_b32 m0, s1
	s_mov_b64 s[0:1], 0x30000
	v_lshl_add_u64 v[16:17], v[14:15], 0, s[0:1]
	s_add_i32 s0, s94, 0x2cb0
	s_mov_b32 s1, m0
	s_mov_b32 m0, s0
	s_nop 0
	global_load_lds_dwordx4 v[16:17], off nt
	s_mov_b32 m0, s1
	s_mov_b64 s[0:1], 0x40000
	v_lshl_add_u64 v[16:17], v[14:15], 0, s[0:1]
	s_add_i32 s0, s94, 0x30c0
	s_mov_b32 s1, m0
	s_mov_b32 m0, s0
	s_nop 0
	global_load_lds_dwordx4 v[16:17], off nt
	s_mov_b32 m0, s1
	s_mov_b64 s[0:1], 0x50000
	v_lshl_add_u64 v[16:17], v[14:15], 0, s[0:1]
	s_add_i32 s0, s94, 0x34d0
	s_mov_b32 s1, m0
	s_mov_b32 m0, s0
	s_nop 0
	global_load_lds_dwordx4 v[16:17], off nt
	s_mov_b32 m0, s1
	s_mov_b64 s[0:1], 0x60000
	v_lshl_add_u64 v[16:17], v[14:15], 0, s[0:1]
	s_add_i32 s0, s94, 0x38e0
	s_mov_b32 s1, m0
	s_mov_b32 m0, s0
	s_nop 0
	global_load_lds_dwordx4 v[16:17], off nt
	s_mov_b32 m0, s1
	v_ashrrev_i32_e32 v7, 31, v6
	s_mov_b64 s[0:1], 0x70000
	v_lshlrev_b64 v[6:7], 12, v[6:7]
	v_lshl_add_u64 v[14:15], v[14:15], 0, s[0:1]
	s_add_i32 s0, s94, 0x3cf0
	s_mov_b32 s1, m0
	s_mov_b32 m0, s0
	s_nop 0
	global_load_lds_dwordx4 v[14:15], off nt
	s_mov_b32 m0, s1
	v_lshl_add_u64 v[6:7], s[42:43], 0, v[6:7]
	s_lshl_b32 s92, s2, 1
	s_waitcnt vmcnt(8)
	v_lshl_add_u64 v[6:7], v[6:7], 0, s[92:93]
	v_lshlrev_b32_e32 v2, 1, v12
	v_lshl_add_u64 v[6:7], v[6:7], 0, v[2:3]
.LBB0_1779:
	v_mul_u32_u24_e32 v2, 0x410, v13
	v_lshlrev_b32_e32 v13, 2, v10
	v_add3_u32 v13, s94, v2, v13
	ds_read2_b32 v[18:19], v13 offset0:32 offset1:40
	ds_read2_b32 v[20:21], v13 offset1:8
	ds_read2_b32 v[22:23], v13 offset0:64 offset1:72
	ds_read2_b32 v[24:25], v13 offset0:96 offset1:104
	ds_read2_b32 v[26:27], v13 offset0:128 offset1:136
	ds_read2_b32 v[28:29], v13 offset0:160 offset1:168
	ds_read2_b32 v[30:31], v13 offset0:192 offset1:200
	ds_read2_b32 v[32:33], v13 offset0:224 offset1:232
	s_mov_b32 s0, 0x8000
	s_waitcnt lgkmcnt(0)
	v_cvt_pk_bf16_f32 v14, v20, v18
	v_cvt_pk_bf16_f32 v15, v22, v24
	v_cvt_pk_bf16_f32 v16, v26, v28
	v_cvt_pk_bf16_f32 v17, v30, v32
	v_add_co_u32_e32 v18, vcc, s0, v4
	global_store_dwordx4 v[4:5], v[14:17], off nt
	s_mov_b32 s0, 0x10000
	s_nop 0
	v_cvt_pk_bf16_f32 v14, v21, v19
	v_cvt_pk_bf16_f32 v15, v23, v25
	v_cvt_pk_bf16_f32 v16, v27, v29
	v_cvt_pk_bf16_f32 v17, v31, v33
	v_addc_co_u32_e32 v19, vcc, 0, v5, vcc
	global_store_dwordx4 v[18:19], v[14:17], off nt
	ds_read2_b32 v[18:19], v13 offset0:48 offset1:56
	ds_read2_b32 v[20:21], v13 offset0:16 offset1:24
	ds_read2_b32 v[22:23], v13 offset0:80 offset1:88
	ds_read2_b32 v[24:25], v13 offset0:112 offset1:120
	ds_read2_b32 v[26:27], v13 offset0:144 offset1:152
	ds_read2_b32 v[28:29], v13 offset0:176 offset1:184
	ds_read2_b32 v[30:31], v13 offset0:208 offset1:216
	ds_read2_b32 v[32:33], v13 offset0:240 offset1:248
	v_add_co_u32_e32 v34, vcc, s0, v4
	s_waitcnt lgkmcnt(0)
	v_cvt_pk_bf16_f32 v14, v20, v18
	v_addc_co_u32_e32 v35, vcc, 0, v5, vcc
	v_cvt_pk_bf16_f32 v15, v22, v24
	v_cvt_pk_bf16_f32 v16, v26, v28
	v_cvt_pk_bf16_f32 v17, v30, v32
	v_add_co_u32_e32 v18, vcc, 0x18000, v4
	global_store_dwordx4 v[34:35], v[14:17], off nt
	s_nop 1
	v_cvt_pk_bf16_f32 v14, v21, v19
	v_cvt_pk_bf16_f32 v15, v23, v25
	v_cvt_pk_bf16_f32 v16, v27, v29
	v_cvt_pk_bf16_f32 v17, v31, v33
	v_addc_co_u32_e32 v19, vcc, 0, v5, vcc
	global_store_dwordx4 v[18:19], v[14:17], off nt
	s_waitcnt lgkmcnt(0)
	s_andn2_b64 vcc, exec, s[40:41]
	s_cbranch_vccnz .LBB0_1781
	s_waitcnt vmcnt(0)
	s_mov_b32 s22, s23
.LBB0_1781:
	s_andn2_b64 vcc, exec, s[38:39]
	s_cbranch_vccnz .LBB0_1819
	s_add_u32 s23, s36, 0x23840000
	s_addc_u32 s24, s37, 0
	s_add_u32 s25, s36, 0x3840000
	s_addc_u32 s26, s37, 0
	s_branch .LBB0_1786
.LBB0_1783:
	s_lshl_b32 s6, s22, 5
	s_lshl_b32 s7, s22, 6
	s_and_b32 s6, s6, 0x7e0
	s_and_b32 s7, s7, 0xf00
	s_lshl_b32 s8, s8, 7
	s_add_i32 s8, s8, s7
	v_bitop3_b32 v6, s6, v209, v10 bitop3:0xc8
	v_or_b32_e32 v2, s6, v10
	v_or_b32_e32 v6, s8, v6
	s_and_b32 s7, s2, 0x7c0
	v_cndmask_b32_e64 v6, v2, v6, s[0:1]
	v_or_b32_e32 v2, s7, v10
	s_add_u32 s0, s3, s42
	v_lshlrev_b32_e32 v2, 13, v2
	s_addc_u32 s1, s27, s43
	v_lshl_add_u64 v[14:15], s[0:1], 0, v[2:3]
	s_lshl_b32 s92, s6, 2
	v_lshl_add_u64 v[14:15], v[14:15], 0, s[92:93]
	v_lshlrev_b32_e32 v2, 2, v11
	v_lshl_add_u64 v[14:15], v[14:15], 0, v[2:3]
	s_add_i32 s0, s94, 0x2080
	s_mov_b32 s1, m0
	s_mov_b32 m0, s0
	s_nop 0
	global_load_lds_dwordx4 v[14:15], off nt
	s_mov_b32 m0, s1
	s_mov_b64 s[0:1], 0x10000
	v_lshl_add_u64 v[16:17], v[14:15], 0, s[0:1]
	s_add_i32 s0, s94, 0x2490
	s_mov_b32 s1, m0
	s_mov_b32 m0, s0
	s_nop 0
	global_load_lds_dwordx4 v[16:17], off nt
	s_mov_b32 m0, s1
	v_lshl_add_u64 v[16:17], v[14:15], 0, s[84:85]
	s_add_i32 s0, s94, 0x28a0
	s_mov_b32 s1, m0
	s_mov_b32 m0, s0
	s_nop 0
	global_load_lds_dwordx4 v[16:17], off nt
	s_mov_b32 m0, s1
	s_mov_b64 s[0:1], 0x30000
	v_lshl_add_u64 v[16:17], v[14:15], 0, s[0:1]
	s_add_i32 s0, s94, 0x2cb0
	s_mov_b32 s1, m0
	s_mov_b32 m0, s0
	s_nop 0
	global_load_lds_dwordx4 v[16:17], off nt
	s_mov_b32 m0, s1
	s_mov_b64 s[0:1], 0x40000
	v_lshl_add_u64 v[16:17], v[14:15], 0, s[0:1]
	s_add_i32 s0, s94, 0x30c0
	s_mov_b32 s1, m0
	s_mov_b32 m0, s0
	s_nop 0
	global_load_lds_dwordx4 v[16:17], off nt
	s_mov_b32 m0, s1
	s_mov_b64 s[0:1], 0x50000
	v_lshl_add_u64 v[16:17], v[14:15], 0, s[0:1]
	s_add_i32 s0, s94, 0x34d0
	s_mov_b32 s1, m0
	s_mov_b32 m0, s0
	s_nop 0
	global_load_lds_dwordx4 v[16:17], off nt
	s_mov_b32 m0, s1
	s_mov_b64 s[0:1], 0x60000
	v_lshl_add_u64 v[16:17], v[14:15], 0, s[0:1]
	s_add_i32 s0, s94, 0x38e0
	s_mov_b32 s1, m0
	s_mov_b32 m0, s0
	s_nop 0
	global_load_lds_dwordx4 v[16:17], off nt
	s_mov_b32 m0, s1
	v_ashrrev_i32_e32 v7, 31, v6
	s_mov_b64 s[0:1], 0x70000
	v_lshlrev_b64 v[6:7], 12, v[6:7]
	v_lshl_add_u64 v[14:15], v[14:15], 0, s[0:1]
	s_add_i32 s0, s94, 0x3cf0
	s_mov_b32 s1, m0
	s_mov_b32 m0, s0
	s_nop 0
	global_load_lds_dwordx4 v[14:15], off nt
	s_mov_b32 m0, s1
	v_lshl_add_u64 v[6:7], s[40:41], 0, v[6:7]
	s_lshl_b32 s92, s7, 1
	s_waitcnt vmcnt(12)
	v_lshl_add_u64 v[6:7], v[6:7], 0, s[92:93]
	v_lshlrev_b32_e32 v2, 1, v12
	v_lshl_add_u64 v[6:7], v[6:7], 0, v[2:3]
	s_mov_b32 s27, s2

.LBB0_1785:
	s_and_b64 vcc, exec, s[38:39]
	s_mov_b32 s22, s27
	s_cbranch_vccnz .LBB0_1818
.LBB0_1786:
	s_add_i32 s27, s22, 0x200
	s_cmp_lt_i32 s27, s12
	s_cselect_b64 s[40:41], -1, 0
	s_cmp_ge_i32 s27, s12
	s_mov_b64 s[0:1], -1
	s_cbranch_scc0 .LBB0_1788
	s_waitcnt vmcnt(0)
	s_mov_b64 s[0:1], 0
.LBB0_1788:
	s_andn2_b64 vcc, exec, s[0:1]
	s_cbranch_vccnz .LBB0_1802
	s_mul_hi_i32 s0, s27, 0x2aaaaaab
	s_lshr_b32 s1, s0, 31
	s_ashr_i32 s6, s0, 14
	s_add_i32 s6, s6, s1
	s_mul_i32 s8, s6, 0xfffe8000
	s_add_i32 s8, s8, s27
	s_add_i32 s0, s8, 0x7fff
	s_cmpk_gt_u32 s0, 0xfffe
	s_mov_b64 s[0:1], -1
	s_cbranch_scc0 .LBB0_1795
	s_and_b32 s0, s8, 0xffff8000
	s_cmpk_lg_u32 s0, 0x8000
	s_mov_b64 s[0:1], -1
	s_cbranch_scc0 .LBB0_1792
	v_readlane_b32 s0, v253, 6
	s_nop 1
	v_mov_b32_e32 v2, s0
	ds_read_b64 v[4:5], v2
	s_mov_b64 s[0:1], 0
	s_waitcnt lgkmcnt(0)
	v_readfirstlane_b32 s2, v4
	v_readfirstlane_b32 s3, v5

.LBB0_1797:
	s_ashr_i32 s0, s8, 31
	s_lshr_b32 s0, s0, 17
	s_add_i32 s28, s8, s0
	s_and_b32 s0, s28, 0xffff8000
	s_sub_i32 s0, s8, s0
	s_ashr_i32 s0, s0, 11
	s_lshl_b32 s1, s6, 4
	s_add_i32 s6, s0, s1
	s_ashr_i32 s7, s6, 31
	s_cmp_lt_i32 s8, 0x10000
	s_cselect_b64 s[0:1], -1, 0
	s_cmp_gt_i32 s8, 0xffff
	s_mov_b64 s[8:9], -1
	s_cbranch_scc0 .LBB0_1799
	s_lshl_b64 s[8:9], s[6:7], 23
	s_add_u32 s38, s23, s8
	s_addc_u32 s39, s24, s9
	s_lshl_b64 s[42:43], s[6:7], 24
	s_mov_b64 s[8:9], 0
.LBB0_1799:
	s_andn2_b64 vcc, exec, s[8:9]
	s_ashr_i32 s8, s28, 15
	s_cbranch_vccnz .LBB0_1801
	s_lshl_b64 s[42:43], s[6:7], 24
	s_add_u32 s38, s25, s42
	s_addc_u32 s39, s26, s43
.LBB0_1801:
	s_lshl_b32 s6, s22, 5
	s_lshl_b32 s7, s22, 6
	s_and_b32 s6, s6, 0x7e0
	s_and_b32 s7, s7, 0xf00
	s_lshl_b32 s8, s8, 7
	s_add_i32 s8, s8, s7
	v_bitop3_b32 v4, s6, v209, v10 bitop3:0xc8
	v_or_b32_e32 v2, s6, v10
	v_or_b32_e32 v4, s8, v4
	s_and_b32 s7, s27, 0x7c0
	v_cndmask_b32_e64 v4, v2, v4, s[0:1]
	v_or_b32_e32 v2, s7, v10
	s_add_u32 s0, s2, s42
	v_lshlrev_b32_e32 v2, 13, v2
	s_addc_u32 s1, s3, s43
	v_lshl_add_u64 v[14:15], s[0:1], 0, v[2:3]
	s_lshl_b32 s92, s6, 2
	v_lshl_add_u64 v[14:15], v[14:15], 0, s[92:93]
	v_lshlrev_b32_e32 v2, 2, v11
	v_lshl_add_u64 v[14:15], v[14:15], 0, v[2:3]
	s_mov_b32 s0, m0
	s_mov_b32 m0, s94
	s_nop 0
	global_load_lds_dwordx4 v[14:15], off nt
	s_mov_b32 m0, s0
	s_mov_b64 s[0:1], 0x10000
	v_lshl_add_u64 v[16:17], v[14:15], 0, s[0:1]
	s_mov_b32 s0, m0
	s_mov_b32 m0, s15
	s_nop 0
	global_load_lds_dwordx4 v[16:17], off nt
	s_mov_b32 m0, s0
	v_lshl_add_u64 v[16:17], v[14:15], 0, s[84:85]
	s_mov_b32 s0, m0
	s_mov_b32 m0, s16
	s_nop 0
	global_load_lds_dwordx4 v[16:17], off nt
	s_mov_b32 m0, s0
	s_mov_b64 s[0:1], 0x30000
	v_lshl_add_u64 v[16:17], v[14:15], 0, s[0:1]
	s_mov_b32 s0, m0
	s_mov_b32 m0, s17
	s_nop 0
	global_load_lds_dwordx4 v[16:17], off nt
	s_mov_b32 m0, s0
	s_mov_b64 s[0:1], 0x40000
	v_lshl_add_u64 v[16:17], v[14:15], 0, s[0:1]
	s_mov_b32 s0, m0
	s_mov_b32 m0, s18
	s_nop 0
	global_load_lds_dwordx4 v[16:17], off nt
	s_mov_b32 m0, s0
	s_mov_b64 s[0:1], 0x50000
	v_lshl_add_u64 v[16:17], v[14:15], 0, s[0:1]
	s_mov_b32 s0, m0
	s_mov_b32 m0, s19
	s_nop 0
	global_load_lds_dwordx4 v[16:17], off nt
	s_mov_b32 m0, s0
	s_mov_b64 s[0:1], 0x60000
	v_lshl_add_u64 v[16:17], v[14:15], 0, s[0:1]
	s_mov_b32 s0, m0
	s_mov_b32 m0, s20
	s_nop 0
	global_load_lds_dwordx4 v[16:17], off nt
	s_mov_b32 m0, s0
	v_ashrrev_i32_e32 v5, 31, v4
	s_mov_b64 s[0:1], 0x70000
	v_lshlrev_b64 v[4:5], 12, v[4:5]
	v_lshl_add_u64 v[14:15], v[14:15], 0, s[0:1]
	s_mov_b32 s0, m0
	s_mov_b32 m0, s21
	s_nop 0
	global_load_lds_dwordx4 v[14:15], off nt
	s_mov_b32 m0, s0
	v_lshl_add_u64 v[4:5], s[38:39], 0, v[4:5]
	s_lshl_b32 s92, s7, 1
	s_waitcnt vmcnt(12)
	v_lshl_add_u64 v[4:5], v[4:5], 0, s[92:93]
	v_lshlrev_b32_e32 v2, 1, v12
	v_lshl_add_u64 v[4:5], v[4:5], 0, v[2:3]
.LBB0_1802:
	v_add_u32_e32 v2, 0x2000, v13
	v_add_u32_e32 v34, 0x2400, v13
	ds_read2_b32 v[18:19], v2 offset0:64 offset1:72
	ds_read2_b32 v[20:21], v2 offset0:32 offset1:40
	ds_read2_b32 v[22:23], v2 offset0:96 offset1:104
	ds_read2_b32 v[24:25], v2 offset0:128 offset1:136
	ds_read2_b32 v[26:27], v2 offset0:160 offset1:168
	ds_read2_b32 v[28:29], v2 offset0:192 offset1:200
	ds_read2_b32 v[30:31], v2 offset0:224 offset1:232
	ds_read2_b32 v[32:33], v34 offset1:8
	s_mov_b32 s0, 0x8000
	s_waitcnt lgkmcnt(0)
	v_cvt_pk_bf16_f32 v14, v20, v18
	v_cvt_pk_bf16_f32 v15, v22, v24
	v_cvt_pk_bf16_f32 v16, v26, v28
	v_cvt_pk_bf16_f32 v17, v30, v32
	v_add_co_u32_e32 v18, vcc, s0, v6
	global_store_dwordx4 v[6:7], v[14:17], off nt
	s_mov_b32 s0, 0x10000
	s_mov_b64 s[38:39], -1
	v_cvt_pk_bf16_f32 v14, v21, v19
	v_cvt_pk_bf16_f32 v15, v23, v25
	v_cvt_pk_bf16_f32 v16, v27, v29
	v_cvt_pk_bf16_f32 v17, v31, v33
	v_addc_co_u32_e32 v19, vcc, 0, v7, vcc
	global_store_dwordx4 v[18:19], v[14:17], off nt
	ds_read2_b32 v[18:19], v2 offset0:80 offset1:88
	ds_read2_b32 v[20:21], v2 offset0:48 offset1:56
	ds_read2_b32 v[22:23], v2 offset0:112 offset1:120
	ds_read2_b32 v[24:25], v2 offset0:144 offset1:152
	ds_read2_b32 v[26:27], v2 offset0:176 offset1:184
	ds_read2_b32 v[28:29], v2 offset0:208 offset1:216
	ds_read2_b32 v[30:31], v2 offset0:240 offset1:248
	ds_read2_b32 v[32:33], v34 offset0:16 offset1:24
	v_add_co_u32_e32 v34, vcc, s0, v6
	s_waitcnt lgkmcnt(0)
	v_cvt_pk_bf16_f32 v14, v20, v18
	v_addc_co_u32_e32 v35, vcc, 0, v7, vcc
	v_cvt_pk_bf16_f32 v15, v22, v24
	v_cvt_pk_bf16_f32 v16, v26, v28
	v_cvt_pk_bf16_f32 v17, v30, v32
	v_add_co_u32_e32 v18, vcc, 0x18000, v6
	global_store_dwordx4 v[34:35], v[14:17], off nt
	s_nop 1
	v_cvt_pk_bf16_f32 v14, v21, v19
	v_cvt_pk_bf16_f32 v15, v23, v25
	v_cvt_pk_bf16_f32 v16, v27, v29
	v_cvt_pk_bf16_f32 v17, v31, v33
	v_addc_co_u32_e32 v19, vcc, 0, v7, vcc
	global_store_dwordx4 v[18:19], v[14:17], off nt
	s_waitcnt lgkmcnt(0)
	s_andn2_b64 vcc, exec, s[40:41]
	s_cbranch_vccnz .LBB0_1785
	s_add_i32 s2, s22, 0x400
	s_cmp_ge_i32 s2, s12
	s_cselect_b64 s[38:39], -1, 0
	s_mov_b64 s[0:1], -1
	s_and_b64 vcc, exec, s[38:39]
	s_cbranch_vccz .LBB0_1805
	s_waitcnt vmcnt(0)
	s_mov_b64 s[0:1], 0
.LBB0_1805:
	s_andn2_b64 vcc, exec, s[0:1]
	s_cbranch_vccnz .LBB0_1784
	s_mul_hi_i32 s0, s2, 0x2aaaaaab
	s_lshr_b32 s1, s0, 31
	s_ashr_i32 s6, s0, 14
	s_add_i32 s6, s6, s1
	s_mul_i32 s8, s6, 0xfffe8000
	s_add_i32 s8, s8, s2
	s_add_i32 s0, s8, 0x7fff
	s_cmpk_gt_u32 s0, 0xfffe
	s_mov_b64 s[0:1], -1
	s_cbranch_scc0 .LBB0_1812
	s_and_b32 s0, s8, 0xffff8000
	s_cmpk_lg_u32 s0, 0x8000
	s_mov_b64 s[0:1], -1
	s_cbranch_scc0 .LBB0_1809
	v_readlane_b32 s0, v253, 6
	s_nop 1
	v_mov_b32_e32 v2, s0
	ds_read_b64 v[6:7], v2
	s_mov_b64 s[0:1], 0
	s_waitcnt lgkmcnt(0)
	v_readfirstlane_b32 s3, v6
	v_readfirstlane_b32 s27, v7
.LBB0_1809:
	s_andn2_b64 vcc, exec, s[0:1]
	s_cbranch_vccnz .LBB0_1811
	v_readlane_b32 s0, v252, 36
	s_nop 1
	v_mov_b32_e32 v2, s0
	ds_read_b64 v[6:7], v2
	s_waitcnt lgkmcnt(0)
	v_readfirstlane_b32 s3, v6
	v_readfirstlane_b32 s27, v7

.LBB0_1812:
	s_andn2_b64 vcc, exec, s[0:1]
	s_cbranch_vccnz .LBB0_1814
	v_readlane_b32 s0, v253, 31
	s_nop 1
	v_mov_b32_e32 v2, s0
	ds_read_b64 v[6:7], v2
	s_waitcnt lgkmcnt(0)
	v_readfirstlane_b32 s3, v6
	v_readfirstlane_b32 s27, v7
.LBB0_1814:
	s_ashr_i32 s0, s8, 31
	s_lshr_b32 s0, s0, 17
	s_add_i32 s28, s8, s0
	s_and_b32 s0, s28, 0xffff8000
	s_sub_i32 s0, s8, s0
	s_ashr_i32 s0, s0, 11
	s_lshl_b32 s1, s6, 4
	s_add_i32 s6, s0, s1
	s_ashr_i32 s7, s6, 31
	s_cmp_lt_i32 s8, 0x10000
	s_cselect_b64 s[0:1], -1, 0
	s_cmp_gt_i32 s8, 0xffff
	s_mov_b64 s[8:9], -1
	s_cbranch_scc0 .LBB0_1816
	s_lshl_b64 s[8:9], s[6:7], 23
	s_add_u32 s40, s23, s8
	s_addc_u32 s41, s24, s9
	s_lshl_b64 s[42:43], s[6:7], 24
	s_mov_b64 s[8:9], 0
.LBB0_1816:
	s_andn2_b64 vcc, exec, s[8:9]
	s_ashr_i32 s8, s28, 15
	s_cbranch_vccnz .LBB0_1783
	s_lshl_b64 s[42:43], s[6:7], 24
	s_add_u32 s40, s25, s42
	s_addc_u32 s41, s26, s43
	s_branch .LBB0_1783
.LBB0_1818:
	s_waitcnt vmcnt(0)
	v_readlane_b32 s26, v254, 28
	v_readlane_b32 s27, v254, 29
.LBB0_1819:
	s_mov_b64 s[0:1], 0
.LBB0_1820:
	s_andn2_b64 vcc, exec, s[0:1]
	s_cbranch_vccnz .LBB0_1890
	s_and_b32 s2, s65, -8
	v_readlane_b32 s0, v253, 7
	s_add_i32 s2, s2, s0
	s_add_i32 s3, s2, s68
	s_cmpk_gt_i32 s3, 0x7ff
	s_cbranch_scc1 .LBB0_1890
	s_add_i32 s22, s3, s64
	s_mul_hi_i32 s0, s22, 0x2aaaaaab
	s_lshr_b32 s1, s0, 31
	s_ashr_i32 s7, s0, 14
	s_add_i32 s7, s7, s1
	s_mul_i32 s6, s7, 0xfffe8000
	s_add_i32 s6, s6, s22
	s_add_i32 s0, s6, 0x7fff
	s_cmpk_gt_u32 s0, 0xfffe
	s_mov_b64 s[0:1], -1
	s_cbranch_scc0 .LBB0_1828
	s_and_b32 s0, s6, 0xffff8000
	s_cmpk_lg_u32 s0, 0x8000
	s_mov_b64 s[0:1], -1
	s_cbranch_scc0 .LBB0_1825
	v_readlane_b32 s0, v253, 6
	s_nop 1
	v_mov_b32_e32 v2, s0
	ds_read_b64 v[4:5], v2
	s_mov_b64 s[0:1], 0
	s_waitcnt lgkmcnt(0)
	v_readfirstlane_b32 s12, v4
	v_readfirstlane_b32 s15, v5
.LBB0_1825:
	s_andn2_b64 vcc, exec, s[0:1]
	s_cbranch_vccnz .LBB0_1827
	v_readlane_b32 s0, v252, 36
	s_nop 1
	v_mov_b32_e32 v2, s0
	ds_read_b64 v[4:5], v2
	s_waitcnt lgkmcnt(0)
	v_readfirstlane_b32 s12, v4
	v_readfirstlane_b32 s15, v5

.LBB0_1828:
	s_andn2_b64 vcc, exec, s[0:1]
	s_cbranch_vccnz .LBB0_1830
	v_readlane_b32 s0, v253, 31
	s_nop 1
	v_mov_b32_e32 v2, s0
	ds_read_b64 v[4:5], v2
	s_waitcnt lgkmcnt(0)
	v_readfirstlane_b32 s12, v4
	v_readfirstlane_b32 s15, v5
.LBB0_1830:
	s_ashr_i32 s0, s6, 31
	s_lshr_b32 s0, s0, 17
	s_add_i32 s23, s6, s0
	s_and_b32 s0, s23, 0xffff8000
	s_sub_i32 s0, s6, s0
	s_ashr_i32 s0, s0, 11
	s_lshl_b32 s1, s7, 4
	s_add_i32 s38, s0, s1
	s_ashr_i32 s39, s38, 31
	s_cmp_lt_i32 s6, 0x10000
	s_cselect_b64 s[0:1], -1, 0
	s_cmp_gt_i32 s6, 0xffff
	s_mov_b64 s[8:9], -1
	s_cbranch_scc0 .LBB0_1832
	s_lshl_b64 s[6:7], s[38:39], 23
	s_add_u32 s6, s36, s6
	s_addc_u32 s7, s37, s7
	s_add_u32 s42, s6, 0x23840000
	s_addc_u32 s43, s7, 0
	s_lshl_b64 s[6:7], s[38:39], 24
	s_mov_b64 s[8:9], 0

.LBB0_1834:
	s_lshl_b32 s8, s2, 5
	s_and_b32 s8, s8, 0x7e0
	v_lshrrev_b32_e32 v9, 3, v9
	s_and_b32 s3, s3, 0x7c0
	v_or_b32_e32 v2, s3, v9
	s_add_u32 s6, s12, s6
	v_lshlrev_b32_e32 v2, 13, v2
	s_addc_u32 s7, s15, s7
	v_lshl_add_u64 v[4:5], s[6:7], 0, v[2:3]
	s_lshl_b32 s92, s8, 2
	v_and_b32_e32 v11, 7, v8
	v_lshl_add_u64 v[4:5], v[4:5], 0, s[92:93]
	v_lshlrev_b32_e32 v2, 4, v11
	v_lshl_add_u64 v[4:5], v[4:5], 0, v[2:3]
	s_mov_b32 s6, m0
	s_mov_b32 m0, s94
	s_nop 0
	global_load_lds_dwordx4 v[4:5], off nt
	s_mov_b32 m0, s6
	s_mov_b64 s[6:7], 0x10000
	v_lshl_add_u64 v[6:7], v[4:5], 0, s[6:7]
	s_add_i32 s12, s94, 0x410
	s_mov_b32 s6, m0
	s_mov_b32 m0, s12
	s_nop 0
	global_load_lds_dwordx4 v[6:7], off nt
	s_mov_b32 m0, s6
	v_lshl_add_u64 v[6:7], v[4:5], 0, s[84:85]
	s_add_i32 s15, s94, 0x820
	s_mov_b32 s6, m0
	s_mov_b32 m0, s15
	s_nop 0
	global_load_lds_dwordx4 v[6:7], off nt
	s_mov_b32 m0, s6
	s_mov_b64 s[6:7], 0x30000
	v_lshl_add_u64 v[6:7], v[4:5], 0, s[6:7]
	s_add_i32 s16, s94, 0xc30
	s_mov_b32 s6, m0
	s_mov_b32 m0, s16
	s_nop 0
	global_load_lds_dwordx4 v[6:7], off nt
	s_mov_b32 m0, s6
	s_mov_b64 s[6:7], 0x40000
	v_lshl_add_u64 v[6:7], v[4:5], 0, s[6:7]
	s_add_i32 s17, s94, 0x1040
	s_mov_b32 s6, m0
	s_mov_b32 m0, s17
	s_nop 0
	global_load_lds_dwordx4 v[6:7], off nt
	s_mov_b32 m0, s6
	s_mov_b64 s[6:7], 0x50000
	v_lshl_add_u64 v[6:7], v[4:5], 0, s[6:7]
	s_add_i32 s18, s94, 0x1450
	s_mov_b32 s6, m0
	s_mov_b32 m0, s18
	s_nop 0
	global_load_lds_dwordx4 v[6:7], off nt
	s_mov_b32 m0, s6
	s_mov_b64 s[6:7], 0x60000
	v_lshl_add_u64 v[6:7], v[4:5], 0, s[6:7]
	s_add_i32 s19, s94, 0x1860
	s_mov_b32 s6, m0
	s_mov_b32 m0, s19
	s_nop 0
	global_load_lds_dwordx4 v[6:7], off nt
	s_mov_b32 m0, s6
	s_add_i32 s20, s94, 0x1c70
	s_add_i32 s21, s22, 0x200
	s_mov_b64 s[6:7], 0x70000
	s_cmp_lt_i32 s21, s66
	v_lshl_add_u64 v[4:5], v[4:5], 0, s[6:7]
	s_mov_b32 s6, m0
	s_mov_b32 m0, s20
	s_nop 0
	global_load_lds_dwordx4 v[4:5], off nt
	s_mov_b32 m0, s6
	s_cselect_b64 s[38:39], -1, 0
	s_cmp_ge_i32 s21, s66
	s_cselect_b64 s[40:41], -1, 0
	s_mov_b64 s[6:7], -1
	s_and_b64 vcc, exec, s[40:41]
	s_cbranch_vccz .LBB0_1836
	s_waitcnt vmcnt(0)
	s_mov_b64 s[6:7], 0
.LBB0_1836:
	s_ashr_i32 s9, s23, 15
	s_lshl_b32 s2, s2, 6
	v_or_b32_e32 v12, s8, v9
	s_and_b32 s2, s2, 0xf00
	s_lshl_b32 s9, s9, 7
	v_mov_b32_e32 v4, s8
	s_movk_i32 s8, 0x67
	s_add_i32 s9, s9, s2
	v_bitop3_b32 v13, v9, s8, v4 bitop3:0xc8
	v_or_b32_e32 v4, s9, v13
	v_cndmask_b32_e64 v4, v12, v4, s[0:1]
	v_ashrrev_i32_e32 v5, 31, v4
	v_lshlrev_b64 v[4:5], 12, v[4:5]
	v_lshl_add_u64 v[4:5], s[42:43], 0, v[4:5]
	s_lshl_b32 s0, s3, 1
	s_mov_b32 s1, s93
	v_lshl_add_u64 v[4:5], v[4:5], 0, s[0:1]
	v_lshl_add_u64 v[4:5], v[4:5], 0, v[2:3]
	v_lshlrev_b32_e32 v8, 2, v11
	v_lshlrev_b32_e32 v10, 3, v11
	s_andn2_b64 vcc, exec, s[6:7]
	v_mov_b64_e32 v[6:7], v[4:5]
	s_cbranch_vccnz .LBB0_1850
	s_mul_hi_i32 s0, s21, 0x2aaaaaab
	s_lshr_b32 s1, s0, 31
	s_ashr_i32 s7, s0, 14
	s_add_i32 s7, s7, s1
	s_mul_i32 s6, s7, 0xfffe8000
	s_add_i32 s6, s6, s21
	s_add_i32 s0, s6, 0x7fff
	s_cmpk_gt_u32 s0, 0xfffe
	s_mov_b64 s[0:1], -1
	s_cbranch_scc0 .LBB0_1843
	s_and_b32 s0, s6, 0xffff8000
	s_cmpk_lg_u32 s0, 0x8000
	s_mov_b64 s[0:1], -1
	s_cbranch_scc0 .LBB0_1840
	v_readlane_b32 s0, v253, 6
	s_nop 1
	v_mov_b32_e32 v2, s0
	ds_read_b64 v[6:7], v2
	s_mov_b64 s[0:1], 0
	s_waitcnt lgkmcnt(0)
	v_readfirstlane_b32 s3, v6
	v_readfirstlane_b32 s23, v7
.LBB0_1840:
	s_andn2_b64 vcc, exec, s[0:1]
	s_cbranch_vccnz .LBB0_1842
	v_readlane_b32 s0, v252, 36
	s_nop 1
	v_mov_b32_e32 v2, s0
	ds_read_b64 v[6:7], v2
	s_waitcnt lgkmcnt(0)
	v_readfirstlane_b32 s3, v6
	v_readfirstlane_b32 s23, v7

.LBB0_1843:
	s_andn2_b64 vcc, exec, s[0:1]
	s_cbranch_vccnz .LBB0_1845
	v_readlane_b32 s0, v253, 31
	s_nop 1
	v_mov_b32_e32 v2, s0
	ds_read_b64 v[6:7], v2
	s_waitcnt lgkmcnt(0)
	v_readfirstlane_b32 s3, v6
	v_readfirstlane_b32 s23, v7
.LBB0_1845:
	s_ashr_i32 s0, s6, 31
	s_lshr_b32 s0, s0, 17
	s_add_i32 s24, s6, s0
	s_and_b32 s0, s24, 0xffff8000
	s_sub_i32 s0, s6, s0
	s_ashr_i32 s0, s0, 11
	s_lshl_b32 s1, s7, 4
	s_add_i32 s44, s0, s1
	s_ashr_i32 s45, s44, 31
	s_cmp_lt_i32 s6, 0x10000
	s_cselect_b64 s[0:1], -1, 0
	s_cmp_gt_i32 s6, 0xffff
	s_mov_b64 s[8:9], -1
	s_cbranch_scc0 .LBB0_1847
	s_lshl_b64 s[6:7], s[44:45], 23
	s_add_u32 s6, s36, s6
	s_addc_u32 s7, s37, s7
	s_add_u32 s42, s6, 0x23840000
	s_addc_u32 s43, s7, 0
	s_lshl_b64 s[6:7], s[44:45], 24
	s_mov_b64 s[8:9], 0
.LBB0_1847:
	s_andn2_b64 vcc, exec, s[8:9]
	s_ashr_i32 s8, s24, 15
	s_cbranch_vccnz .LBB0_1849
	s_lshl_b64 s[6:7], s[44:45], 24
	s_add_u32 s9, s36, s6
	s_addc_u32 s24, s37, s7
	s_add_u32 s42, s9, 0x3840000
	s_addc_u32 s43, s24, 0
.LBB0_1849:
	s_lshl_b32 s8, s8, 7
	s_add_i32 s8, s8, s2
	v_or_b32_e32 v2, s8, v13
	s_and_b32 s2, s21, 0x7c0
	v_cndmask_b32_e64 v6, v12, v2, s[0:1]
	v_or_b32_e32 v2, s2, v9
	s_add_u32 s0, s3, s6
	v_lshlrev_b32_e32 v2, 13, v2
	s_addc_u32 s1, s23, s7
	v_lshl_add_u64 v[12:13], s[0:1], 0, v[2:3]
	v_lshl_add_u64 v[12:13], v[12:13], 0, s[92:93]
	v_lshlrev_b32_e32 v2, 2, v8
	v_lshl_add_u64 v[12:13], v[12:13], 0, v[2:3]
	s_add_i32 s0, s94, 0x2080
	s_mov_b32 s1, m0
	s_mov_b32 m0, s0
	s_nop 0
	global_load_lds_dwordx4 v[12:13], off nt
	s_mov_b32 m0, s1
	s_mov_b64 s[0:1], 0x10000
	v_lshl_add_u64 v[14:15], v[12:13], 0, s[0:1]
	s_add_i32 s0, s94, 0x2490
	s_mov_b32 s1, m0
	s_mov_b32 m0, s0
	s_nop 0
	global_load_lds_dwordx4 v[14:15], off nt
	s_mov_b32 m0, s1
	v_lshl_add_u64 v[14:15], v[12:13], 0, s[84:85]
	s_add_i32 s0, s94, 0x28a0
	s_mov_b32 s1, m0
	s_mov_b32 m0, s0
	s_nop 0
	global_load_lds_dwordx4 v[14:15], off nt
	s_mov_b32 m0, s1
	s_mov_b64 s[0:1], 0x30000
	v_lshl_add_u64 v[14:15], v[12:13], 0, s[0:1]
	s_add_i32 s0, s94, 0x2cb0
	s_mov_b32 s1, m0
	s_mov_b32 m0, s0
	s_nop 0
	global_load_lds_dwordx4 v[14:15], off nt
	s_mov_b32 m0, s1
	s_mov_b64 s[0:1], 0x40000
	v_lshl_add_u64 v[14:15], v[12:13], 0, s[0:1]
	s_add_i32 s0, s94, 0x30c0
	s_mov_b32 s1, m0
	s_mov_b32 m0, s0
	s_nop 0
	global_load_lds_dwordx4 v[14:15], off nt
	s_mov_b32 m0, s1
	s_mov_b64 s[0:1], 0x50000
	v_lshl_add_u64 v[14:15], v[12:13], 0, s[0:1]
	s_add_i32 s0, s94, 0x34d0
	s_mov_b32 s1, m0
	s_mov_b32 m0, s0
	s_nop 0
	global_load_lds_dwordx4 v[14:15], off nt
	s_mov_b32 m0, s1
	s_mov_b64 s[0:1], 0x60000
	v_lshl_add_u64 v[14:15], v[12:13], 0, s[0:1]
	s_add_i32 s0, s94, 0x38e0
	s_mov_b32 s1, m0
	s_mov_b32 m0, s0
	s_nop 0
	global_load_lds_dwordx4 v[14:15], off nt
	s_mov_b32 m0, s1
	v_ashrrev_i32_e32 v7, 31, v6
	s_mov_b64 s[0:1], 0x70000
	v_lshlrev_b64 v[6:7], 12, v[6:7]
	v_lshl_add_u64 v[12:13], v[12:13], 0, s[0:1]
	s_add_i32 s0, s94, 0x3cf0
	s_mov_b32 s1, m0
	s_mov_b32 m0, s0
	s_nop 0
	global_load_lds_dwordx4 v[12:13], off nt
	s_mov_b32 m0, s1
	v_lshl_add_u64 v[6:7], s[42:43], 0, v[6:7]
	s_lshl_b32 s92, s2, 1
	s_waitcnt vmcnt(8)
	v_lshl_add_u64 v[6:7], v[6:7], 0, s[92:93]
	v_lshlrev_b32_e32 v2, 1, v10
	v_lshl_add_u64 v[6:7], v[6:7], 0, v[2:3]
.LBB0_1850:
	v_mul_u32_u24_e32 v2, 0x410, v11
	v_lshlrev_b32_e32 v11, 2, v9
	v_add3_u32 v11, s94, v2, v11
	ds_read2_b32 v[16:17], v11 offset0:32 offset1:40
	ds_read2_b32 v[18:19], v11 offset1:8
	ds_read2_b32 v[20:21], v11 offset0:64 offset1:72
	ds_read2_b32 v[22:23], v11 offset0:96 offset1:104
	ds_read2_b32 v[24:25], v11 offset0:128 offset1:136
	ds_read2_b32 v[26:27], v11 offset0:160 offset1:168
	ds_read2_b32 v[28:29], v11 offset0:192 offset1:200
	ds_read2_b32 v[30:31], v11 offset0:224 offset1:232
	s_mov_b32 s0, 0x8000
	s_waitcnt lgkmcnt(0)
	v_cvt_pk_bf16_f32 v12, v18, v16
	v_cvt_pk_bf16_f32 v13, v20, v22
	v_cvt_pk_bf16_f32 v14, v24, v26
	v_cvt_pk_bf16_f32 v15, v28, v30
	v_add_co_u32_e32 v16, vcc, s0, v4
	global_store_dwordx4 v[4:5], v[12:15], off nt
	s_mov_b32 s0, 0x10000
	s_nop 0
	v_cvt_pk_bf16_f32 v12, v19, v17
	v_cvt_pk_bf16_f32 v13, v21, v23
	v_cvt_pk_bf16_f32 v14, v25, v27
	v_cvt_pk_bf16_f32 v15, v29, v31
	v_addc_co_u32_e32 v17, vcc, 0, v5, vcc
	global_store_dwordx4 v[16:17], v[12:15], off nt
	ds_read2_b32 v[16:17], v11 offset0:48 offset1:56
	ds_read2_b32 v[18:19], v11 offset0:16 offset1:24
	ds_read2_b32 v[20:21], v11 offset0:80 offset1:88
	ds_read2_b32 v[22:23], v11 offset0:112 offset1:120
	ds_read2_b32 v[24:25], v11 offset0:144 offset1:152
	ds_read2_b32 v[26:27], v11 offset0:176 offset1:184
	ds_read2_b32 v[28:29], v11 offset0:208 offset1:216
	ds_read2_b32 v[30:31], v11 offset0:240 offset1:248
	v_add_co_u32_e32 v32, vcc, s0, v4
	s_waitcnt lgkmcnt(0)
	v_cvt_pk_bf16_f32 v12, v18, v16
	v_addc_co_u32_e32 v33, vcc, 0, v5, vcc
	v_cvt_pk_bf16_f32 v13, v20, v22
	v_cvt_pk_bf16_f32 v14, v24, v26
	v_cvt_pk_bf16_f32 v15, v28, v30
	v_add_co_u32_e32 v16, vcc, 0x18000, v4
	global_store_dwordx4 v[32:33], v[12:15], off nt
	s_nop 1
	v_cvt_pk_bf16_f32 v12, v19, v17
	v_cvt_pk_bf16_f32 v13, v21, v23
	v_cvt_pk_bf16_f32 v14, v25, v27
	v_cvt_pk_bf16_f32 v15, v29, v31
	v_addc_co_u32_e32 v17, vcc, 0, v5, vcc
	global_store_dwordx4 v[16:17], v[12:15], off nt
	s_waitcnt lgkmcnt(0)
	s_andn2_b64 vcc, exec, s[40:41]
	s_cbranch_vccnz .LBB0_1852
	s_waitcnt vmcnt(0)
	s_mov_b32 s21, s22
.LBB0_1852:
	s_andn2_b64 vcc, exec, s[38:39]
	s_cbranch_vccnz .LBB0_1890
	s_add_u32 s22, s36, 0x23840000
	s_addc_u32 s23, s37, 0
	s_add_u32 s24, s36, 0x3840000
	s_addc_u32 s25, s37, 0
	s_branch .LBB0_1857
.LBB0_1854:
	s_lshl_b32 s6, s21, 5
	s_lshl_b32 s7, s21, 6
	s_and_b32 s6, s6, 0x7e0
	s_and_b32 s7, s7, 0xf00
	s_lshl_b32 s8, s8, 7
	s_add_i32 s8, s8, s7
	v_bitop3_b32 v6, s6, v209, v9 bitop3:0xc8
	v_or_b32_e32 v2, s6, v9
	v_or_b32_e32 v6, s8, v6
	s_and_b32 s7, s2, 0x7c0
	v_cndmask_b32_e64 v6, v2, v6, s[0:1]
	v_or_b32_e32 v2, s7, v9
	s_add_u32 s0, s3, s40
	v_lshlrev_b32_e32 v2, 13, v2
	s_addc_u32 s1, s26, s41
	v_lshl_add_u64 v[12:13], s[0:1], 0, v[2:3]
	s_lshl_b32 s92, s6, 2
	v_lshl_add_u64 v[12:13], v[12:13], 0, s[92:93]
	v_lshlrev_b32_e32 v2, 2, v8
	v_lshl_add_u64 v[12:13], v[12:13], 0, v[2:3]
	s_add_i32 s0, s94, 0x2080
	s_mov_b32 s1, m0
	s_mov_b32 m0, s0
	s_nop 0
	global_load_lds_dwordx4 v[12:13], off nt
	s_mov_b32 m0, s1
	s_mov_b64 s[0:1], 0x10000
	v_lshl_add_u64 v[14:15], v[12:13], 0, s[0:1]
	s_add_i32 s0, s94, 0x2490
	s_mov_b32 s1, m0
	s_mov_b32 m0, s0
	s_nop 0
	global_load_lds_dwordx4 v[14:15], off nt
	s_mov_b32 m0, s1
	v_lshl_add_u64 v[14:15], v[12:13], 0, s[84:85]
	s_add_i32 s0, s94, 0x28a0
	s_mov_b32 s1, m0
	s_mov_b32 m0, s0
	s_nop 0
	global_load_lds_dwordx4 v[14:15], off nt
	s_mov_b32 m0, s1
	s_mov_b64 s[0:1], 0x30000
	v_lshl_add_u64 v[14:15], v[12:13], 0, s[0:1]
	s_add_i32 s0, s94, 0x2cb0
	s_mov_b32 s1, m0
	s_mov_b32 m0, s0
	s_nop 0
	global_load_lds_dwordx4 v[14:15], off nt
	s_mov_b32 m0, s1
	s_mov_b64 s[0:1], 0x40000
	v_lshl_add_u64 v[14:15], v[12:13], 0, s[0:1]
	s_add_i32 s0, s94, 0x30c0
	s_mov_b32 s1, m0
	s_mov_b32 m0, s0
	s_nop 0
	global_load_lds_dwordx4 v[14:15], off nt
	s_mov_b32 m0, s1
	s_mov_b64 s[0:1], 0x50000
	v_lshl_add_u64 v[14:15], v[12:13], 0, s[0:1]
	s_add_i32 s0, s94, 0x34d0
	s_mov_b32 s1, m0
	s_mov_b32 m0, s0
	s_nop 0
	global_load_lds_dwordx4 v[14:15], off nt
	s_mov_b32 m0, s1
	s_mov_b64 s[0:1], 0x60000
	v_lshl_add_u64 v[14:15], v[12:13], 0, s[0:1]
	s_add_i32 s0, s94, 0x38e0
	s_mov_b32 s1, m0
	s_mov_b32 m0, s0
	s_nop 0
	global_load_lds_dwordx4 v[14:15], off nt
	s_mov_b32 m0, s1
	v_ashrrev_i32_e32 v7, 31, v6
	s_mov_b64 s[0:1], 0x70000
	v_lshlrev_b64 v[6:7], 12, v[6:7]
	v_lshl_add_u64 v[12:13], v[12:13], 0, s[0:1]
	s_add_i32 s0, s94, 0x3cf0
	s_mov_b32 s1, m0
	s_mov_b32 m0, s0
	s_nop 0
	global_load_lds_dwordx4 v[12:13], off nt
	s_mov_b32 m0, s1
	v_lshl_add_u64 v[6:7], s[38:39], 0, v[6:7]
	s_lshl_b32 s92, s7, 1
	s_waitcnt vmcnt(12)
	v_lshl_add_u64 v[6:7], v[6:7], 0, s[92:93]
	v_lshlrev_b32_e32 v2, 1, v10
	v_lshl_add_u64 v[6:7], v[6:7], 0, v[2:3]
	s_mov_b32 s26, s2
.LBB0_1855:
	ds_read2_b32 v[16:17], v11 offset0:32 offset1:40
	ds_read2_b32 v[18:19], v11 offset1:8
	ds_read2_b32 v[20:21], v11 offset0:64 offset1:72
	ds_read2_b32 v[22:23], v11 offset0:96 offset1:104
	ds_read2_b32 v[24:25], v11 offset0:128 offset1:136
	ds_read2_b32 v[26:27], v11 offset0:160 offset1:168
	ds_read2_b32 v[28:29], v11 offset0:192 offset1:200
	ds_read2_b32 v[30:31], v11 offset0:224 offset1:232
	s_mov_b32 s0, 0x8000
	s_waitcnt lgkmcnt(0)
	v_cvt_pk_bf16_f32 v12, v18, v16
	v_cvt_pk_bf16_f32 v13, v20, v22
	v_cvt_pk_bf16_f32 v14, v24, v26
	v_cvt_pk_bf16_f32 v15, v28, v30
	v_add_co_u32_e32 v16, vcc, s0, v4
	global_store_dwordx4 v[4:5], v[12:15], off nt
	s_mov_b32 s0, 0x10000
	s_nop 0
	v_cvt_pk_bf16_f32 v12, v19, v17
	v_cvt_pk_bf16_f32 v13, v21, v23
	v_cvt_pk_bf16_f32 v14, v25, v27
	v_cvt_pk_bf16_f32 v15, v29, v31
	v_addc_co_u32_e32 v17, vcc, 0, v5, vcc
	global_store_dwordx4 v[16:17], v[12:15], off nt
	ds_read2_b32 v[16:17], v11 offset0:48 offset1:56
	ds_read2_b32 v[18:19], v11 offset0:16 offset1:24
	ds_read2_b32 v[20:21], v11 offset0:80 offset1:88
	ds_read2_b32 v[22:23], v11 offset0:112 offset1:120
	ds_read2_b32 v[24:25], v11 offset0:144 offset1:152
	ds_read2_b32 v[26:27], v11 offset0:176 offset1:184
	ds_read2_b32 v[28:29], v11 offset0:208 offset1:216
	ds_read2_b32 v[30:31], v11 offset0:240 offset1:248
	v_add_co_u32_e32 v32, vcc, s0, v4
	s_waitcnt lgkmcnt(0)
	v_cvt_pk_bf16_f32 v12, v18, v16
	v_addc_co_u32_e32 v33, vcc, 0, v5, vcc
	v_cvt_pk_bf16_f32 v13, v20, v22
	v_cvt_pk_bf16_f32 v14, v24, v26
	v_cvt_pk_bf16_f32 v15, v28, v30
	v_add_co_u32_e32 v16, vcc, 0x18000, v4
	global_store_dwordx4 v[32:33], v[12:15], off nt
	s_nop 1
	v_cvt_pk_bf16_f32 v12, v19, v17
	v_cvt_pk_bf16_f32 v13, v21, v23
	v_cvt_pk_bf16_f32 v14, v25, v27
	v_cvt_pk_bf16_f32 v15, v29, v31
	v_addc_co_u32_e32 v17, vcc, 0, v5, vcc
	global_store_dwordx4 v[16:17], v[12:15], off nt
	s_waitcnt lgkmcnt(0)
.LBB0_1856:
	s_and_b64 vcc, exec, s[36:37]
	s_mov_b32 s21, s26
	s_cbranch_vccnz .LBB0_1889
.LBB0_1857:
	s_add_i32 s26, s21, 0x200
	s_cmp_lt_i32 s26, s66
	s_cselect_b64 s[38:39], -1, 0
	s_cmp_ge_i32 s26, s66
	s_mov_b64 s[0:1], -1
	s_cbranch_scc0 .LBB0_1859
	s_waitcnt vmcnt(0)
	s_mov_b64 s[0:1], 0

.LBB0_1868:
	s_ashr_i32 s0, s8, 31
	s_lshr_b32 s0, s0, 17
	s_add_i32 s27, s8, s0
	s_and_b32 s0, s27, 0xffff8000
	s_sub_i32 s0, s8, s0
	s_ashr_i32 s0, s0, 11
	s_lshl_b32 s1, s6, 4
	s_add_i32 s6, s0, s1
	s_ashr_i32 s7, s6, 31
	s_cmp_lt_i32 s8, 0x10000
	s_cselect_b64 s[0:1], -1, 0
	s_cmp_gt_i32 s8, 0xffff
	s_mov_b64 s[8:9], -1
	s_cbranch_scc0 .LBB0_1870
	s_lshl_b64 s[8:9], s[6:7], 23
	s_add_u32 s36, s22, s8
	s_addc_u32 s37, s23, s9
	s_lshl_b64 s[40:41], s[6:7], 24
	s_mov_b64 s[8:9], 0
.LBB0_1870:
	s_andn2_b64 vcc, exec, s[8:9]
	s_ashr_i32 s8, s27, 15
	s_cbranch_vccnz .LBB0_1872
	s_lshl_b64 s[40:41], s[6:7], 24
	s_add_u32 s36, s24, s40
	s_addc_u32 s37, s25, s41
.LBB0_1872:
	s_lshl_b32 s6, s21, 5
	s_lshl_b32 s7, s21, 6
	s_and_b32 s6, s6, 0x7e0
	s_and_b32 s7, s7, 0xf00
	s_lshl_b32 s8, s8, 7
	s_add_i32 s8, s8, s7
	v_bitop3_b32 v4, s6, v209, v9 bitop3:0xc8
	v_or_b32_e32 v2, s6, v9
	v_or_b32_e32 v4, s8, v4
	s_and_b32 s7, s26, 0x7c0
	v_cndmask_b32_e64 v4, v2, v4, s[0:1]
	v_or_b32_e32 v2, s7, v9
	s_add_u32 s0, s2, s40
	v_lshlrev_b32_e32 v2, 13, v2
	s_addc_u32 s1, s3, s41
	v_lshl_add_u64 v[12:13], s[0:1], 0, v[2:3]
	s_lshl_b32 s92, s6, 2
	v_lshl_add_u64 v[12:13], v[12:13], 0, s[92:93]
	v_lshlrev_b32_e32 v2, 2, v8
	v_lshl_add_u64 v[12:13], v[12:13], 0, v[2:3]
	s_mov_b32 s0, m0
	s_mov_b32 m0, s94
	s_nop 0
	global_load_lds_dwordx4 v[12:13], off nt
	s_mov_b32 m0, s0
	s_mov_b64 s[0:1], 0x10000
	v_lshl_add_u64 v[14:15], v[12:13], 0, s[0:1]
	s_mov_b32 s0, m0
	s_mov_b32 m0, s12
	s_nop 0
	global_load_lds_dwordx4 v[14:15], off nt
	s_mov_b32 m0, s0
	v_lshl_add_u64 v[14:15], v[12:13], 0, s[84:85]
	s_mov_b32 s0, m0
	s_mov_b32 m0, s15
	s_nop 0
	global_load_lds_dwordx4 v[14:15], off nt
	s_mov_b32 m0, s0
	s_mov_b64 s[0:1], 0x30000
	v_lshl_add_u64 v[14:15], v[12:13], 0, s[0:1]
	s_mov_b32 s0, m0
	s_mov_b32 m0, s16
	s_nop 0
	global_load_lds_dwordx4 v[14:15], off nt
	s_mov_b32 m0, s0
	s_mov_b64 s[0:1], 0x40000
	v_lshl_add_u64 v[14:15], v[12:13], 0, s[0:1]
	s_mov_b32 s0, m0
	s_mov_b32 m0, s17
	s_nop 0
	global_load_lds_dwordx4 v[14:15], off nt
	s_mov_b32 m0, s0
	s_mov_b64 s[0:1], 0x50000
	v_lshl_add_u64 v[14:15], v[12:13], 0, s[0:1]
	s_mov_b32 s0, m0
	s_mov_b32 m0, s18
	s_nop 0
	global_load_lds_dwordx4 v[14:15], off nt
	s_mov_b32 m0, s0
	s_mov_b64 s[0:1], 0x60000
	v_lshl_add_u64 v[14:15], v[12:13], 0, s[0:1]
	s_mov_b32 s0, m0
	s_mov_b32 m0, s19
	s_nop 0
	global_load_lds_dwordx4 v[14:15], off nt
	s_mov_b32 m0, s0
	v_ashrrev_i32_e32 v5, 31, v4
	s_mov_b64 s[0:1], 0x70000
	v_lshlrev_b64 v[4:5], 12, v[4:5]
	v_lshl_add_u64 v[12:13], v[12:13], 0, s[0:1]
	s_mov_b32 s0, m0
	s_mov_b32 m0, s20
	s_nop 0
	global_load_lds_dwordx4 v[12:13], off nt
	s_mov_b32 m0, s0
	v_lshl_add_u64 v[4:5], s[36:37], 0, v[4:5]
	s_lshl_b32 s92, s7, 1
	s_waitcnt vmcnt(12)
	v_lshl_add_u64 v[4:5], v[4:5], 0, s[92:93]
	v_lshlrev_b32_e32 v2, 1, v10
	v_lshl_add_u64 v[4:5], v[4:5], 0, v[2:3]
.LBB0_1873:
	v_add_u32_e32 v2, 0x2000, v11
	v_add_u32_e32 v32, 0x2400, v11
	ds_read2_b32 v[16:17], v2 offset0:64 offset1:72
	ds_read2_b32 v[18:19], v2 offset0:32 offset1:40
	ds_read2_b32 v[20:21], v2 offset0:96 offset1:104
	ds_read2_b32 v[22:23], v2 offset0:128 offset1:136
	ds_read2_b32 v[24:25], v2 offset0:160 offset1:168
	ds_read2_b32 v[26:27], v2 offset0:192 offset1:200
	ds_read2_b32 v[28:29], v2 offset0:224 offset1:232
	ds_read2_b32 v[30:31], v32 offset1:8
	s_mov_b32 s0, 0x8000
	s_waitcnt lgkmcnt(0)
	v_cvt_pk_bf16_f32 v12, v18, v16
	v_cvt_pk_bf16_f32 v13, v20, v22
	v_cvt_pk_bf16_f32 v14, v24, v26
	v_cvt_pk_bf16_f32 v15, v28, v30
	v_add_co_u32_e32 v16, vcc, s0, v6
	global_store_dwordx4 v[6:7], v[12:15], off nt
	s_mov_b32 s0, 0x10000
	s_mov_b64 s[36:37], -1
	v_cvt_pk_bf16_f32 v12, v19, v17
	v_cvt_pk_bf16_f32 v13, v21, v23
	v_cvt_pk_bf16_f32 v14, v25, v27
	v_cvt_pk_bf16_f32 v15, v29, v31
	v_addc_co_u32_e32 v17, vcc, 0, v7, vcc
	global_store_dwordx4 v[16:17], v[12:15], off nt
	ds_read2_b32 v[16:17], v2 offset0:80 offset1:88
	ds_read2_b32 v[18:19], v2 offset0:48 offset1:56
	ds_read2_b32 v[20:21], v2 offset0:112 offset1:120
	ds_read2_b32 v[22:23], v2 offset0:144 offset1:152
	ds_read2_b32 v[24:25], v2 offset0:176 offset1:184
	ds_read2_b32 v[26:27], v2 offset0:208 offset1:216
	ds_read2_b32 v[28:29], v2 offset0:240 offset1:248
	ds_read2_b32 v[30:31], v32 offset0:16 offset1:24
	v_add_co_u32_e32 v32, vcc, s0, v6
	s_waitcnt lgkmcnt(0)
	v_cvt_pk_bf16_f32 v12, v18, v16
	v_addc_co_u32_e32 v33, vcc, 0, v7, vcc
	v_cvt_pk_bf16_f32 v13, v20, v22
	v_cvt_pk_bf16_f32 v14, v24, v26
	v_cvt_pk_bf16_f32 v15, v28, v30
	v_add_co_u32_e32 v16, vcc, 0x18000, v6
	global_store_dwordx4 v[32:33], v[12:15], off nt
	s_nop 1
	v_cvt_pk_bf16_f32 v12, v19, v17
	v_cvt_pk_bf16_f32 v13, v21, v23
	v_cvt_pk_bf16_f32 v14, v25, v27
	v_cvt_pk_bf16_f32 v15, v29, v31
	v_addc_co_u32_e32 v17, vcc, 0, v7, vcc
	global_store_dwordx4 v[16:17], v[12:15], off nt
	s_waitcnt lgkmcnt(0)
	s_andn2_b64 vcc, exec, s[38:39]
	s_cbranch_vccnz .LBB0_1856
	s_add_i32 s2, s21, 0x400
	s_cmp_ge_i32 s2, s66
	s_cselect_b64 s[36:37], -1, 0
	s_mov_b64 s[0:1], -1
	s_and_b64 vcc, exec, s[36:37]
	s_cbranch_vccz .LBB0_1876
	s_waitcnt vmcnt(0)
	s_mov_b64 s[0:1], 0

.LBB0_1885:
	s_ashr_i32 s0, s8, 31
	s_lshr_b32 s0, s0, 17
	s_add_i32 s27, s8, s0
	s_and_b32 s0, s27, 0xffff8000
	s_sub_i32 s0, s8, s0
	s_ashr_i32 s0, s0, 11
	s_lshl_b32 s1, s6, 4
	s_add_i32 s6, s0, s1
	s_ashr_i32 s7, s6, 31
	s_cmp_lt_i32 s8, 0x10000
	s_cselect_b64 s[0:1], -1, 0
	s_cmp_gt_i32 s8, 0xffff
	s_mov_b64 s[8:9], -1
	s_cbranch_scc0 .LBB0_1887
	s_lshl_b64 s[8:9], s[6:7], 23
	s_add_u32 s38, s22, s8
	s_addc_u32 s39, s23, s9
	s_lshl_b64 s[40:41], s[6:7], 24
	s_mov_b64 s[8:9], 0
.LBB0_1887:
	s_andn2_b64 vcc, exec, s[8:9]
	s_ashr_i32 s8, s27, 15
	s_cbranch_vccnz .LBB0_1854
	s_lshl_b64 s[40:41], s[6:7], 24
	s_add_u32 s38, s24, s40
	s_addc_u32 s39, s25, s41
	s_branch .LBB0_1854
.LBB0_1889:
	s_waitcnt vmcnt(0)
	v_readlane_b32 s26, v254, 28
	v_readlane_b32 s27, v254, 29
.LBB0_1890:
	s_movk_i32 s0, 0x400

	.amdhsa_kernel _Z8mega_fwd4Args
		.amdhsa_group_segment_fixed_size 0
		.amdhsa_private_segment_fixed_size 0
		.amdhsa_kernarg_size 448
		.amdhsa_user_sgpr_count 2
		.amdhsa_user_sgpr_dispatch_ptr 0
		.amdhsa_user_sgpr_queue_ptr 0
		.amdhsa_user_sgpr_kernarg_segment_ptr 1
		.amdhsa_user_sgpr_dispatch_id 0
		.amdhsa_user_sgpr_kernarg_preload_length 0
		.amdhsa_user_sgpr_kernarg_preload_offset 0
		.amdhsa_user_sgpr_private_segment_size 0
		.amdhsa_uses_dynamic_stack 0
		.amdhsa_enable_private_segment 0
		.amdhsa_system_sgpr_workgroup_id_x 1
		.amdhsa_system_sgpr_workgroup_id_y 0
		.amdhsa_system_sgpr_workgroup_id_z 0
		.amdhsa_system_sgpr_workgroup_info 0
		.amdhsa_system_vgpr_workitem_id 0
		.amdhsa_next_free_vgpr 255
		.amdhsa_next_free_sgpr 100
		.amdhsa_accum_offset 256
		.amdhsa_reserve_vcc 1
		.amdhsa_float_round_mode_32 0
		.amdhsa_float_round_mode_16_64 0
		.amdhsa_float_denorm_mode_32 3
		.amdhsa_float_denorm_mode_16_64 3
		.amdhsa_dx10_clamp 1
		.amdhsa_ieee_mode 1
		.amdhsa_fp16_overflow 0
		.amdhsa_tg_split 0
		.amdhsa_exception_fp_ieee_invalid_op 0
		.amdhsa_exception_fp_denorm_src 0
		.amdhsa_exception_fp_ieee_div_zero 0
		.amdhsa_exception_fp_ieee_overflow 0
		.amdhsa_exception_fp_ieee_underflow 0
		.amdhsa_exception_fp_ieee_inexact 0
		.amdhsa_exception_int_div_zero 0
	.end_amdhsa_kernel

amdhsa.kernels:
  - .agpr_count:     0
    .args:
      - .offset:         0
        .size:           192
        .value_kind:     by_value
      - .offset:         192
        .size:           4
        .value_kind:     hidden_block_count_x
      - .offset:         196
        .size:           4
        .value_kind:     hidden_block_count_y
      - .offset:         200
        .size:           4
        .value_kind:     hidden_block_count_z
      - .offset:         204
        .size:           2
        .value_kind:     hidden_group_size_x
      - .offset:         206
        .size:           2
        .value_kind:     hidden_group_size_y
      - .offset:         208
        .size:           2
        .value_kind:     hidden_group_size_z
      - .offset:         210
        .size:           2
        .value_kind:     hidden_remainder_x
      - .offset:         212
        .size:           2
        .value_kind:     hidden_remainder_y
      - .offset:         214
        .size:           2
        .value_kind:     hidden_remainder_z
      - .offset:         232
        .size:           8
        .value_kind:     hidden_global_offset_x
      - .offset:         240
        .size:           8
        .value_kind:     hidden_global_offset_y
      - .offset:         248
        .size:           8
        .value_kind:     hidden_global_offset_z
      - .offset:         256
        .size:           2
        .value_kind:     hidden_grid_dims
      - .offset:         312
        .size:           4
        .value_kind:     hidden_dynamic_lds_size
    .group_segment_fixed_size: 0
    .kernarg_segment_align: 8
    .kernarg_segment_size: 448
    .language:       OpenCL C
    .language_version:
      - 2
      - 0
    .max_flat_workgroup_size: 512
    .name:           _Z8mega_fwd4Args
    .private_segment_fixed_size: 0
    .sgpr_count:     106
    .sgpr_spill_count: 242
    .symbol:         _Z8mega_fwd4Args.kd
    .uniform_work_group_size: 1
    .uses_dynamic_stack: false
    .vgpr_count:     255
    .vgpr_spill_count: 0
    .wavefront_size: 64
